# permuted epilogue stores pipelined three deep (was two) on the v16 chain
# baseline (speedup 1.0000x reference)
.LBB0_174:
	v_mbcnt_lo_u32_b32 v250, -1, 0
	v_mbcnt_hi_u32_b32 v250, -1, v250
	v_lshrrev_b32_e32 v251, 2, v250
	v_and_b32_e32 v250, 3, v250
	v_lshl_add_u32 v250, v250, 4, v251
	v_lshlrev_b32_e32 v250, 2, v250
	s_ashr_i32 s15, s60, 3
	s_add_i32 s62, s15, s75
	s_lshl_b32 s15, s60, 8
	s_and_b32 s15, s15, 0x700
	s_cmp_eq_u32 s62, 0
	v_lshl_add_u32 v174, s28, 8, v1
	s_cselect_b64 s[26:27], -1, 0
	v_or_b32_e32 v82, s15, v209
	s_and_b64 s[26:27], s[50:51], s[26:27]
	v_or_b32_e32 v180, 16, v174
	v_or_b32_e32 v178, 32, v174
	v_or_b32_e32 v176, 48, v174
	s_mov_b64 s[64:65], -1
	s_and_b64 vcc, exec, s[26:27]
	v_lshlrev_b32_e32 v114, 1, v82
	v_ashrrev_i32_e32 v175, 31, v174
	v_ashrrev_i32_e32 v181, 31, v180
	v_ashrrev_i32_e32 v179, 31, v178
	v_ashrrev_i32_e32 v177, 31, v176
	s_cbranch_vccnz .LBB0_177
	v_lshl_add_u32 v158, s14, 10, v210
	ds_read2_b32 v[88:89], v158 offset1:16
	s_ashr_i32 s63, s62, 31
	s_lshl_b64 s[26:27], s[62:63], 25
	s_add_u32 s26, s84, s26
	s_addc_u32 s27, s85, s27
	v_lshl_add_u64 v[90:91], s[26:27], 0, v[114:115]
	v_lshlrev_b64 v[82:83], 12, v[174:175]
	s_waitcnt lgkmcnt(0)
	v_pk_mul_f32 v[84:85], v[144:145], v[88:89] op_sel_hi:[1,0]
	v_lshl_add_u64 v[82:83], v[90:91], 0, v[82:83]
	v_pk_mul_f32 v[86:87], v[146:147], v[88:89] op_sel_hi:[1,0]
	v_cvt_pk_bf16_f32 v84, v84, v85
	v_pk_mul_f32 v[92:93], v[142:143], v[88:89] op_sel_hi:[1,0]
	v_cvt_pk_bf16_f32 v85, v86, v87
	v_pk_mul_f32 v[94:95], v[140:141], v[88:89] op_sel_hi:[1,0]
	v_cvt_pk_bf16_f32 v87, v92, v93
	v_pk_mul_f32 v[92:93], v[134:135], v[88:89] op_sel_hi:[1,0]
	v_cvt_pk_bf16_f32 v86, v94, v95
	ds_bpermute_b32 v232, v250, v84
	ds_bpermute_b32 v233, v250, v85
	ds_bpermute_b32 v234, v250, v86
	ds_bpermute_b32 v235, v250, v87
	ds_bpermute_b32 v236, v250, v82
	v_pk_mul_f32 v[94:95], v[132:133], v[88:89] op_sel_hi:[1,0]
	s_mov_b32 s15, 0x80000
	v_pk_mul_f32 v[84:85], v[136:137], v[88:89] op_sel_hi:[1,0]
	v_pk_mul_f32 v[86:87], v[138:139], v[88:89] op_sel_hi:[1,0]
	v_cvt_pk_bf16_f32 v84, v84, v85
	v_mov_b32_e32 v88, v89
	v_cvt_pk_bf16_f32 v85, v86, v87
	v_cvt_pk_bf16_f32 v86, v94, v95
	v_cvt_pk_bf16_f32 v87, v92, v93
	ds_bpermute_b32 v238, v250, v84
	ds_bpermute_b32 v239, v250, v85
	ds_bpermute_b32 v240, v250, v86
	ds_bpermute_b32 v241, v250, v87
	ds_bpermute_b32 v242, v250, v82
	v_pk_mul_f32 v[94:95], v[126:127], v[88:89] op_sel_hi:[1,0]
	v_pk_mul_f32 v[96:97], v[124:125], v[88:89] op_sel_hi:[1,0]
	v_lshlrev_b64 v[84:85], 12, v[180:181]
	v_lshl_add_u64 v[92:93], v[90:91], 0, v[84:85]
	v_pk_mul_f32 v[86:87], v[130:131], v[88:89] op_sel_hi:[1,0]
	v_pk_mul_f32 v[84:85], v[128:129], v[88:89] op_sel_hi:[1,0]
	s_mov_b64 s[16:17], 0x80000
	v_cvt_pk_bf16_f32 v84, v84, v85
	v_cvt_pk_bf16_f32 v85, v86, v87
	v_cvt_pk_bf16_f32 v86, v96, v97
	v_cvt_pk_bf16_f32 v87, v94, v95
	ds_bpermute_b32 v244, v250, v84
	ds_bpermute_b32 v245, v250, v85
	ds_bpermute_b32 v246, v250, v86
	ds_bpermute_b32 v247, v250, v87
	ds_bpermute_b32 v248, v250, v92
	v_pk_mul_f32 v[94:95], v[118:119], v[88:89] op_sel_hi:[1,0]
	s_nop 0
	v_pk_mul_f32 v[86:87], v[122:123], v[88:89] op_sel_hi:[1,0]
	v_pk_mul_f32 v[84:85], v[120:121], v[88:89] op_sel_hi:[1,0]
	v_pk_mul_f32 v[88:89], v[116:117], v[88:89] op_sel_hi:[1,0]
	v_cvt_pk_bf16_f32 v84, v84, v85
	v_cvt_pk_bf16_f32 v85, v86, v87
	v_cvt_pk_bf16_f32 v87, v94, v95
	s_nop 0
	v_cvt_pk_bf16_f32 v86, v88, v89
	ds_read2_b32 v[88:89], v158 offset0:32 offset1:48
	s_waitcnt lgkmcnt(11)
	v_subrev_u32_e32 v236, s82, v236
	global_store_dwordx4 v236, v[232:235], s[82:83]
	ds_bpermute_b32 v232, v250, v84
	ds_bpermute_b32 v233, v250, v85
	ds_bpermute_b32 v234, v250, v86
	ds_bpermute_b32 v235, v250, v87
	ds_bpermute_b32 v236, v250, v92
	s_waitcnt lgkmcnt(0)
	v_pk_mul_f32 v[94:95], v[108:109], v[88:89] op_sel_hi:[1,0]
	v_lshlrev_b64 v[84:85], 12, v[178:179]
	v_lshl_add_u64 v[92:93], v[90:91], 0, v[84:85]
	v_pk_mul_f32 v[84:85], v[110:111], v[88:89] op_sel_hi:[1,0]
	v_pk_mul_f32 v[86:87], v[112:113], v[88:89] op_sel_hi:[1,0]
	v_cvt_pk_bf16_f32 v84, v84, v85
	v_pk_mul_f32 v[96:97], v[106:107], v[88:89] op_sel_hi:[1,0]
	v_cvt_pk_bf16_f32 v85, v86, v87
	v_cvt_pk_bf16_f32 v87, v94, v95
	v_pk_mul_f32 v[94:95], v[100:101], v[88:89] op_sel_hi:[1,0]
	v_cvt_pk_bf16_f32 v86, v96, v97
	s_waitcnt lgkmcnt(11)
	v_subrev_u32_e32 v242, s82, v242
	global_store_dwordx4 v242, v[238:241], s[82:83] offset:64
	ds_bpermute_b32 v238, v250, v84
	ds_bpermute_b32 v239, v250, v85
	ds_bpermute_b32 v240, v250, v86
	ds_bpermute_b32 v241, v250, v87
	ds_bpermute_b32 v242, v250, v92
	v_pk_mul_f32 v[96:97], v[98:99], v[88:89] op_sel_hi:[1,0]
	s_nop 0
	v_pk_mul_f32 v[84:85], v[102:103], v[88:89] op_sel_hi:[1,0]
	v_pk_mul_f32 v[86:87], v[104:105], v[88:89] op_sel_hi:[1,0]
	v_cvt_pk_bf16_f32 v84, v84, v85
	v_mov_b32_e32 v88, v89
	v_cvt_pk_bf16_f32 v85, v86, v87
	v_cvt_pk_bf16_f32 v86, v96, v97
	v_cvt_pk_bf16_f32 v87, v94, v95
	s_waitcnt lgkmcnt(11)
	v_subrev_u32_e32 v248, s82, v248
	global_store_dwordx4 v248, v[244:247], s[82:83]
	ds_bpermute_b32 v244, v250, v84
	ds_bpermute_b32 v245, v250, v85
	ds_bpermute_b32 v246, v250, v86
	ds_bpermute_b32 v247, v250, v87
	ds_bpermute_b32 v248, v250, v92
	v_pk_mul_f32 v[94:95], v[74:75], v[88:89] op_sel_hi:[1,0]
	v_pk_mul_f32 v[92:93], v[76:77], v[88:89] op_sel_hi:[1,0]
	v_lshlrev_b64 v[84:85], 12, v[176:177]
	v_lshl_add_u64 v[90:91], v[90:91], 0, v[84:85]
	v_pk_mul_f32 v[86:87], v[80:81], v[88:89] op_sel_hi:[1,0]
	v_pk_mul_f32 v[84:85], v[78:79], v[88:89] op_sel_hi:[1,0]
	s_nop 0
	v_cvt_pk_bf16_f32 v84, v84, v85
	v_cvt_pk_bf16_f32 v85, v86, v87
	v_cvt_pk_bf16_f32 v86, v94, v95
	ds_read2_b32 v[94:95], v158 offset0:128 offset1:144
	v_cvt_pk_bf16_f32 v87, v92, v93
	s_waitcnt lgkmcnt(11)
	v_subrev_u32_e32 v236, s82, v236
	global_store_dwordx4 v236, v[232:235], s[82:83] offset:64
	ds_bpermute_b32 v232, v250, v84
	ds_bpermute_b32 v233, v250, v85
	ds_bpermute_b32 v234, v250, v86
	ds_bpermute_b32 v235, v250, v87
	ds_bpermute_b32 v236, v250, v90
	v_pk_mul_f32 v[92:93], v[68:69], v[88:89] op_sel_hi:[1,0]
	s_nop 0
	v_pk_mul_f32 v[86:87], v[72:73], v[88:89] op_sel_hi:[1,0]
	v_pk_mul_f32 v[84:85], v[70:71], v[88:89] op_sel_hi:[1,0]
	v_pk_mul_f32 v[88:89], v[66:67], v[88:89] op_sel_hi:[1,0]
	v_cvt_pk_bf16_f32 v84, v84, v85
	v_cvt_pk_bf16_f32 v85, v86, v87
	v_cvt_pk_bf16_f32 v87, v92, v93
	s_waitcnt lgkmcnt(0)
	v_pk_mul_f32 v[92:93], v[58:59], v[94:95] op_sel_hi:[1,0]
	v_cvt_pk_bf16_f32 v86, v88, v89
	s_waitcnt lgkmcnt(11)
	v_subrev_u32_e32 v242, s82, v242
	global_store_dwordx4 v242, v[238:241], s[82:83]
	ds_bpermute_b32 v238, v250, v84
	ds_bpermute_b32 v239, v250, v85
	ds_bpermute_b32 v240, v250, v86
	ds_bpermute_b32 v241, v250, v87
	ds_bpermute_b32 v242, v250, v90
	v_pk_mul_f32 v[90:91], v[60:61], v[94:95] op_sel_hi:[1,0]
	v_lshl_add_u64 v[88:89], v[82:83], 0, s[16:17]
	v_pk_mul_f32 v[86:87], v[64:65], v[94:95] op_sel_hi:[1,0]
	v_pk_mul_f32 v[84:85], v[62:63], v[94:95] op_sel_hi:[1,0]
	s_mov_b64 s[16:17], 0x90000
	v_cvt_pk_bf16_f32 v84, v84, v85
	v_cvt_pk_bf16_f32 v85, v86, v87
	v_cvt_pk_bf16_f32 v87, v90, v91
	v_add_co_u32_e32 v90, vcc, s15, v82
	v_cvt_pk_bf16_f32 v86, v92, v93
	v_pk_mul_f32 v[92:93], v[50:51], v[94:95] op_sel_hi:[1,0]
	s_nop 0
	v_addc_co_u32_e32 v91, vcc, 0, v83, vcc
	s_waitcnt lgkmcnt(11)
	v_subrev_u32_e32 v248, s82, v248
	global_store_dwordx4 v248, v[244:247], s[82:83] offset:64
	ds_bpermute_b32 v244, v250, v84
	ds_bpermute_b32 v245, v250, v85
	ds_bpermute_b32 v246, v250, v86
	ds_bpermute_b32 v247, v250, v87
	ds_bpermute_b32 v248, v250, v90
	v_pk_mul_f32 v[90:91], v[52:53], v[94:95] op_sel_hi:[1,0]
	s_mov_b32 s15, 0x90000
	v_pk_mul_f32 v[86:87], v[56:57], v[94:95] op_sel_hi:[1,0]
	v_pk_mul_f32 v[84:85], v[54:55], v[94:95] op_sel_hi:[1,0]
	s_nop 0
	v_cvt_pk_bf16_f32 v84, v84, v85
	v_cvt_pk_bf16_f32 v85, v86, v87
	v_cvt_pk_bf16_f32 v86, v92, v93
	v_cvt_pk_bf16_f32 v87, v90, v91
	v_mov_b32_e32 v90, v95
	s_waitcnt lgkmcnt(10)
	v_subrev_u32_e32 v236, s82, v236
	global_store_dwordx4 v236, v[232:235], s[82:83]
	ds_bpermute_b32 v232, v250, v84
	ds_bpermute_b32 v233, v250, v85
	ds_bpermute_b32 v234, v250, v86
	ds_bpermute_b32 v235, v250, v87
	ds_bpermute_b32 v236, v250, v88
	v_pk_mul_f32 v[94:95], v[42:43], v[90:91] op_sel_hi:[1,0]
	v_pk_mul_f32 v[92:93], v[44:45], v[90:91] op_sel_hi:[1,0]
	v_pk_mul_f32 v[86:87], v[48:49], v[90:91] op_sel_hi:[1,0]
	v_pk_mul_f32 v[84:85], v[46:47], v[90:91] op_sel_hi:[1,0]
	v_lshl_add_u64 v[88:89], v[82:83], 0, s[16:17]
	v_cvt_pk_bf16_f32 v84, v84, v85
	v_cvt_pk_bf16_f32 v85, v86, v87
	v_cvt_pk_bf16_f32 v86, v94, v95
	ds_read2_b32 v[94:95], v158 offset0:160 offset1:176
	v_cvt_pk_bf16_f32 v87, v92, v93
	v_add_co_u32_e32 v92, vcc, s15, v82
	s_mov_b32 s15, 0xa0000
	s_nop 0
	v_addc_co_u32_e32 v93, vcc, 0, v83, vcc
	s_waitcnt lgkmcnt(11)
	v_subrev_u32_e32 v242, s82, v242
	global_store_dwordx4 v242, v[238:241], s[82:83] offset:64
	ds_bpermute_b32 v238, v250, v84
	ds_bpermute_b32 v239, v250, v85
	ds_bpermute_b32 v240, v250, v86
	ds_bpermute_b32 v241, v250, v87
	ds_bpermute_b32 v242, v250, v92
	v_pk_mul_f32 v[92:93], v[36:37], v[90:91] op_sel_hi:[1,0]
	s_mov_b64 s[16:17], 0xa0000
	v_pk_mul_f32 v[86:87], v[40:41], v[90:91] op_sel_hi:[1,0]
	v_pk_mul_f32 v[84:85], v[38:39], v[90:91] op_sel_hi:[1,0]
	v_pk_mul_f32 v[90:91], v[34:35], v[90:91] op_sel_hi:[1,0]
	v_cvt_pk_bf16_f32 v84, v84, v85
	v_cvt_pk_bf16_f32 v85, v86, v87
	v_cvt_pk_bf16_f32 v87, v92, v93
	s_waitcnt lgkmcnt(0)
	v_pk_mul_f32 v[92:93], v[26:27], v[94:95] op_sel_hi:[1,0]
	v_cvt_pk_bf16_f32 v86, v90, v91
	s_waitcnt lgkmcnt(11)
	v_subrev_u32_e32 v248, s82, v248
	global_store_dwordx4 v248, v[244:247], s[82:83]
	ds_bpermute_b32 v244, v250, v84
	ds_bpermute_b32 v245, v250, v85
	ds_bpermute_b32 v246, v250, v86
	ds_bpermute_b32 v247, v250, v87
	ds_bpermute_b32 v248, v250, v88
	v_pk_mul_f32 v[90:91], v[28:29], v[94:95] op_sel_hi:[1,0]
	v_lshl_add_u64 v[88:89], v[82:83], 0, s[16:17]
	v_pk_mul_f32 v[86:87], v[32:33], v[94:95] op_sel_hi:[1,0]
	v_pk_mul_f32 v[84:85], v[30:31], v[94:95] op_sel_hi:[1,0]
	s_mov_b64 s[16:17], 0xb0000
	v_cvt_pk_bf16_f32 v84, v84, v85
	v_cvt_pk_bf16_f32 v85, v86, v87
	v_cvt_pk_bf16_f32 v87, v90, v91
	v_add_co_u32_e32 v90, vcc, s15, v82
	v_cvt_pk_bf16_f32 v86, v92, v93
	s_mov_b32 s15, 0xb0000
	s_nop 0
	v_addc_co_u32_e32 v91, vcc, 0, v83, vcc
	s_waitcnt lgkmcnt(11)
	v_subrev_u32_e32 v236, s82, v236
	global_store_dwordx4 v236, v[232:235], s[82:83] offset:64
	ds_bpermute_b32 v232, v250, v84
	ds_bpermute_b32 v233, v250, v85
	ds_bpermute_b32 v234, v250, v86
	ds_bpermute_b32 v235, v250, v87
	ds_bpermute_b32 v236, v250, v90
	v_pk_mul_f32 v[90:91], v[20:21], v[94:95] op_sel_hi:[1,0]
	v_pk_mul_f32 v[92:93], v[18:19], v[94:95] op_sel_hi:[1,0]
	v_pk_mul_f32 v[86:87], v[24:25], v[94:95] op_sel_hi:[1,0]
	v_pk_mul_f32 v[84:85], v[22:23], v[94:95] op_sel_hi:[1,0]
	s_nop 0
	v_cvt_pk_bf16_f32 v84, v84, v85
	v_cvt_pk_bf16_f32 v85, v86, v87
	v_cvt_pk_bf16_f32 v87, v90, v91
	v_mov_b32_e32 v90, v95
	v_cvt_pk_bf16_f32 v86, v92, v93
	s_waitcnt lgkmcnt(10)
	v_subrev_u32_e32 v242, s82, v242
	global_store_dwordx4 v242, v[238:241], s[82:83]
	ds_bpermute_b32 v238, v250, v84
	ds_bpermute_b32 v239, v250, v85
	ds_bpermute_b32 v240, v250, v86
	ds_bpermute_b32 v241, v250, v87
	ds_bpermute_b32 v242, v250, v88
	v_lshl_add_u64 v[88:89], v[82:83], 0, s[16:17]
	v_add_co_u32_e32 v82, vcc, s15, v82
	v_pk_mul_f32 v[84:85], v[14:15], v[90:91] op_sel_hi:[1,0]
	v_pk_mul_f32 v[86:87], v[16:17], v[90:91] op_sel_hi:[1,0]
	v_cvt_pk_bf16_f32 v84, v84, v85
	v_addc_co_u32_e32 v83, vcc, 0, v83, vcc
	v_cvt_pk_bf16_f32 v85, v86, v87
	v_pk_mul_f32 v[92:93], v[12:13], v[90:91] op_sel_hi:[1,0]
	v_pk_mul_f32 v[94:95], v[10:11], v[90:91] op_sel_hi:[1,0]
	v_cvt_pk_bf16_f32 v87, v92, v93
	s_nop 0
	v_cvt_pk_bf16_f32 v86, v94, v95
	s_waitcnt lgkmcnt(10)
	v_subrev_u32_e32 v248, s82, v248
	global_store_dwordx4 v248, v[244:247], s[82:83] offset:64
	ds_bpermute_b32 v244, v250, v84
	ds_bpermute_b32 v245, v250, v85
	ds_bpermute_b32 v246, v250, v86
	ds_bpermute_b32 v247, v250, v87
	ds_bpermute_b32 v248, v250, v82
	v_pk_mul_f32 v[82:83], v[6:7], v[90:91] op_sel_hi:[1,0]
	s_nop 0
	v_pk_mul_f32 v[84:85], v[8:9], v[90:91] op_sel_hi:[1,0]
	v_pk_mul_f32 v[86:87], v[4:5], v[90:91] op_sel_hi:[1,0]
	v_pk_mul_f32 v[90:91], v[2:3], v[90:91] op_sel_hi:[1,0]
	v_cvt_pk_bf16_f32 v82, v82, v83
	v_cvt_pk_bf16_f32 v83, v84, v85
	v_cvt_pk_bf16_f32 v85, v86, v87
	s_nop 0
	v_cvt_pk_bf16_f32 v84, v90, v91
	s_waitcnt lgkmcnt(10)
	v_subrev_u32_e32 v236, s82, v236
	global_store_dwordx4 v236, v[232:235], s[82:83]
	ds_bpermute_b32 v232, v250, v82
	ds_bpermute_b32 v233, v250, v83
	ds_bpermute_b32 v234, v250, v84
	ds_bpermute_b32 v235, v250, v85
	ds_bpermute_b32 v236, v250, v88
	s_waitcnt lgkmcnt(10)
	v_subrev_u32_e32 v242, s82, v242
	global_store_dwordx4 v242, v[238:241], s[82:83] offset:64
	s_waitcnt lgkmcnt(5)
	v_subrev_u32_e32 v248, s82, v248
	global_store_dwordx4 v248, v[244:247], s[82:83]
	s_waitcnt lgkmcnt(0)
	v_subrev_u32_e32 v236, s82, v236
	global_store_dwordx4 v236, v[232:235], s[82:83] offset:64
	s_cbranch_execz .LBB0_178

.LBB0_178:
	s_lshl_b32 s14, s14, 10
	v_add_u32_e32 v213, s14, v211
	ds_read_b32 v82, v213
	s_waitcnt lgkmcnt(0)
	v_pk_mul_f32 v[84:85], v[146:147], v[82:83] op_sel_hi:[1,0]
	v_pk_mul_f32 v[86:87], v[144:145], v[82:83] op_sel_hi:[1,0]
	v_pk_mul_f32 v[84:85], v[84:85], v[84:85]
	v_pk_mul_f32 v[88:89], v[140:141], v[82:83] op_sel_hi:[1,0]
	v_pk_fma_f32 v[84:85], v[86:87], v[86:87], v[84:85]
	v_pk_mul_f32 v[86:87], v[142:143], v[82:83] op_sel_hi:[1,0]
	s_nop 0
	v_pk_mul_f32 v[86:87], v[86:87], v[86:87]
	s_nop 0
	v_pk_fma_f32 v[86:87], v[88:89], v[88:89], v[86:87]
	v_pk_mul_f32 v[88:89], v[136:137], v[82:83] op_sel_hi:[1,0]
	v_pk_add_f32 v[84:85], v[84:85], v[86:87]
	v_pk_mul_f32 v[86:87], v[138:139], v[82:83] op_sel_hi:[1,0]
	s_nop 0
	v_pk_mul_f32 v[86:87], v[86:87], v[86:87]
	s_nop 0
	v_pk_fma_f32 v[86:87], v[88:89], v[88:89], v[86:87]
	s_nop 0
	v_pk_add_f32 v[84:85], v[86:87], v[84:85]
	v_pk_mul_f32 v[86:87], v[134:135], v[82:83] op_sel_hi:[1,0]
	v_pk_mul_f32 v[82:83], v[132:133], v[82:83] op_sel_hi:[1,0]
	v_pk_mul_f32 v[86:87], v[86:87], v[86:87]
	s_nop 0
	v_pk_fma_f32 v[82:83], v[82:83], v[82:83], v[86:87]
	s_nop 0
	v_pk_add_f32 v[82:83], v[82:83], v[84:85]
	s_nop 0
	v_add_f32_e32 v82, v82, v83
	ds_swizzle_b32 v83, v82 offset:swizzle(SWAP,16)
	s_waitcnt lgkmcnt(0)
	v_add_f32_e32 v82, v82, v83
	v_mov_b32_e32 v83, v82
	s_nop 1
	v_permlane32_swap_b32_e32 v82, v83
	s_and_saveexec_b64 s[62:63], s[38:39]
	v_add_f32_e32 v82, v82, v83
	ds_write_b32 v183, v82
	s_or_b64 exec, exec, s[62:63]
	ds_read_b32 v82, v213 offset:64
	s_waitcnt lgkmcnt(0)
	v_pk_mul_f32 v[84:85], v[130:131], v[82:83] op_sel_hi:[1,0]
	v_pk_mul_f32 v[86:87], v[128:129], v[82:83] op_sel_hi:[1,0]
	v_pk_mul_f32 v[84:85], v[84:85], v[84:85]
	v_pk_mul_f32 v[88:89], v[124:125], v[82:83] op_sel_hi:[1,0]
	v_pk_fma_f32 v[84:85], v[86:87], v[86:87], v[84:85]
	v_pk_mul_f32 v[86:87], v[126:127], v[82:83] op_sel_hi:[1,0]
	s_nop 0
	v_pk_mul_f32 v[86:87], v[86:87], v[86:87]
	s_nop 0
	v_pk_fma_f32 v[86:87], v[88:89], v[88:89], v[86:87]
	v_pk_mul_f32 v[88:89], v[120:121], v[82:83] op_sel_hi:[1,0]
	v_pk_add_f32 v[84:85], v[84:85], v[86:87]
	v_pk_mul_f32 v[86:87], v[122:123], v[82:83] op_sel_hi:[1,0]
	s_nop 0
	v_pk_mul_f32 v[86:87], v[86:87], v[86:87]
	s_nop 0
	v_pk_fma_f32 v[86:87], v[88:89], v[88:89], v[86:87]
	s_nop 0
	v_pk_add_f32 v[84:85], v[86:87], v[84:85]
	v_pk_mul_f32 v[86:87], v[118:119], v[82:83] op_sel_hi:[1,0]
	v_pk_mul_f32 v[82:83], v[116:117], v[82:83] op_sel_hi:[1,0]
	v_pk_mul_f32 v[86:87], v[86:87], v[86:87]
	s_nop 0
	v_pk_fma_f32 v[82:83], v[82:83], v[82:83], v[86:87]
	s_nop 0
	v_pk_add_f32 v[82:83], v[82:83], v[84:85]
	s_nop 0
	v_add_f32_e32 v82, v82, v83
	ds_swizzle_b32 v83, v82 offset:swizzle(SWAP,16)
	s_waitcnt lgkmcnt(0)
	v_add_f32_e32 v82, v82, v83
	v_mov_b32_e32 v83, v82
	s_nop 1
	v_permlane32_swap_b32_e32 v82, v83
	s_and_saveexec_b64 s[62:63], s[38:39]
	v_add_f32_e32 v82, v82, v83
	ds_write_b32 v195, v82
	s_or_b64 exec, exec, s[62:63]
	ds_read_b32 v82, v213 offset:128
	s_waitcnt lgkmcnt(0)
	v_pk_mul_f32 v[84:85], v[112:113], v[82:83] op_sel_hi:[1,0]
	v_pk_mul_f32 v[86:87], v[110:111], v[82:83] op_sel_hi:[1,0]
	v_pk_mul_f32 v[84:85], v[84:85], v[84:85]
	v_pk_mul_f32 v[88:89], v[106:107], v[82:83] op_sel_hi:[1,0]
	v_pk_fma_f32 v[84:85], v[86:87], v[86:87], v[84:85]
	v_pk_mul_f32 v[86:87], v[108:109], v[82:83] op_sel_hi:[1,0]
	s_nop 0
	v_pk_mul_f32 v[86:87], v[86:87], v[86:87]
	s_nop 0
	v_pk_fma_f32 v[86:87], v[88:89], v[88:89], v[86:87]
	v_pk_mul_f32 v[88:89], v[102:103], v[82:83] op_sel_hi:[1,0]
	v_pk_add_f32 v[84:85], v[84:85], v[86:87]
	v_pk_mul_f32 v[86:87], v[104:105], v[82:83] op_sel_hi:[1,0]
	s_nop 0
	v_pk_mul_f32 v[86:87], v[86:87], v[86:87]
	s_nop 0
	v_pk_fma_f32 v[86:87], v[88:89], v[88:89], v[86:87]
	s_nop 0
	v_pk_add_f32 v[84:85], v[86:87], v[84:85]
	v_pk_mul_f32 v[86:87], v[100:101], v[82:83] op_sel_hi:[1,0]
	v_pk_mul_f32 v[82:83], v[98:99], v[82:83] op_sel_hi:[1,0]
	v_pk_mul_f32 v[86:87], v[86:87], v[86:87]
	s_nop 0
	v_pk_fma_f32 v[82:83], v[82:83], v[82:83], v[86:87]
	s_nop 0
	v_pk_add_f32 v[82:83], v[82:83], v[84:85]
	s_nop 0
	v_add_f32_e32 v82, v82, v83
	ds_swizzle_b32 v83, v82 offset:swizzle(SWAP,16)
	s_waitcnt lgkmcnt(0)
	v_add_f32_e32 v82, v82, v83
	v_mov_b32_e32 v83, v82
	s_nop 1
	v_permlane32_swap_b32_e32 v82, v83
	s_and_saveexec_b64 s[62:63], s[38:39]
	v_add_f32_e32 v82, v82, v83
	ds_write_b32 v197, v82
	s_or_b64 exec, exec, s[62:63]
	ds_read_b32 v82, v213 offset:192
	s_waitcnt lgkmcnt(0)
	v_pk_mul_f32 v[84:85], v[80:81], v[82:83] op_sel_hi:[1,0]
	v_pk_mul_f32 v[86:87], v[78:79], v[82:83] op_sel_hi:[1,0]
	v_pk_mul_f32 v[84:85], v[84:85], v[84:85]
	v_pk_mul_f32 v[88:89], v[74:75], v[82:83] op_sel_hi:[1,0]
	v_pk_fma_f32 v[84:85], v[86:87], v[86:87], v[84:85]
	v_pk_mul_f32 v[86:87], v[76:77], v[82:83] op_sel_hi:[1,0]
	s_nop 0
	v_pk_mul_f32 v[86:87], v[86:87], v[86:87]
	s_nop 0
	v_pk_fma_f32 v[86:87], v[88:89], v[88:89], v[86:87]
	v_pk_mul_f32 v[88:89], v[70:71], v[82:83] op_sel_hi:[1,0]
	v_pk_add_f32 v[84:85], v[84:85], v[86:87]
	v_pk_mul_f32 v[86:87], v[72:73], v[82:83] op_sel_hi:[1,0]
	s_nop 0
	v_pk_mul_f32 v[86:87], v[86:87], v[86:87]
	s_nop 0
	v_pk_fma_f32 v[86:87], v[88:89], v[88:89], v[86:87]
	s_nop 0
	v_pk_add_f32 v[84:85], v[86:87], v[84:85]
	v_pk_mul_f32 v[86:87], v[68:69], v[82:83] op_sel_hi:[1,0]
	v_pk_mul_f32 v[82:83], v[66:67], v[82:83] op_sel_hi:[1,0]
	v_pk_mul_f32 v[86:87], v[86:87], v[86:87]
	s_nop 0
	v_pk_fma_f32 v[82:83], v[82:83], v[82:83], v[86:87]
	s_nop 0
	v_pk_add_f32 v[82:83], v[82:83], v[84:85]
	s_nop 0
	v_add_f32_e32 v82, v82, v83
	ds_swizzle_b32 v83, v82 offset:swizzle(SWAP,16)
	s_waitcnt lgkmcnt(0)
	v_add_f32_e32 v82, v82, v83
	v_mov_b32_e32 v83, v82
	s_nop 1
	v_permlane32_swap_b32_e32 v82, v83
	s_and_saveexec_b64 s[62:63], s[38:39]
	v_add_f32_e32 v82, v82, v83
	ds_write_b32 v199, v82
	s_or_b64 exec, exec, s[62:63]
	ds_read_b32 v82, v213 offset:512
	s_waitcnt lgkmcnt(0)
	v_pk_mul_f32 v[84:85], v[64:65], v[82:83] op_sel_hi:[1,0]
	v_pk_mul_f32 v[86:87], v[62:63], v[82:83] op_sel_hi:[1,0]
	v_pk_mul_f32 v[84:85], v[84:85], v[84:85]
	v_pk_mul_f32 v[88:89], v[58:59], v[82:83] op_sel_hi:[1,0]
	v_pk_fma_f32 v[84:85], v[86:87], v[86:87], v[84:85]
	v_pk_mul_f32 v[86:87], v[60:61], v[82:83] op_sel_hi:[1,0]
	s_nop 0
	v_pk_mul_f32 v[86:87], v[86:87], v[86:87]
	s_nop 0
	v_pk_fma_f32 v[86:87], v[88:89], v[88:89], v[86:87]
	v_pk_mul_f32 v[88:89], v[54:55], v[82:83] op_sel_hi:[1,0]
	v_pk_add_f32 v[84:85], v[84:85], v[86:87]
	v_pk_mul_f32 v[86:87], v[56:57], v[82:83] op_sel_hi:[1,0]
	s_nop 0
	v_pk_mul_f32 v[86:87], v[86:87], v[86:87]
	s_nop 0
	v_pk_fma_f32 v[86:87], v[88:89], v[88:89], v[86:87]
	s_nop 0
	v_pk_add_f32 v[84:85], v[86:87], v[84:85]
	v_pk_mul_f32 v[86:87], v[52:53], v[82:83] op_sel_hi:[1,0]
	v_pk_mul_f32 v[82:83], v[50:51], v[82:83] op_sel_hi:[1,0]
	v_pk_mul_f32 v[86:87], v[86:87], v[86:87]
	s_nop 0
	v_pk_fma_f32 v[82:83], v[82:83], v[82:83], v[86:87]
	s_nop 0
	v_pk_add_f32 v[82:83], v[82:83], v[84:85]
	s_nop 0
	v_add_f32_e32 v82, v82, v83
	ds_swizzle_b32 v83, v82 offset:swizzle(SWAP,16)
	s_waitcnt lgkmcnt(0)
	v_add_f32_e32 v82, v82, v83
	v_mov_b32_e32 v83, v82
	s_nop 1
	v_permlane32_swap_b32_e32 v82, v83
	s_and_saveexec_b64 s[62:63], s[38:39]
	v_add_f32_e32 v82, v82, v83
	ds_write_b32 v201, v82
	s_or_b64 exec, exec, s[62:63]
	ds_read_b32 v82, v213 offset:576
	s_waitcnt lgkmcnt(0)
	v_pk_mul_f32 v[84:85], v[48:49], v[82:83] op_sel_hi:[1,0]
	v_pk_mul_f32 v[86:87], v[46:47], v[82:83] op_sel_hi:[1,0]
	v_pk_mul_f32 v[84:85], v[84:85], v[84:85]
	v_pk_mul_f32 v[88:89], v[42:43], v[82:83] op_sel_hi:[1,0]
	v_pk_fma_f32 v[84:85], v[86:87], v[86:87], v[84:85]
	v_pk_mul_f32 v[86:87], v[44:45], v[82:83] op_sel_hi:[1,0]
	s_nop 0
	v_pk_mul_f32 v[86:87], v[86:87], v[86:87]
	s_nop 0
	v_pk_fma_f32 v[86:87], v[88:89], v[88:89], v[86:87]
	v_pk_mul_f32 v[88:89], v[38:39], v[82:83] op_sel_hi:[1,0]
	v_pk_add_f32 v[84:85], v[84:85], v[86:87]
	v_pk_mul_f32 v[86:87], v[40:41], v[82:83] op_sel_hi:[1,0]
	s_nop 0
	v_pk_mul_f32 v[86:87], v[86:87], v[86:87]
	s_nop 0
	v_pk_fma_f32 v[86:87], v[88:89], v[88:89], v[86:87]
	s_nop 0
	v_pk_add_f32 v[84:85], v[86:87], v[84:85]
	v_pk_mul_f32 v[86:87], v[36:37], v[82:83] op_sel_hi:[1,0]
	v_pk_mul_f32 v[82:83], v[34:35], v[82:83] op_sel_hi:[1,0]
	v_pk_mul_f32 v[86:87], v[86:87], v[86:87]
	s_nop 0
	v_pk_fma_f32 v[82:83], v[82:83], v[82:83], v[86:87]
	s_nop 0
	v_pk_add_f32 v[82:83], v[82:83], v[84:85]
	s_nop 0
	v_add_f32_e32 v82, v82, v83
	ds_swizzle_b32 v83, v82 offset:swizzle(SWAP,16)
	s_waitcnt lgkmcnt(0)
	v_add_f32_e32 v82, v82, v83
	v_mov_b32_e32 v83, v82
	s_nop 1
	v_permlane32_swap_b32_e32 v82, v83
	s_and_saveexec_b64 s[62:63], s[38:39]
	v_add_f32_e32 v82, v82, v83
	ds_write_b32 v203, v82
	s_or_b64 exec, exec, s[62:63]
	ds_read_b32 v82, v213 offset:640
	s_waitcnt lgkmcnt(0)
	v_pk_mul_f32 v[84:85], v[32:33], v[82:83] op_sel_hi:[1,0]
	v_pk_mul_f32 v[86:87], v[30:31], v[82:83] op_sel_hi:[1,0]
	v_pk_mul_f32 v[84:85], v[84:85], v[84:85]
	v_pk_mul_f32 v[88:89], v[26:27], v[82:83] op_sel_hi:[1,0]
	v_pk_fma_f32 v[84:85], v[86:87], v[86:87], v[84:85]
	v_pk_mul_f32 v[86:87], v[28:29], v[82:83] op_sel_hi:[1,0]
	s_nop 0
	v_pk_mul_f32 v[86:87], v[86:87], v[86:87]
	s_nop 0
	v_pk_fma_f32 v[86:87], v[88:89], v[88:89], v[86:87]
	v_pk_mul_f32 v[88:89], v[22:23], v[82:83] op_sel_hi:[1,0]
	v_pk_add_f32 v[84:85], v[84:85], v[86:87]
	v_pk_mul_f32 v[86:87], v[24:25], v[82:83] op_sel_hi:[1,0]
	s_nop 0
	v_pk_mul_f32 v[86:87], v[86:87], v[86:87]
	s_nop 0
	v_pk_fma_f32 v[86:87], v[88:89], v[88:89], v[86:87]
	s_nop 0
	v_pk_add_f32 v[84:85], v[86:87], v[84:85]
	v_pk_mul_f32 v[86:87], v[20:21], v[82:83] op_sel_hi:[1,0]
	v_pk_mul_f32 v[82:83], v[18:19], v[82:83] op_sel_hi:[1,0]
	v_pk_mul_f32 v[86:87], v[86:87], v[86:87]
	s_nop 0
	v_pk_fma_f32 v[82:83], v[82:83], v[82:83], v[86:87]
	s_nop 0
	v_pk_add_f32 v[82:83], v[82:83], v[84:85]
	s_nop 0
	v_add_f32_e32 v82, v82, v83
	ds_swizzle_b32 v83, v82 offset:swizzle(SWAP,16)
	s_waitcnt lgkmcnt(0)
	v_add_f32_e32 v82, v82, v83
	v_mov_b32_e32 v83, v82
	s_nop 1
	v_permlane32_swap_b32_e32 v82, v83
	s_and_saveexec_b64 s[62:63], s[38:39]
	v_add_f32_e32 v82, v82, v83
	ds_write_b32 v205, v82
	s_or_b64 exec, exec, s[62:63]
	ds_read_b32 v82, v213 offset:704
	s_waitcnt lgkmcnt(0)
	v_pk_mul_f32 v[84:85], v[16:17], v[82:83] op_sel_hi:[1,0]
	v_pk_mul_f32 v[86:87], v[14:15], v[82:83] op_sel_hi:[1,0]
	v_pk_mul_f32 v[84:85], v[84:85], v[84:85]
	v_pk_mul_f32 v[88:89], v[10:11], v[82:83] op_sel_hi:[1,0]
	v_pk_fma_f32 v[84:85], v[86:87], v[86:87], v[84:85]
	v_pk_mul_f32 v[86:87], v[12:13], v[82:83] op_sel_hi:[1,0]
	s_nop 0
	v_pk_mul_f32 v[86:87], v[86:87], v[86:87]
	s_nop 0
	v_pk_fma_f32 v[86:87], v[88:89], v[88:89], v[86:87]
	v_pk_mul_f32 v[88:89], v[6:7], v[82:83] op_sel_hi:[1,0]
	v_pk_add_f32 v[84:85], v[84:85], v[86:87]
	v_pk_mul_f32 v[86:87], v[8:9], v[82:83] op_sel_hi:[1,0]
	s_nop 0
	v_pk_mul_f32 v[86:87], v[86:87], v[86:87]
	s_nop 0
	v_pk_fma_f32 v[86:87], v[88:89], v[88:89], v[86:87]
	s_nop 0
	v_pk_add_f32 v[84:85], v[86:87], v[84:85]
	v_pk_mul_f32 v[86:87], v[4:5], v[82:83] op_sel_hi:[1,0]
	v_pk_mul_f32 v[82:83], v[2:3], v[82:83] op_sel_hi:[1,0]
	v_pk_mul_f32 v[86:87], v[86:87], v[86:87]
	s_nop 0
	v_pk_fma_f32 v[82:83], v[82:83], v[82:83], v[86:87]
	s_nop 0
	v_pk_add_f32 v[82:83], v[82:83], v[84:85]
	s_nop 0
	v_add_f32_e32 v82, v82, v83
	ds_swizzle_b32 v83, v82 offset:swizzle(SWAP,16)
	s_waitcnt lgkmcnt(0)
	v_add_f32_e32 v82, v82, v83
	v_mov_b32_e32 v83, v82
	s_nop 1
	v_permlane32_swap_b32_e32 v82, v83
	s_and_saveexec_b64 s[62:63], s[38:39]
	v_add_f32_e32 v82, v82, v83
	ds_write_b32 v207, v82
	s_or_b64 exec, exec, s[62:63]
	s_waitcnt lgkmcnt(0)
	s_barrier
	global_load_dwordx4 v[94:97], v[168:169], off offset:16
	global_load_dwordx4 v[90:93], v[168:169], off
	global_load_dwordx4 v[82:85], v[168:169], off offset:144
	global_load_dwordx4 v[86:89], v[168:169], off offset:128
	ds_read_b32 v158, v183
	ds_read_b32 v159, v194
	s_lshl_b32 s14, s60, 1
	s_and_b32 s14, s14, 14
	s_lshl_b32 s15, s28, 1
	s_or_b32 s14, s88, s14
	s_waitcnt lgkmcnt(0)
	v_add_f32_e32 v158, v158, v159
	v_fmamk_f32 v158, v158, 0x3c000000, v185
	v_rsq_f32_e32 v160, v158
	ds_read2_b32 v[158:159], v213 offset1:16
	s_and_b32 s15, s15, 0x7fffff0
	s_or_b32 s14, s15, s14
	s_lshl_b32 s15, s28, 2
	s_and_b32 s15, s15, 28
	s_waitcnt lgkmcnt(0)
	v_mul_f32_e32 v158, v158, v160
	v_lshlrev_b64 v[160:161], 12, v[174:175]
	v_lshl_add_u64 v[160:161], s[46:47], 0, v[160:161]
	v_pk_mul_f32 v[144:145], v[144:145], v[158:159] op_sel_hi:[1,0]
	v_pk_mul_f32 v[146:147], v[146:147], v[158:159] op_sel_hi:[1,0]
	v_pk_mul_f32 v[218:219], v[140:141], v[158:159] op_sel_hi:[1,0]
	v_lshl_add_u64 v[160:161], v[160:161], 0, v[114:115]
	v_pk_mul_f32 v[140:141], v[142:143], v[158:159] op_sel_hi:[1,0]
	s_lshl_b32 s14, s14, 5
	s_add_i32 s15, s15, s8
	s_add_i32 s28, s15, s14
	s_ashr_i32 s29, s28, 31
	s_lshl_b64 s[14:15], s[28:29], 9
	s_waitcnt vmcnt(0)
	v_pk_mul_f32 v[142:143], v[94:95], v[218:219]
	v_pk_mul_f32 v[214:215], v[92:93], v[146:147]
	v_pk_mul_f32 v[216:217], v[90:91], v[144:145]
	v_pk_fma_f32 v[218:219], v[90:91], v[144:145], 0 op_sel_hi:[1,1,0]
	v_cvt_pk_bf16_f32 v144, v216, v217
	v_cvt_pk_bf16_f32 v145, v214, v215
	v_pk_mul_f32 v[140:141], v[96:97], v[140:141]
	v_pk_fma_f32 v[220:221], v[92:93], v[146:147], 0 op_sel_hi:[1,1,0]
	v_cvt_pk_bf16_f32 v146, v142, v143
	v_cvt_pk_bf16_f32 v147, v140, v141
	ds_bpermute_b32 v238, v250, v144
	ds_bpermute_b32 v239, v250, v145
	ds_bpermute_b32 v240, v250, v146
	ds_bpermute_b32 v241, v250, v147
	ds_bpermute_b32 v242, v250, v160
	s_nop 1
	v_pk_mul_f32 v[144:145], v[136:137], v[158:159] op_sel_hi:[1,0]
	v_pk_mul_f32 v[136:137], v[138:139], v[158:159] op_sel_hi:[1,0]
	v_pk_mul_f32 v[138:139], v[86:87], v[144:145]
	v_pk_mul_f32 v[144:145], v[132:133], v[158:159] op_sel_hi:[1,0]
	v_pk_mul_f32 v[132:133], v[134:135], v[158:159] op_sel_hi:[1,0]
	v_pk_mul_f32 v[136:137], v[88:89], v[136:137]
	v_pk_mul_f32 v[132:133], v[84:85], v[132:133]
	v_pk_mul_f32 v[134:135], v[82:83], v[144:145]
	v_cvt_pk_bf16_f32 v144, v138, v139
	v_cvt_pk_bf16_f32 v145, v136, v137
	v_cvt_pk_bf16_f32 v147, v132, v133
	s_nop 0
	v_cvt_pk_bf16_f32 v146, v134, v135
	ds_bpermute_b32 v244, v250, v144
	ds_bpermute_b32 v245, v250, v145
	ds_bpermute_b32 v246, v250, v146
	ds_bpermute_b32 v247, v250, v147
	ds_bpermute_b32 v248, v250, v160
	ds_read_b32 v144, v195
	ds_read_b32 v145, v196
	v_lshlrev_b64 v[146:147], 12, v[180:181]
	v_lshl_add_u64 v[146:147], s[46:47], 0, v[146:147]
	v_lshl_add_u64 v[146:147], v[146:147], 0, v[114:115]
	s_waitcnt lgkmcnt(0)
	v_add_f32_e32 v144, v144, v145
	v_fmamk_f32 v144, v144, 0x3c000000, v185
	v_rsq_f32_e32 v144, v144
	s_nop 0
	v_mul_f32_e32 v144, v159, v144
	v_pk_mul_f32 v[128:129], v[128:129], v[144:145] op_sel_hi:[1,0]
	v_pk_mul_f32 v[130:131], v[130:131], v[144:145] op_sel_hi:[1,0]
	v_pk_mul_f32 v[160:161], v[90:91], v[128:129]
	v_pk_mul_f32 v[158:159], v[92:93], v[130:131]
	v_pk_mul_f32 v[180:181], v[124:125], v[144:145] op_sel_hi:[1,0]
	v_pk_mul_f32 v[124:125], v[126:127], v[144:145] op_sel_hi:[1,0]
	v_pk_fma_f32 v[214:215], v[90:91], v[128:129], v[218:219]
	v_cvt_pk_bf16_f32 v128, v160, v161
	v_cvt_pk_bf16_f32 v129, v158, v159
	v_pk_mul_f32 v[124:125], v[96:97], v[124:125]
	v_pk_mul_f32 v[126:127], v[94:95], v[180:181]
	v_pk_fma_f32 v[180:181], v[92:93], v[130:131], v[220:221]
	v_cvt_pk_bf16_f32 v130, v126, v127
	v_cvt_pk_bf16_f32 v131, v124, v125
	ds_bpermute_b32 v232, v250, v128
	ds_bpermute_b32 v233, v250, v129
	ds_bpermute_b32 v234, v250, v130
	ds_bpermute_b32 v235, v250, v131
	ds_bpermute_b32 v236, v250, v146
	s_nop 1
	v_pk_mul_f32 v[128:129], v[120:121], v[144:145] op_sel_hi:[1,0]
	v_pk_mul_f32 v[120:121], v[122:123], v[144:145] op_sel_hi:[1,0]
	v_pk_mul_f32 v[122:123], v[86:87], v[128:129]
	v_pk_mul_f32 v[128:129], v[116:117], v[144:145] op_sel_hi:[1,0]
	v_pk_mul_f32 v[116:117], v[118:119], v[144:145] op_sel_hi:[1,0]
	v_pk_mul_f32 v[120:121], v[88:89], v[120:121]
	v_pk_mul_f32 v[116:117], v[84:85], v[116:117]
	v_pk_mul_f32 v[118:119], v[82:83], v[128:129]
	v_cvt_pk_bf16_f32 v128, v122, v123
	v_cvt_pk_bf16_f32 v129, v120, v121
	v_cvt_pk_bf16_f32 v131, v116, v117
	s_nop 0
	v_cvt_pk_bf16_f32 v130, v118, v119
	s_waitcnt lgkmcnt(12)
	v_subrev_u32_e32 v242, s82, v242
	global_store_dwordx4 v242, v[238:241], s[82:83]
	ds_bpermute_b32 v238, v250, v128
	ds_bpermute_b32 v239, v250, v129
	ds_bpermute_b32 v240, v250, v130
	ds_bpermute_b32 v241, v250, v131
	ds_bpermute_b32 v242, v250, v146
	ds_read_b32 v128, v197
	ds_read_b32 v129, v198
	s_waitcnt lgkmcnt(0)
	v_add_f32_e32 v128, v128, v129
	v_fmamk_f32 v128, v128, 0x3c000000, v185
	v_rsq_f32_e32 v130, v128
	ds_read2_b32 v[128:129], v213 offset0:32 offset1:48
	s_waitcnt lgkmcnt(0)
	v_mul_f32_e32 v128, v128, v130
	v_lshlrev_b64 v[130:131], 12, v[178:179]
	v_pk_mul_f32 v[110:111], v[110:111], v[128:129] op_sel_hi:[1,0]
	v_lshl_add_u64 v[130:131], s[46:47], 0, v[130:131]
	v_pk_mul_f32 v[112:113], v[112:113], v[128:129] op_sel_hi:[1,0]
	v_pk_mul_f32 v[144:145], v[90:91], v[110:111]
	v_lshl_add_u64 v[130:131], v[130:131], 0, v[114:115]
	v_pk_mul_f32 v[146:147], v[92:93], v[112:113]
	v_pk_mul_f32 v[158:159], v[106:107], v[128:129] op_sel_hi:[1,0]
	v_pk_mul_f32 v[106:107], v[108:109], v[128:129] op_sel_hi:[1,0]
	v_cvt_pk_bf16_f32 v144, v144, v145
	v_cvt_pk_bf16_f32 v145, v146, v147
	v_pk_mul_f32 v[108:109], v[94:95], v[158:159]
	v_pk_mul_f32 v[106:107], v[96:97], v[106:107]
	v_cvt_pk_bf16_f32 v146, v108, v109
	v_pk_fma_f32 v[110:111], v[90:91], v[110:111], v[214:215]
	v_cvt_pk_bf16_f32 v147, v106, v107
	s_waitcnt lgkmcnt(15)
	v_subrev_u32_e32 v248, s82, v248
	global_store_dwordx4 v248, v[244:247], s[82:83] offset:64
	ds_bpermute_b32 v244, v250, v144
	ds_bpermute_b32 v245, v250, v145
	ds_bpermute_b32 v246, v250, v146
	ds_bpermute_b32 v247, v250, v147
	ds_bpermute_b32 v248, v250, v130
	v_pk_fma_f32 v[112:113], v[92:93], v[112:113], v[180:181]
	s_nop 0
	v_pk_mul_f32 v[144:145], v[102:103], v[128:129] op_sel_hi:[1,0]
	v_pk_mul_f32 v[102:103], v[104:105], v[128:129] op_sel_hi:[1,0]
	v_pk_mul_f32 v[104:105], v[86:87], v[144:145]
	v_pk_mul_f32 v[144:145], v[98:99], v[128:129] op_sel_hi:[1,0]
	v_pk_mul_f32 v[98:99], v[100:101], v[128:129] op_sel_hi:[1,0]
	v_pk_mul_f32 v[102:103], v[88:89], v[102:103]
	v_pk_mul_f32 v[98:99], v[84:85], v[98:99]
	v_pk_mul_f32 v[100:101], v[82:83], v[144:145]
	v_cvt_pk_bf16_f32 v144, v104, v105
	v_cvt_pk_bf16_f32 v145, v102, v103
	v_cvt_pk_bf16_f32 v147, v98, v99
	s_nop 0
	v_cvt_pk_bf16_f32 v146, v100, v101
	s_waitcnt lgkmcnt(13)
	v_subrev_u32_e32 v236, s82, v236
	global_store_dwordx4 v236, v[232:235], s[82:83]
	ds_bpermute_b32 v232, v250, v144
	ds_bpermute_b32 v233, v250, v145
	ds_bpermute_b32 v234, v250, v146
	ds_bpermute_b32 v235, v250, v147
	ds_bpermute_b32 v236, v250, v130
	ds_read_b32 v128, v199
	ds_read_b32 v130, v200
	s_waitcnt lgkmcnt(0)
	v_add_f32_e32 v128, v128, v130
	v_fmamk_f32 v128, v128, 0x3c000000, v185
	v_rsq_f32_e32 v128, v128
	v_lshlrev_b64 v[130:131], 12, v[176:177]
	v_lshl_add_u64 v[130:131], s[46:47], 0, v[130:131]
	v_lshl_add_u64 v[130:131], v[130:131], 0, v[114:115]
	v_mul_f32_e32 v128, v129, v128
	v_pk_mul_f32 v[144:145], v[78:79], v[128:129] op_sel_hi:[1,0]
	v_pk_mul_f32 v[80:81], v[80:81], v[128:129] op_sel_hi:[1,0]
	v_pk_mul_f32 v[74:75], v[74:75], v[128:129] op_sel_hi:[1,0]
	v_pk_mul_f32 v[76:77], v[76:77], v[128:129] op_sel_hi:[1,0]
	v_pk_mul_f32 v[146:147], v[92:93], v[80:81]
	v_pk_mul_f32 v[158:159], v[90:91], v[144:145]
	v_pk_mul_f32 v[76:77], v[96:97], v[76:77]
	v_pk_mul_f32 v[78:79], v[94:95], v[74:75]
	v_pk_fma_f32 v[160:161], v[92:93], v[80:81], v[112:113]
	v_pk_fma_f32 v[80:81], v[90:91], v[144:145], v[110:111]
	v_cvt_pk_bf16_f32 v110, v158, v159
	v_cvt_pk_bf16_f32 v111, v146, v147
	v_cvt_pk_bf16_f32 v112, v78, v79
	v_cvt_pk_bf16_f32 v113, v76, v77
	v_pk_mul_f32 v[70:71], v[70:71], v[128:129] op_sel_hi:[1,0]
	v_pk_mul_f32 v[72:73], v[72:73], v[128:129] op_sel_hi:[1,0]
	v_pk_mul_f32 v[66:67], v[66:67], v[128:129] op_sel_hi:[1,0]
	v_pk_mul_f32 v[68:69], v[68:69], v[128:129] op_sel_hi:[1,0]
	s_waitcnt lgkmcnt(15)
	v_subrev_u32_e32 v242, s82, v242
	global_store_dwordx4 v242, v[238:241], s[82:83] offset:64
	ds_bpermute_b32 v238, v250, v110
	ds_bpermute_b32 v239, v250, v111
	ds_bpermute_b32 v240, v250, v112
	ds_bpermute_b32 v241, v250, v113
	ds_bpermute_b32 v242, v250, v130
	v_pk_mul_f32 v[72:73], v[88:89], v[72:73]
	v_pk_mul_f32 v[74:75], v[86:87], v[70:71]
	v_pk_mul_f32 v[68:69], v[84:85], v[68:69]
	v_pk_mul_f32 v[70:71], v[82:83], v[66:67]
	v_cvt_pk_bf16_f32 v110, v74, v75
	v_cvt_pk_bf16_f32 v111, v72, v73
	v_cvt_pk_bf16_f32 v113, v68, v69
	v_lshl_add_u64 v[66:67], v[166:167], 0, s[14:15]
	v_cvt_pk_bf16_f32 v112, v70, v71
	s_waitcnt lgkmcnt(12)
	v_subrev_u32_e32 v248, s82, v248
	global_store_dwordx4 v248, v[244:247], s[82:83]
	ds_bpermute_b32 v244, v250, v110
	ds_bpermute_b32 v245, v250, v111
	ds_bpermute_b32 v246, v250, v112
	ds_bpermute_b32 v247, v250, v113
	ds_bpermute_b32 v248, v250, v130
	ds_swizzle_b32 v110, v80 offset:swizzle(SWAP,1)
	ds_swizzle_b32 v111, v81 offset:swizzle(SWAP,1)
	ds_swizzle_b32 v112, v160 offset:swizzle(SWAP,1)
	ds_swizzle_b32 v113, v161 offset:swizzle(SWAP,1)
	s_waitcnt lgkmcnt(2)
	v_pk_add_f32 v[80:81], v[80:81], v[110:111]
	ds_swizzle_b32 v110, v80 offset:swizzle(SWAP,2)
	s_waitcnt lgkmcnt(1)
	v_pk_add_f32 v[112:113], v[160:161], v[112:113]
	ds_swizzle_b32 v111, v81 offset:swizzle(SWAP,2)
	ds_swizzle_b32 v128, v112 offset:swizzle(SWAP,2)
	ds_swizzle_b32 v129, v113 offset:swizzle(SWAP,2)
	s_waitcnt lgkmcnt(2)
	v_pk_add_f32 v[80:81], v[80:81], v[110:111]
	ds_swizzle_b32 v110, v80 offset:swizzle(SWAP,4)
	s_waitcnt lgkmcnt(1)
	v_pk_add_f32 v[112:113], v[112:113], v[128:129]
	ds_swizzle_b32 v111, v81 offset:swizzle(SWAP,4)
	ds_swizzle_b32 v128, v112 offset:swizzle(SWAP,4)
	ds_swizzle_b32 v129, v113 offset:swizzle(SWAP,4)
	s_waitcnt lgkmcnt(2)
	v_pk_add_f32 v[80:81], v[80:81], v[110:111]
	ds_swizzle_b32 v110, v80 offset:swizzle(SWAP,8)
	s_waitcnt lgkmcnt(1)
	v_pk_add_f32 v[112:113], v[112:113], v[128:129]
	ds_swizzle_b32 v111, v81 offset:swizzle(SWAP,8)
	ds_swizzle_b32 v128, v112 offset:swizzle(SWAP,8)
	ds_swizzle_b32 v129, v113 offset:swizzle(SWAP,8)
	s_waitcnt lgkmcnt(15)
	v_subrev_u32_e32 v236, s82, v236
	global_store_dwordx4 v236, v[232:235], s[82:83] offset:64
	s_waitcnt lgkmcnt(15)
	v_subrev_u32_e32 v242, s82, v242
	global_store_dwordx4 v242, v[238:241], s[82:83]
	s_waitcnt lgkmcnt(15)
	v_subrev_u32_e32 v248, s82, v248
	global_store_dwordx4 v248, v[244:247], s[82:83] offset:64
	s_and_saveexec_b64 s[60:61], s[40:41]
	s_cbranch_execz .LBB0_196
	s_waitcnt lgkmcnt(0)
	v_pk_add_f32 v[112:113], v[112:113], v[128:129]
	v_pk_add_f32 v[110:111], v[80:81], v[110:111]
	global_store_dwordx4 v[66:67], v[110:113], off

.LBB0_202:
	s_or_b64 exec, exec, s[60:61]
	ds_read_b32 v66, v201
	ds_read_b32 v67, v202
	ds_read2_b32 v[68:69], v213 offset0:128 offset1:144
	s_mov_b64 s[14:15], 0x80000
	s_waitcnt lgkmcnt(1)
	v_add_f32_e32 v66, v66, v67
	v_fmamk_f32 v66, v66, 0x3c000000, v185
	v_rsq_f32_e32 v66, v66
	s_waitcnt lgkmcnt(0)
	v_mul_f32_e32 v68, v68, v66
	v_lshlrev_b64 v[66:67], 12, v[174:175]
	v_lshl_add_u64 v[66:67], s[46:47], 0, v[66:67]
	v_lshl_add_u64 v[66:67], v[66:67], 0, v[114:115]
	v_pk_mul_f32 v[64:65], v[64:65], v[68:69] op_sel_hi:[1,0]
	v_lshl_add_u64 v[70:71], v[66:67], 0, s[14:15]
	v_pk_mul_f32 v[62:63], v[62:63], v[68:69] op_sel_hi:[1,0]
	v_pk_mul_f32 v[72:73], v[92:93], v[64:65]
	v_pk_mul_f32 v[76:77], v[58:59], v[68:69] op_sel_hi:[1,0]
	s_mov_b32 s14, 0x80000
	v_pk_mul_f32 v[74:75], v[90:91], v[62:63]
	v_pk_mul_f32 v[58:59], v[60:61], v[68:69] op_sel_hi:[1,0]
	v_pk_mul_f32 v[60:61], v[94:95], v[76:77]
	v_pk_fma_f32 v[76:77], v[90:91], v[62:63], 0 op_sel_hi:[1,1,0]
	v_cvt_pk_bf16_f32 v63, v72, v73
	v_add_co_u32_e32 v72, vcc, s14, v66
	v_cvt_pk_bf16_f32 v62, v74, v75
	v_pk_mul_f32 v[58:59], v[96:97], v[58:59]
	s_nop 0
	v_addc_co_u32_e32 v73, vcc, 0, v67, vcc
	v_pk_fma_f32 v[78:79], v[92:93], v[64:65], 0 op_sel_hi:[1,1,0]
	v_cvt_pk_bf16_f32 v64, v60, v61
	v_cvt_pk_bf16_f32 v65, v58, v59
	ds_bpermute_b32 v232, v250, v62
	ds_bpermute_b32 v233, v250, v63
	ds_bpermute_b32 v234, v250, v64
	ds_bpermute_b32 v235, v250, v65
	ds_bpermute_b32 v236, v250, v72
	s_mov_b64 s[14:15], 0x90000
	s_nop 0
	v_pk_mul_f32 v[62:63], v[54:55], v[68:69] op_sel_hi:[1,0]
	v_pk_mul_f32 v[54:55], v[56:57], v[68:69] op_sel_hi:[1,0]
	v_pk_mul_f32 v[56:57], v[86:87], v[62:63]
	v_pk_mul_f32 v[62:63], v[50:51], v[68:69] op_sel_hi:[1,0]
	v_pk_mul_f32 v[50:51], v[52:53], v[68:69] op_sel_hi:[1,0]
	v_pk_mul_f32 v[54:55], v[88:89], v[54:55]
	v_pk_mul_f32 v[50:51], v[84:85], v[50:51]
	v_pk_mul_f32 v[52:53], v[82:83], v[62:63]
	v_cvt_pk_bf16_f32 v62, v56, v57
	v_cvt_pk_bf16_f32 v63, v54, v55
	v_cvt_pk_bf16_f32 v65, v50, v51
	s_nop 0
	v_cvt_pk_bf16_f32 v64, v52, v53
	ds_bpermute_b32 v238, v250, v62
	ds_bpermute_b32 v239, v250, v63
	ds_bpermute_b32 v240, v250, v64
	ds_bpermute_b32 v241, v250, v65
	ds_bpermute_b32 v242, v250, v70
	ds_read_b32 v62, v203
	ds_read_b32 v63, v204
	v_lshl_add_u64 v[64:65], v[66:67], 0, s[14:15]
	s_mov_b32 s14, 0x90000
	s_waitcnt lgkmcnt(0)
	v_add_f32_e32 v62, v62, v63
	v_fmamk_f32 v62, v62, 0x3c000000, v185
	v_rsq_f32_e32 v62, v62
	s_nop 0
	v_mul_f32_e32 v62, v69, v62
	v_pk_mul_f32 v[48:49], v[48:49], v[62:63] op_sel_hi:[1,0]
	v_pk_mul_f32 v[46:47], v[46:47], v[62:63] op_sel_hi:[1,0]
	v_pk_mul_f32 v[68:69], v[92:93], v[48:49]
	v_pk_mul_f32 v[70:71], v[90:91], v[46:47]
	v_pk_fma_f32 v[74:75], v[90:91], v[46:47], v[76:77]
	v_cvt_pk_bf16_f32 v47, v68, v69
	v_add_co_u32_e32 v68, vcc, s14, v66
	v_pk_mul_f32 v[72:73], v[42:43], v[62:63] op_sel_hi:[1,0]
	v_pk_mul_f32 v[42:43], v[44:45], v[62:63] op_sel_hi:[1,0]
	v_cvt_pk_bf16_f32 v46, v70, v71
	v_addc_co_u32_e32 v69, vcc, 0, v67, vcc
	v_pk_mul_f32 v[42:43], v[96:97], v[42:43]
	v_pk_mul_f32 v[44:45], v[94:95], v[72:73]
	v_pk_fma_f32 v[72:73], v[92:93], v[48:49], v[78:79]
	v_cvt_pk_bf16_f32 v48, v44, v45
	v_cvt_pk_bf16_f32 v49, v42, v43
	ds_bpermute_b32 v244, v250, v46
	ds_bpermute_b32 v245, v250, v47
	ds_bpermute_b32 v246, v250, v48
	ds_bpermute_b32 v247, v250, v49
	ds_bpermute_b32 v248, v250, v68
	s_mov_b64 s[14:15], 0xa0000
	s_nop 0
	v_pk_mul_f32 v[46:47], v[38:39], v[62:63] op_sel_hi:[1,0]
	v_pk_mul_f32 v[38:39], v[40:41], v[62:63] op_sel_hi:[1,0]
	v_pk_mul_f32 v[40:41], v[86:87], v[46:47]
	v_pk_mul_f32 v[46:47], v[34:35], v[62:63] op_sel_hi:[1,0]
	v_pk_mul_f32 v[34:35], v[36:37], v[62:63] op_sel_hi:[1,0]
	v_pk_mul_f32 v[38:39], v[88:89], v[38:39]
	v_pk_mul_f32 v[34:35], v[84:85], v[34:35]
	v_pk_mul_f32 v[36:37], v[82:83], v[46:47]
	v_cvt_pk_bf16_f32 v46, v40, v41
	v_cvt_pk_bf16_f32 v47, v38, v39
	v_cvt_pk_bf16_f32 v49, v34, v35
	s_nop 0
	v_cvt_pk_bf16_f32 v48, v36, v37
	s_waitcnt lgkmcnt(12)
	v_subrev_u32_e32 v236, s82, v236
	global_store_dwordx4 v236, v[232:235], s[82:83]
	ds_bpermute_b32 v232, v250, v46
	ds_bpermute_b32 v233, v250, v47
	ds_bpermute_b32 v234, v250, v48
	ds_bpermute_b32 v235, v250, v49
	ds_bpermute_b32 v236, v250, v64
	ds_read_b32 v46, v205
	ds_read_b32 v47, v206
	s_waitcnt lgkmcnt(0)
	v_add_f32_e32 v46, v46, v47
	v_fmamk_f32 v46, v46, 0x3c000000, v185
	v_rsq_f32_e32 v48, v46
	ds_read2_b32 v[46:47], v213 offset0:160 offset1:176
	s_waitcnt lgkmcnt(0)
	v_mul_f32_e32 v46, v46, v48
	v_lshl_add_u64 v[48:49], v[66:67], 0, s[14:15]
	v_pk_mul_f32 v[30:31], v[30:31], v[46:47] op_sel_hi:[1,0]
	v_pk_mul_f32 v[68:69], v[26:27], v[46:47] op_sel_hi:[1,0]
	s_mov_b32 s14, 0xa0000
	v_pk_mul_f32 v[32:33], v[32:33], v[46:47] op_sel_hi:[1,0]
	v_pk_mul_f32 v[62:63], v[90:91], v[30:31]
	v_pk_mul_f32 v[26:27], v[28:29], v[46:47] op_sel_hi:[1,0]
	v_pk_mul_f32 v[28:29], v[94:95], v[68:69]
	v_add_co_u32_e32 v68, vcc, s14, v66
	v_pk_mul_f32 v[64:65], v[92:93], v[32:33]
	v_cvt_pk_bf16_f32 v62, v62, v63
	s_nop 0
	v_addc_co_u32_e32 v69, vcc, 0, v67, vcc
	v_cvt_pk_bf16_f32 v63, v64, v65
	v_pk_mul_f32 v[26:27], v[96:97], v[26:27]
	v_cvt_pk_bf16_f32 v64, v28, v29
	s_mov_b64 s[14:15], 0xb0000
	v_cvt_pk_bf16_f32 v65, v26, v27
	s_waitcnt lgkmcnt(15)
	v_subrev_u32_e32 v242, s82, v242
	global_store_dwordx4 v242, v[238:241], s[82:83] offset:64
	ds_bpermute_b32 v238, v250, v62
	ds_bpermute_b32 v239, v250, v63
	ds_bpermute_b32 v240, v250, v64
	ds_bpermute_b32 v241, v250, v65
	ds_bpermute_b32 v242, v250, v68
	v_pk_fma_f32 v[30:31], v[90:91], v[30:31], v[74:75]
	v_pk_fma_f32 v[32:33], v[92:93], v[32:33], v[72:73]
	v_pk_mul_f32 v[62:63], v[22:23], v[46:47] op_sel_hi:[1,0]
	v_pk_mul_f32 v[22:23], v[24:25], v[46:47] op_sel_hi:[1,0]
	v_pk_mul_f32 v[24:25], v[86:87], v[62:63]
	v_pk_mul_f32 v[62:63], v[18:19], v[46:47] op_sel_hi:[1,0]
	v_pk_mul_f32 v[18:19], v[20:21], v[46:47] op_sel_hi:[1,0]
	v_pk_mul_f32 v[22:23], v[88:89], v[22:23]
	v_pk_mul_f32 v[18:19], v[84:85], v[18:19]
	v_pk_mul_f32 v[20:21], v[82:83], v[62:63]
	v_cvt_pk_bf16_f32 v62, v24, v25
	v_cvt_pk_bf16_f32 v63, v22, v23
	v_cvt_pk_bf16_f32 v65, v18, v19
	s_nop 0
	v_cvt_pk_bf16_f32 v64, v20, v21
	s_waitcnt lgkmcnt(13)
	v_subrev_u32_e32 v248, s82, v248
	global_store_dwordx4 v248, v[244:247], s[82:83]
	ds_bpermute_b32 v244, v250, v62
	ds_bpermute_b32 v245, v250, v63
	ds_bpermute_b32 v246, v250, v64
	ds_bpermute_b32 v247, v250, v65
	ds_bpermute_b32 v248, v250, v48
	ds_read_b32 v46, v207
	ds_read_b32 v48, v208
	s_waitcnt lgkmcnt(0)
	v_add_f32_e32 v46, v46, v48
	v_fmamk_f32 v46, v46, 0x3c000000, v185
	v_rsq_f32_e32 v46, v46
	v_lshl_add_u64 v[48:49], v[66:67], 0, s[14:15]
	s_mov_b32 s14, 0xb0000
	v_mul_f32_e32 v46, v47, v46
	v_pk_mul_f32 v[10:11], v[10:11], v[46:47] op_sel_hi:[1,0]
	v_pk_mul_f32 v[62:63], v[14:15], v[46:47] op_sel_hi:[1,0]
	v_pk_mul_f32 v[16:17], v[16:17], v[46:47] op_sel_hi:[1,0]
	v_pk_mul_f32 v[12:13], v[12:13], v[46:47] op_sel_hi:[1,0]
	v_pk_mul_f32 v[14:15], v[94:95], v[10:11]
	v_add_co_u32_e32 v10, vcc, s14, v66
	v_pk_mul_f32 v[64:65], v[92:93], v[16:17]
	v_pk_mul_f32 v[68:69], v[90:91], v[62:63]
	v_pk_mul_f32 v[12:13], v[96:97], v[12:13]
	v_pk_fma_f32 v[70:71], v[92:93], v[16:17], v[32:33]
	v_pk_fma_f32 v[16:17], v[90:91], v[62:63], v[30:31]
	v_cvt_pk_bf16_f32 v30, v68, v69
	v_cvt_pk_bf16_f32 v31, v64, v65
	v_cvt_pk_bf16_f32 v32, v14, v15
	v_cvt_pk_bf16_f32 v33, v12, v13
	v_addc_co_u32_e32 v11, vcc, 0, v67, vcc
	v_pk_mul_f32 v[6:7], v[6:7], v[46:47] op_sel_hi:[1,0]
	v_pk_mul_f32 v[8:9], v[8:9], v[46:47] op_sel_hi:[1,0]
	v_pk_mul_f32 v[2:3], v[2:3], v[46:47] op_sel_hi:[1,0]
	v_pk_mul_f32 v[4:5], v[4:5], v[46:47] op_sel_hi:[1,0]
	s_waitcnt lgkmcnt(15)
	v_subrev_u32_e32 v236, s82, v236
	global_store_dwordx4 v236, v[232:235], s[82:83] offset:64
	ds_bpermute_b32 v232, v250, v30
	ds_bpermute_b32 v233, v250, v31
	ds_bpermute_b32 v234, v250, v32
	ds_bpermute_b32 v235, v250, v33
	ds_bpermute_b32 v236, v250, v10
	v_pk_mul_f32 v[8:9], v[88:89], v[8:9]
	v_pk_mul_f32 v[10:11], v[86:87], v[6:7]
	v_pk_mul_f32 v[4:5], v[84:85], v[4:5]
	v_pk_mul_f32 v[6:7], v[82:83], v[2:3]
	v_cvt_pk_bf16_f32 v30, v10, v11
	v_cvt_pk_bf16_f32 v31, v8, v9
	v_cvt_pk_bf16_f32 v33, v4, v5
	s_add_i32 s14, s28, 2
	v_cvt_pk_bf16_f32 v32, v6, v7
	s_waitcnt lgkmcnt(12)
	v_subrev_u32_e32 v242, s82, v242
	global_store_dwordx4 v242, v[238:241], s[82:83]
	ds_bpermute_b32 v238, v250, v30
	ds_bpermute_b32 v239, v250, v31
	ds_bpermute_b32 v240, v250, v32
	ds_bpermute_b32 v241, v250, v33
	ds_bpermute_b32 v242, v250, v48
	ds_swizzle_b32 v30, v16 offset:swizzle(SWAP,1)
	ds_swizzle_b32 v31, v17 offset:swizzle(SWAP,1)
	ds_swizzle_b32 v32, v70 offset:swizzle(SWAP,1)
	ds_swizzle_b32 v33, v71 offset:swizzle(SWAP,1)
	s_ashr_i32 s15, s14, 31
	s_lshl_b64 s[14:15], s[14:15], 9
	s_waitcnt lgkmcnt(2)
	v_pk_add_f32 v[16:17], v[16:17], v[30:31]
	ds_swizzle_b32 v30, v16 offset:swizzle(SWAP,2)
	s_waitcnt lgkmcnt(1)
	v_pk_add_f32 v[32:33], v[70:71], v[32:33]
	ds_swizzle_b32 v31, v17 offset:swizzle(SWAP,2)
	ds_swizzle_b32 v46, v32 offset:swizzle(SWAP,2)
	ds_swizzle_b32 v47, v33 offset:swizzle(SWAP,2)
	v_lshl_add_u64 v[2:3], v[166:167], 0, s[14:15]
	s_waitcnt lgkmcnt(2)
	v_pk_add_f32 v[16:17], v[16:17], v[30:31]
	ds_swizzle_b32 v30, v16 offset:swizzle(SWAP,4)
	s_waitcnt lgkmcnt(1)
	v_pk_add_f32 v[32:33], v[32:33], v[46:47]
	ds_swizzle_b32 v31, v17 offset:swizzle(SWAP,4)
	ds_swizzle_b32 v46, v32 offset:swizzle(SWAP,4)
	ds_swizzle_b32 v47, v33 offset:swizzle(SWAP,4)
	s_waitcnt lgkmcnt(2)
	v_pk_add_f32 v[16:17], v[16:17], v[30:31]
	ds_swizzle_b32 v30, v16 offset:swizzle(SWAP,8)
	s_waitcnt lgkmcnt(1)
	v_pk_add_f32 v[32:33], v[32:33], v[46:47]
	ds_swizzle_b32 v31, v17 offset:swizzle(SWAP,8)
	ds_swizzle_b32 v46, v32 offset:swizzle(SWAP,8)
	ds_swizzle_b32 v47, v33 offset:swizzle(SWAP,8)
	s_waitcnt lgkmcnt(15)
	v_subrev_u32_e32 v248, s82, v248
	global_store_dwordx4 v248, v[244:247], s[82:83] offset:64
	s_waitcnt lgkmcnt(15)
	v_subrev_u32_e32 v236, s82, v236
	global_store_dwordx4 v236, v[232:235], s[82:83]
	s_waitcnt lgkmcnt(15)
	v_subrev_u32_e32 v242, s82, v242
	global_store_dwordx4 v242, v[238:241], s[82:83] offset:64
	s_and_saveexec_b64 s[28:29], s[40:41]
	s_cbranch_execz .LBB0_204
	s_waitcnt lgkmcnt(0)
	v_pk_add_f32 v[32:33], v[32:33], v[46:47]
	v_pk_add_f32 v[30:31], v[16:17], v[30:31]
	global_store_dwordx4 v[2:3], v[30:33], off

.LBB0_384:
	s_and_b64 vcc, exec, s[40:41]
	s_cbranch_vccz .LBB0_383
	v_lshlrev_b32_e32 v155, 2, v177
	global_load_dwordx4 v[136:139], v155, s[44:45]
	global_load_dwordx4 v[132:135], v155, s[44:45] offset:16
	s_waitcnt lgkmcnt(0)
	v_mul_f32_e32 v160, v128, v154
	v_mul_f32_e32 v161, v129, v154
	v_mul_f32_e32 v166, v130, v154
	v_mul_f32_e32 v167, v131, v154
	v_mul_f32_e32 v168, v124, v154
	v_mul_f32_e32 v169, v125, v154
	v_mul_f32_e32 v170, v126, v154
	v_mul_f32_e32 v171, v127, v154
	global_load_dwordx4 v[124:127], v155, s[44:45] offset:144
	global_load_dwordx4 v[128:131], v155, s[44:45] offset:128
	v_ashrrev_i32_e32 v153, 31, v152
	v_lshlrev_b64 v[158:159], 12, v[152:153]
	v_max_f32_e32 v153, 0xc2a00000, v160
	v_max_f32_e32 v155, 0xc2a00000, v161
	v_max_f32_e32 v160, 0xc2a00000, v166
	v_max_f32_e32 v161, 0xc2a00000, v167
	v_max_f32_e32 v166, 0xc2a00000, v168
	v_max_f32_e32 v167, 0xc2a00000, v169
	v_max_f32_e32 v168, 0xc2a00000, v170
	v_max_f32_e32 v169, 0xc2a00000, v171
	v_mul_f32_e32 v153, 0xbfb8aa3b, v153
	v_mul_f32_e32 v155, 0xbfb8aa3b, v155
	v_mul_f32_e32 v168, 0xbfb8aa3b, v168
	v_mul_f32_e32 v169, 0xbfb8aa3b, v169
	v_exp_f32_e32 v153, v153
	v_exp_f32_e32 v155, v155
	v_mul_f32_e32 v160, 0xbfb8aa3b, v160
	v_mul_f32_e32 v161, 0xbfb8aa3b, v161
	v_exp_f32_e32 v168, v168
	v_exp_f32_e32 v169, v169
	v_exp_f32_e32 v160, v160
	v_exp_f32_e32 v161, v161
	v_mul_f32_e32 v120, v120, v154
	v_max_f32_e32 v120, 0xc2a00000, v120
	v_add_f32_e32 v153, 1.0, v153
	v_add_f32_e32 v155, 1.0, v155
	v_mul_f32_e32 v121, v121, v154
	v_lshlrev_b32_e32 v114, 1, v177
	v_mul_f32_e32 v166, 0xbfb8aa3b, v166
	v_mul_f32_e32 v167, 0xbfb8aa3b, v167
	v_lshl_add_u64 v[158:159], s[42:43], 0, v[158:159]
	v_add_f32_e32 v168, 1.0, v168
	v_add_f32_e32 v169, 1.0, v169
	v_rcp_f32_e32 v153, v153
	v_rcp_f32_e32 v181, v155
	v_mul_f32_e32 v120, 0xbfb8aa3b, v120
	v_max_f32_e32 v121, 0xc2a00000, v121
	v_exp_f32_e32 v170, v166
	v_exp_f32_e32 v171, v167
	v_lshl_add_u64 v[166:167], v[158:159], 0, v[114:115]
	v_add_f32_e32 v158, 1.0, v160
	v_add_f32_e32 v159, 1.0, v161
	v_rcp_f32_e32 v168, v168
	v_rcp_f32_e32 v182, v169
	v_exp_f32_e32 v120, v120
	v_mul_f32_e32 v121, 0xbfb8aa3b, v121
	v_rcp_f32_e32 v158, v158
	v_rcp_f32_e32 v159, v159
	v_exp_f32_e32 v121, v121
	v_add_f32_e32 v120, 1.0, v120
	v_rcp_f32_e32 v120, v120
	v_mul_f32_e32 v116, v116, v154
	v_add_f32_e32 v121, 1.0, v121
	v_rcp_f32_e32 v121, v121
	v_add_f32_e32 v160, 1.0, v170
	v_add_f32_e32 v161, 1.0, v171
	v_max_f32_e32 v116, 0xc2a00000, v116
	v_mul_f32_e32 v117, v117, v154
	v_rcp_f32_e32 v160, v160
	v_rcp_f32_e32 v161, v161
	v_mul_f32_e32 v116, 0xbfb8aa3b, v116
	v_max_f32_e32 v117, 0xc2a00000, v117
	v_exp_f32_e32 v116, v116
	v_mul_f32_e32 v117, 0xbfb8aa3b, v117
	v_exp_f32_e32 v117, v117
	s_mov_b64 s[14:15], 0x80000
	v_add_f32_e32 v116, 1.0, v116
	v_rcp_f32_e32 v116, v116
	v_add_f32_e32 v117, 1.0, v117
	s_waitcnt vmcnt(0)
	v_sub_f32_e32 v180, 1.0, v136
	v_sub_f32_e32 v179, 1.0, v137
	v_sub_f32_e32 v169, 1.0, v134
	v_sub_f32_e32 v155, 1.0, v135
	v_fma_f32 v153, v180, v153, v136
	v_fma_f32 v181, v179, v181, v137
	v_sub_f32_e32 v178, 1.0, v138
	v_sub_f32_e32 v177, 1.0, v139
	v_fma_f32 v168, v169, v168, v134
	v_fma_f32 v182, v155, v182, v135
	v_log_f32_e32 v153, v153
	v_log_f32_e32 v181, v181
	v_fma_f32 v158, v178, v158, v138
	v_fma_f32 v159, v177, v159, v139
	v_log_f32_e32 v168, v168
	v_log_f32_e32 v182, v182
	v_log_f32_e32 v158, v158
	v_log_f32_e32 v159, v159
	v_cvt_pk_f16_f32 v194, v153, v181
	v_sub_f32_e32 v153, 1.0, v128
	v_cvt_pk_f16_f32 v197, v168, v182
	v_fma_f32 v120, v153, v120, v128
	v_sub_f32_e32 v168, 1.0, v129
	v_cvt_pk_f16_f32 v195, v158, v159
	v_log_f32_e32 v158, v120
	v_fma_f32 v120, v168, v121, v129
	v_log_f32_e32 v159, v120
	v_mul_f32_e32 v120, v122, v154
	v_max_f32_e32 v120, 0xc2a00000, v120
	v_mul_f32_e32 v121, v123, v154
	v_mul_f32_e32 v120, 0xbfb8aa3b, v120
	v_max_f32_e32 v121, 0xc2a00000, v121
	v_exp_f32_e32 v120, v120
	v_mul_f32_e32 v121, 0xbfb8aa3b, v121
	v_exp_f32_e32 v122, v121
	v_sub_f32_e32 v171, 1.0, v132
	v_sub_f32_e32 v170, 1.0, v133
	v_add_f32_e32 v120, 1.0, v120
	v_fma_f32 v160, v171, v160, v132
	v_fma_f32 v161, v170, v161, v133
	v_rcp_f32_e32 v120, v120
	v_add_f32_e32 v122, 1.0, v122
	v_log_f32_e32 v160, v160
	v_log_f32_e32 v161, v161
	v_rcp_f32_e32 v123, v122
	v_sub_f32_e32 v121, 1.0, v130
	v_rcp_f32_e32 v117, v117
	v_fma_f32 v120, v121, v120, v130
	v_sub_f32_e32 v122, 1.0, v131
	v_cvt_pk_f16_f32 v196, v160, v161
	v_log_f32_e32 v160, v120
	v_fma_f32 v120, v122, v123, v131
	v_sub_f32_e32 v123, 1.0, v124
	v_log_f32_e32 v161, v120
	v_fma_f32 v116, v123, v116, v124
	v_sub_f32_e32 v120, 1.0, v125
	v_log_f32_e32 v181, v116
	v_fma_f32 v116, v120, v117, v125
	v_log_f32_e32 v182, v116
	v_mul_f32_e32 v116, v118, v154
	v_max_f32_e32 v116, 0xc2a00000, v116
	v_mul_f32_e32 v117, v119, v154
	v_mul_f32_e32 v116, 0xbfb8aa3b, v116
	v_max_f32_e32 v117, 0xc2a00000, v117
	v_exp_f32_e32 v116, v116
	v_mul_f32_e32 v117, 0xbfb8aa3b, v117
	v_exp_f32_e32 v117, v117
	v_sub_f32_e32 v118, 1.0, v126
	v_add_f32_e32 v116, 1.0, v116
	v_rcp_f32_e32 v116, v116
	v_add_f32_e32 v117, 1.0, v117
	v_rcp_f32_e32 v117, v117
	v_sub_f32_e32 v119, 1.0, v127
	v_fma_f32 v116, v118, v116, v126
	v_log_f32_e32 v154, v116
	v_fma_f32 v116, v119, v117, v127
	v_log_f32_e32 v183, v116
	ds_read2_b32 v[116:117], v176 offset0:16 offset1:32
	ds_bpermute_b32 v238, v250, v194
	ds_bpermute_b32 v239, v250, v195
	ds_bpermute_b32 v240, v250, v196
	ds_bpermute_b32 v241, v250, v197
	ds_bpermute_b32 v242, v250, v166
	s_waitcnt lgkmcnt(0)
	v_mul_f32_e32 v106, v106, v116
	v_max_f32_e32 v106, 0xc2a00000, v106
	v_mul_f32_e32 v106, 0xbfb8aa3b, v106
	v_exp_f32_e32 v106, v106
	v_mul_f32_e32 v110, v110, v116
	v_max_f32_e32 v110, 0xc2a00000, v110
	v_mul_f32_e32 v111, v111, v116
	v_mul_f32_e32 v110, 0xbfb8aa3b, v110
	v_max_f32_e32 v111, 0xc2a00000, v111
	v_mul_f32_e32 v107, v107, v116
	v_exp_f32_e32 v110, v110
	v_mul_f32_e32 v111, 0xbfb8aa3b, v111
	v_add_f32_e32 v106, 1.0, v106
	v_max_f32_e32 v107, 0xc2a00000, v107
	v_exp_f32_e32 v111, v111
	v_rcp_f32_e32 v106, v106
	v_mul_f32_e32 v107, 0xbfb8aa3b, v107
	v_exp_f32_e32 v107, v107
	v_cvt_pk_f16_f32 v194, v158, v159
	v_or_b32_e32 v158, 16, v152
	v_add_f32_e32 v110, 1.0, v110
	v_mul_f32_e32 v112, v112, v116
	v_mul_f32_e32 v113, v113, v116
	v_cvt_pk_f16_f32 v197, v154, v183
	v_ashrrev_i32_e32 v159, 31, v158
	v_rcp_f32_e32 v154, v110
	v_add_f32_e32 v110, 1.0, v111
	v_max_f32_e32 v112, 0xc2a00000, v112
	v_max_f32_e32 v113, 0xc2a00000, v113
	v_fma_f32 v106, v171, v106, v132
	v_cvt_pk_f16_f32 v195, v160, v161
	v_rcp_f32_e32 v160, v110
	v_lshlrev_b64 v[110:111], 12, v[158:159]
	v_mul_f32_e32 v112, 0xbfb8aa3b, v112
	v_mul_f32_e32 v113, 0xbfb8aa3b, v113
	v_log_f32_e32 v159, v106
	v_add_f32_e32 v106, 1.0, v107
	v_mul_f32_e32 v107, v108, v116
	v_exp_f32_e32 v112, v112
	v_exp_f32_e32 v113, v113
	v_max_f32_e32 v107, 0xc2a00000, v107
	v_mul_f32_e32 v108, v109, v116
	v_mul_f32_e32 v107, 0xbfb8aa3b, v107
	v_max_f32_e32 v108, 0xc2a00000, v108
	v_exp_f32_e32 v107, v107
	v_mul_f32_e32 v108, 0xbfb8aa3b, v108
	v_exp_f32_e32 v108, v108
	v_add_f32_e32 v112, 1.0, v112
	v_add_f32_e32 v113, 1.0, v113
	v_rcp_f32_e32 v112, v112
	v_rcp_f32_e32 v113, v113
	v_mul_f32_e32 v98, v98, v116
	v_rcp_f32_e32 v106, v106
	v_add_f32_e32 v107, 1.0, v107
	v_max_f32_e32 v98, 0xc2a00000, v98
	v_rcp_f32_e32 v107, v107
	v_add_f32_e32 v108, 1.0, v108
	v_mul_f32_e32 v98, 0xbfb8aa3b, v98
	v_rcp_f32_e32 v108, v108
	v_exp_f32_e32 v98, v98
	v_fma_f32 v112, v178, v112, v138
	v_fma_f32 v113, v177, v113, v139
	v_log_f32_e32 v112, v112
	v_log_f32_e32 v113, v113
	v_fma_f32 v106, v170, v106, v133
	v_log_f32_e32 v109, v106
	v_fma_f32 v106, v169, v107, v134
	v_mul_f32_e32 v102, v102, v116
	v_mul_f32_e32 v99, v99, v116
	v_fma_f32 v154, v180, v154, v136
	v_fma_f32 v158, v179, v160, v137
	v_log_f32_e32 v160, v106
	v_fma_f32 v106, v155, v108, v135
	v_max_f32_e32 v102, 0xc2a00000, v102
	v_add_f32_e32 v98, 1.0, v98
	v_max_f32_e32 v99, 0xc2a00000, v99
	v_log_f32_e32 v154, v154
	v_log_f32_e32 v158, v158
	v_log_f32_e32 v161, v106
	v_mul_f32_e32 v102, 0xbfb8aa3b, v102
	v_rcp_f32_e32 v98, v98
	v_mul_f32_e32 v99, 0xbfb8aa3b, v99
	v_cvt_pk_f16_f32 v107, v112, v113
	v_exp_f32_e32 v112, v102
	v_mul_f32_e32 v102, v103, v116
	v_exp_f32_e32 v99, v99
	v_max_f32_e32 v102, 0xc2a00000, v102
	v_lshl_add_u64 v[110:111], s[42:43], 0, v[110:111]
	v_mul_f32_e32 v102, 0xbfb8aa3b, v102
	v_cvt_pk_f16_f32 v106, v154, v158
	v_cvt_pk_f16_f32 v108, v159, v109
	v_cvt_pk_f16_f32 v109, v160, v161
	v_exp_f32_e32 v113, v102
	v_lshl_add_u64 v[102:103], v[110:111], 0, v[114:115]
	v_fma_f32 v98, v123, v98, v124
	ds_bpermute_b32 v244, v250, v106
	ds_bpermute_b32 v245, v250, v107
	ds_bpermute_b32 v246, v250, v108
	ds_bpermute_b32 v247, v250, v109
	ds_bpermute_b32 v248, v250, v102
	v_mul_f32_e32 v104, v104, v116
	v_mul_f32_e32 v105, v105, v116
	v_log_f32_e32 v108, v98
	v_add_f32_e32 v98, 1.0, v99
	v_mul_f32_e32 v99, v100, v116
	v_max_f32_e32 v99, 0xc2a00000, v99
	v_mul_f32_e32 v100, v101, v116
	v_max_f32_e32 v104, 0xc2a00000, v104
	v_max_f32_e32 v105, 0xc2a00000, v105
	v_mul_f32_e32 v99, 0xbfb8aa3b, v99
	v_max_f32_e32 v100, 0xc2a00000, v100
	v_mul_f32_e32 v104, 0xbfb8aa3b, v104
	v_mul_f32_e32 v105, 0xbfb8aa3b, v105
	v_exp_f32_e32 v99, v99
	v_mul_f32_e32 v100, 0xbfb8aa3b, v100
	v_exp_f32_e32 v104, v104
	v_exp_f32_e32 v105, v105
	v_exp_f32_e32 v100, v100
	v_rcp_f32_e32 v98, v98
	v_add_f32_e32 v99, 1.0, v99
	v_add_f32_e32 v110, 1.0, v112
	v_add_f32_e32 v111, 1.0, v113
	v_add_f32_e32 v104, 1.0, v104
	v_add_f32_e32 v105, 1.0, v105
	v_rcp_f32_e32 v99, v99
	v_add_f32_e32 v100, 1.0, v100
	v_rcp_f32_e32 v110, v110
	v_rcp_f32_e32 v111, v111
	v_rcp_f32_e32 v104, v104
	v_rcp_f32_e32 v105, v105
	v_rcp_f32_e32 v100, v100
	v_mul_f32_e32 v90, v90, v117
	v_fma_f32 v98, v120, v98, v125
	v_mul_f32_e32 v94, v94, v117
	v_max_f32_e32 v90, 0xc2a00000, v90
	v_log_f32_e32 v101, v98
	v_fma_f32 v98, v118, v99, v126
	v_max_f32_e32 v94, 0xc2a00000, v94
	v_mul_f32_e32 v90, 0xbfb8aa3b, v90
	v_fma_f32 v106, v153, v110, v128
	v_fma_f32 v107, v168, v111, v129
	v_fma_f32 v104, v121, v104, v130
	v_fma_f32 v105, v122, v105, v131
	v_log_f32_e32 v109, v98
	v_fma_f32 v98, v119, v100, v127
	v_mul_f32_e32 v94, 0xbfb8aa3b, v94
	v_exp_f32_e32 v90, v90
	v_log_f32_e32 v106, v106
	v_log_f32_e32 v107, v107
	v_log_f32_e32 v104, v104
	v_log_f32_e32 v105, v105
	v_log_f32_e32 v110, v98
	v_exp_f32_e32 v94, v94
	v_mul_f32_e32 v95, v95, v117
	v_max_f32_e32 v95, 0xc2a00000, v95
	v_mul_f32_e32 v91, v91, v117
	v_mul_f32_e32 v95, 0xbfb8aa3b, v95
	v_add_f32_e32 v90, 1.0, v90
	v_max_f32_e32 v91, 0xc2a00000, v91
	v_cvt_pk_f16_f32 v98, v106, v107
	v_cvt_pk_f16_f32 v99, v104, v105
	v_cvt_pk_f16_f32 v100, v108, v101
	v_cvt_pk_f16_f32 v101, v109, v110
	v_exp_f32_e32 v95, v95
	v_add_f32_e32 v94, 1.0, v94
	v_rcp_f32_e32 v90, v90
	v_mul_f32_e32 v91, 0xbfb8aa3b, v91
	ds_bpermute_b32 v232, v250, v98
	ds_bpermute_b32 v233, v250, v99
	ds_bpermute_b32 v234, v250, v100
	ds_bpermute_b32 v235, v250, v101
	ds_bpermute_b32 v236, v250, v102
	v_exp_f32_e32 v91, v91
	v_fma_f32 v90, v171, v90, v132
	v_rcp_f32_e32 v100, v94
	v_or_b32_e32 v98, 32, v152
	v_ashrrev_i32_e32 v99, 31, v98
	v_add_f32_e32 v94, 1.0, v95
	v_rcp_f32_e32 v101, v94
	v_lshlrev_b64 v[94:95], 12, v[98:99]
	v_fma_f32 v98, v180, v100, v136
	v_log_f32_e32 v100, v90
	v_add_f32_e32 v90, 1.0, v91
	v_mul_f32_e32 v91, v92, v117
	v_mul_f32_e32 v96, v96, v117
	v_mul_f32_e32 v97, v97, v117
	v_max_f32_e32 v91, 0xc2a00000, v91
	v_mul_f32_e32 v92, v93, v117
	v_max_f32_e32 v96, 0xc2a00000, v96
	v_max_f32_e32 v97, 0xc2a00000, v97
	v_mul_f32_e32 v91, 0xbfb8aa3b, v91
	v_max_f32_e32 v92, 0xc2a00000, v92
	v_mul_f32_e32 v96, 0xbfb8aa3b, v96
	v_mul_f32_e32 v97, 0xbfb8aa3b, v97
	v_exp_f32_e32 v91, v91
	v_mul_f32_e32 v92, 0xbfb8aa3b, v92
	v_exp_f32_e32 v96, v96
	v_exp_f32_e32 v97, v97
	v_exp_f32_e32 v92, v92
	v_mul_f32_e32 v82, v82, v117
	v_rcp_f32_e32 v90, v90
	v_add_f32_e32 v91, 1.0, v91
	v_max_f32_e32 v82, 0xc2a00000, v82
	v_add_f32_e32 v96, 1.0, v96
	v_add_f32_e32 v97, 1.0, v97
	v_rcp_f32_e32 v91, v91
	v_add_f32_e32 v92, 1.0, v92
	v_mul_f32_e32 v82, 0xbfb8aa3b, v82
	v_rcp_f32_e32 v96, v96
	v_rcp_f32_e32 v97, v97
	v_rcp_f32_e32 v92, v92
	v_exp_f32_e32 v82, v82
	v_fma_f32 v90, v170, v90, v133
	v_log_f32_e32 v93, v90
	v_fma_f32 v90, v169, v91, v134
	v_mul_f32_e32 v83, v83, v117
	v_fma_f32 v99, v179, v101, v137
	v_fma_f32 v96, v178, v96, v138
	v_fma_f32 v97, v177, v97, v139
	v_log_f32_e32 v101, v90
	v_fma_f32 v90, v155, v92, v135
	v_add_f32_e32 v82, 1.0, v82
	v_max_f32_e32 v83, 0xc2a00000, v83
	v_log_f32_e32 v98, v98
	v_log_f32_e32 v99, v99
	v_log_f32_e32 v96, v96
	v_log_f32_e32 v97, v97
	v_log_f32_e32 v102, v90
	v_rcp_f32_e32 v82, v82
	v_mul_f32_e32 v83, 0xbfb8aa3b, v83
	v_exp_f32_e32 v83, v83
	v_lshl_add_u64 v[94:95], s[42:43], 0, v[94:95]
	v_cvt_pk_f16_f32 v90, v98, v99
	v_cvt_pk_f16_f32 v91, v96, v97
	v_cvt_pk_f16_f32 v92, v100, v93
	v_cvt_pk_f16_f32 v93, v101, v102
	v_lshl_add_u64 v[94:95], v[94:95], 0, v[114:115]
	v_fma_f32 v82, v123, v82, v124
	s_waitcnt lgkmcnt(10)
	v_subrev_u32_e32 v242, s82, v242
	global_store_dwordx4 v242, v[238:241], s[82:83]
	ds_bpermute_b32 v238, v250, v90
	ds_bpermute_b32 v239, v250, v91
	ds_bpermute_b32 v240, v250, v92
	ds_bpermute_b32 v241, v250, v93
	ds_bpermute_b32 v242, v250, v94
	v_mul_f32_e32 v86, v86, v117
	v_mul_f32_e32 v87, v87, v117
	v_log_f32_e32 v90, v82
	v_add_f32_e32 v82, 1.0, v83
	v_mul_f32_e32 v83, v84, v117
	v_max_f32_e32 v83, 0xc2a00000, v83
	v_mul_f32_e32 v84, v85, v117
	v_mul_f32_e32 v83, 0xbfb8aa3b, v83
	v_max_f32_e32 v84, 0xc2a00000, v84
	v_exp_f32_e32 v83, v83
	v_mul_f32_e32 v84, 0xbfb8aa3b, v84
	v_exp_f32_e32 v84, v84
	v_rcp_f32_e32 v82, v82
	v_add_f32_e32 v83, 1.0, v83
	v_rcp_f32_e32 v83, v83
	v_add_f32_e32 v84, 1.0, v84
	v_rcp_f32_e32 v84, v84
	v_mul_f32_e32 v88, v88, v117
	v_mul_f32_e32 v89, v89, v117
	v_max_f32_e32 v86, 0xc2a00000, v86
	v_max_f32_e32 v87, 0xc2a00000, v87
	v_max_f32_e32 v88, 0xc2a00000, v88
	v_max_f32_e32 v89, 0xc2a00000, v89
	v_fma_f32 v82, v120, v82, v125
	v_mul_f32_e32 v86, 0xbfb8aa3b, v86
	v_mul_f32_e32 v87, 0xbfb8aa3b, v87
	v_mul_f32_e32 v88, 0xbfb8aa3b, v88
	v_mul_f32_e32 v89, 0xbfb8aa3b, v89
	v_log_f32_e32 v91, v82
	v_fma_f32 v82, v118, v83, v126
	v_exp_f32_e32 v86, v86
	v_exp_f32_e32 v87, v87
	v_exp_f32_e32 v88, v88
	v_exp_f32_e32 v89, v89
	v_log_f32_e32 v92, v82
	v_fma_f32 v82, v119, v84, v127
	v_log_f32_e32 v93, v82
	ds_read2_b32 v[82:83], v176 offset0:48 offset1:128
	v_add_f32_e32 v86, 1.0, v86
	v_add_f32_e32 v87, 1.0, v87
	v_add_f32_e32 v88, 1.0, v88
	v_add_f32_e32 v89, 1.0, v89
	v_rcp_f32_e32 v86, v86
	v_rcp_f32_e32 v87, v87
	v_rcp_f32_e32 v88, v88
	v_rcp_f32_e32 v89, v89
	s_waitcnt lgkmcnt(0)
	v_mul_f32_e32 v74, v74, v82
	v_mul_f32_e32 v78, v78, v82
	v_max_f32_e32 v74, 0xc2a00000, v74
	v_max_f32_e32 v78, 0xc2a00000, v78
	v_mul_f32_e32 v74, 0xbfb8aa3b, v74
	v_fma_f32 v86, v153, v86, v128
	v_fma_f32 v87, v168, v87, v129
	v_fma_f32 v88, v121, v88, v130
	v_fma_f32 v89, v122, v89, v131
	v_mul_f32_e32 v78, 0xbfb8aa3b, v78
	v_exp_f32_e32 v74, v74
	v_log_f32_e32 v86, v86
	v_log_f32_e32 v87, v87
	v_log_f32_e32 v88, v88
	v_log_f32_e32 v89, v89
	v_exp_f32_e32 v78, v78
	v_mul_f32_e32 v79, v79, v82
	v_max_f32_e32 v79, 0xc2a00000, v79
	v_mul_f32_e32 v75, v75, v82
	v_mul_f32_e32 v79, 0xbfb8aa3b, v79
	v_add_f32_e32 v74, 1.0, v74
	v_max_f32_e32 v75, 0xc2a00000, v75
	v_cvt_pk_f16_f32 v84, v86, v87
	v_cvt_pk_f16_f32 v85, v88, v89
	v_cvt_pk_f16_f32 v86, v90, v91
	v_cvt_pk_f16_f32 v87, v92, v93
	v_exp_f32_e32 v79, v79
	v_add_f32_e32 v78, 1.0, v78
	v_rcp_f32_e32 v74, v74
	v_mul_f32_e32 v75, 0xbfb8aa3b, v75
	s_waitcnt lgkmcnt(11)
	v_subrev_u32_e32 v248, s82, v248
	global_store_dwordx4 v248, v[244:247], s[82:83]
	ds_bpermute_b32 v244, v250, v84
	ds_bpermute_b32 v245, v250, v85
	ds_bpermute_b32 v246, v250, v86
	ds_bpermute_b32 v247, v250, v87
	ds_bpermute_b32 v248, v250, v94
	v_exp_f32_e32 v75, v75
	v_mul_f32_e32 v80, v80, v82
	v_rcp_f32_e32 v86, v78
	v_or_b32_e32 v84, 48, v152
	v_mul_f32_e32 v81, v81, v82
	v_ashrrev_i32_e32 v85, 31, v84
	v_add_f32_e32 v78, 1.0, v79
	v_max_f32_e32 v80, 0xc2a00000, v80
	v_max_f32_e32 v81, 0xc2a00000, v81
	v_fma_f32 v74, v171, v74, v132
	v_rcp_f32_e32 v87, v78
	v_lshlrev_b64 v[78:79], 12, v[84:85]
	v_fma_f32 v84, v180, v86, v136
	v_mul_f32_e32 v80, 0xbfb8aa3b, v80
	v_mul_f32_e32 v81, 0xbfb8aa3b, v81
	v_log_f32_e32 v86, v74
	v_add_f32_e32 v74, 1.0, v75
	v_mul_f32_e32 v75, v76, v82
	v_exp_f32_e32 v80, v80
	v_exp_f32_e32 v81, v81
	v_max_f32_e32 v75, 0xc2a00000, v75
	v_mul_f32_e32 v76, v77, v82
	v_mul_f32_e32 v75, 0xbfb8aa3b, v75
	v_max_f32_e32 v76, 0xc2a00000, v76
	v_exp_f32_e32 v75, v75
	v_mul_f32_e32 v76, 0xbfb8aa3b, v76
	v_exp_f32_e32 v76, v76
	v_add_f32_e32 v80, 1.0, v80
	v_add_f32_e32 v81, 1.0, v81
	v_rcp_f32_e32 v80, v80
	v_rcp_f32_e32 v81, v81
	v_mul_f32_e32 v66, v66, v82
	v_rcp_f32_e32 v74, v74
	v_add_f32_e32 v75, 1.0, v75
	v_max_f32_e32 v66, 0xc2a00000, v66
	v_rcp_f32_e32 v75, v75
	v_add_f32_e32 v76, 1.0, v76
	v_mul_f32_e32 v66, 0xbfb8aa3b, v66
	v_rcp_f32_e32 v76, v76
	v_exp_f32_e32 v66, v66
	v_fma_f32 v80, v178, v80, v138
	v_fma_f32 v81, v177, v81, v139
	v_log_f32_e32 v80, v80
	v_log_f32_e32 v81, v81
	v_fma_f32 v74, v170, v74, v133
	v_log_f32_e32 v77, v74
	v_fma_f32 v74, v169, v75, v134
	v_mul_f32_e32 v70, v70, v82
	v_mul_f32_e32 v67, v67, v82
	v_fma_f32 v85, v179, v87, v137
	v_log_f32_e32 v87, v74
	v_fma_f32 v74, v155, v76, v135
	v_max_f32_e32 v70, 0xc2a00000, v70
	v_add_f32_e32 v66, 1.0, v66
	v_max_f32_e32 v67, 0xc2a00000, v67
	v_log_f32_e32 v84, v84
	v_log_f32_e32 v85, v85
	v_log_f32_e32 v88, v74
	v_mul_f32_e32 v70, 0xbfb8aa3b, v70
	v_rcp_f32_e32 v66, v66
	v_mul_f32_e32 v67, 0xbfb8aa3b, v67
	v_cvt_pk_f16_f32 v75, v80, v81
	v_exp_f32_e32 v80, v70
	v_mul_f32_e32 v70, v71, v82
	v_exp_f32_e32 v67, v67
	v_max_f32_e32 v70, 0xc2a00000, v70
	v_lshl_add_u64 v[78:79], s[42:43], 0, v[78:79]
	v_mul_f32_e32 v70, 0xbfb8aa3b, v70
	v_cvt_pk_f16_f32 v74, v84, v85
	v_cvt_pk_f16_f32 v76, v86, v77
	v_cvt_pk_f16_f32 v77, v87, v88
	v_exp_f32_e32 v81, v70
	v_lshl_add_u64 v[70:71], v[78:79], 0, v[114:115]
	v_fma_f32 v66, v123, v66, v124
	s_waitcnt lgkmcnt(11)
	v_subrev_u32_e32 v236, s82, v236
	global_store_dwordx4 v236, v[232:235], s[82:83] offset:64
	ds_bpermute_b32 v232, v250, v74
	ds_bpermute_b32 v233, v250, v75
	ds_bpermute_b32 v234, v250, v76
	ds_bpermute_b32 v235, v250, v77
	ds_bpermute_b32 v236, v250, v70
	v_mul_f32_e32 v72, v72, v82
	v_mul_f32_e32 v73, v73, v82
	v_log_f32_e32 v76, v66
	v_add_f32_e32 v66, 1.0, v67
	v_mul_f32_e32 v67, v68, v82
	v_max_f32_e32 v67, 0xc2a00000, v67
	v_mul_f32_e32 v68, v69, v82
	v_max_f32_e32 v72, 0xc2a00000, v72
	v_max_f32_e32 v73, 0xc2a00000, v73
	v_mul_f32_e32 v67, 0xbfb8aa3b, v67
	v_max_f32_e32 v68, 0xc2a00000, v68
	v_mul_f32_e32 v72, 0xbfb8aa3b, v72
	v_mul_f32_e32 v73, 0xbfb8aa3b, v73
	v_exp_f32_e32 v67, v67
	v_mul_f32_e32 v68, 0xbfb8aa3b, v68
	v_exp_f32_e32 v72, v72
	v_exp_f32_e32 v73, v73
	v_exp_f32_e32 v68, v68
	v_mul_f32_e32 v58, v58, v83
	v_rcp_f32_e32 v66, v66
	v_add_f32_e32 v67, 1.0, v67
	v_max_f32_e32 v58, 0xc2a00000, v58
	v_add_f32_e32 v78, 1.0, v80
	v_add_f32_e32 v79, 1.0, v81
	v_add_f32_e32 v72, 1.0, v72
	v_add_f32_e32 v73, 1.0, v73
	v_rcp_f32_e32 v67, v67
	v_add_f32_e32 v68, 1.0, v68
	v_mul_f32_e32 v58, 0xbfb8aa3b, v58
	v_rcp_f32_e32 v78, v78
	v_rcp_f32_e32 v79, v79
	v_rcp_f32_e32 v72, v72
	v_rcp_f32_e32 v73, v73
	v_rcp_f32_e32 v68, v68
	v_exp_f32_e32 v58, v58
	v_fma_f32 v66, v120, v66, v125
	v_log_f32_e32 v69, v66
	v_fma_f32 v66, v118, v67, v126
	v_mul_f32_e32 v59, v59, v83
	v_fma_f32 v74, v153, v78, v128
	v_fma_f32 v75, v168, v79, v129
	v_fma_f32 v72, v121, v72, v130
	v_fma_f32 v73, v122, v73, v131
	v_log_f32_e32 v77, v66
	v_fma_f32 v66, v119, v68, v127
	v_add_f32_e32 v58, 1.0, v58
	v_max_f32_e32 v59, 0xc2a00000, v59
	v_log_f32_e32 v74, v74
	v_log_f32_e32 v75, v75
	v_log_f32_e32 v72, v72
	v_log_f32_e32 v73, v73
	v_log_f32_e32 v78, v66
	v_rcp_f32_e32 v58, v58
	v_mul_f32_e32 v59, 0xbfb8aa3b, v59
	v_exp_f32_e32 v59, v59
	v_mul_f32_e32 v64, v64, v83
	v_mul_f32_e32 v65, v65, v83
	v_max_f32_e32 v64, 0xc2a00000, v64
	v_max_f32_e32 v65, 0xc2a00000, v65
	v_cvt_pk_f16_f32 v66, v74, v75
	v_cvt_pk_f16_f32 v67, v72, v73
	v_cvt_pk_f16_f32 v68, v76, v69
	v_mul_f32_e32 v62, v62, v83
	v_mul_f32_e32 v63, v63, v83
	v_cvt_pk_f16_f32 v69, v77, v78
	v_mul_f32_e32 v64, 0xbfb8aa3b, v64
	v_mul_f32_e32 v65, 0xbfb8aa3b, v65
	v_fma_f32 v58, v171, v58, v132
	v_max_f32_e32 v62, 0xc2a00000, v62
	v_max_f32_e32 v63, 0xc2a00000, v63
	s_waitcnt lgkmcnt(11)
	v_subrev_u32_e32 v242, s82, v242
	global_store_dwordx4 v242, v[238:241], s[82:83]
	ds_bpermute_b32 v238, v250, v66
	ds_bpermute_b32 v239, v250, v67
	ds_bpermute_b32 v240, v250, v68
	ds_bpermute_b32 v241, v250, v69
	ds_bpermute_b32 v242, v250, v70
	v_exp_f32_e32 v64, v64
	v_exp_f32_e32 v65, v65
	v_log_f32_e32 v66, v58
	v_add_f32_e32 v58, 1.0, v59
	v_mul_f32_e32 v59, v60, v83
	v_mul_f32_e32 v62, 0xbfb8aa3b, v62
	v_mul_f32_e32 v63, 0xbfb8aa3b, v63
	v_max_f32_e32 v59, 0xc2a00000, v59
	v_mul_f32_e32 v60, v61, v83
	v_exp_f32_e32 v62, v62
	v_exp_f32_e32 v63, v63
	v_mul_f32_e32 v59, 0xbfb8aa3b, v59
	v_max_f32_e32 v60, 0xc2a00000, v60
	v_exp_f32_e32 v59, v59
	v_mul_f32_e32 v60, 0xbfb8aa3b, v60
	v_add_f32_e32 v64, 1.0, v64
	v_add_f32_e32 v65, 1.0, v65
	v_exp_f32_e32 v60, v60
	v_rcp_f32_e32 v64, v64
	v_rcp_f32_e32 v65, v65
	v_add_f32_e32 v62, 1.0, v62
	v_add_f32_e32 v63, 1.0, v63
	v_mul_f32_e32 v50, v50, v83
	v_rcp_f32_e32 v62, v62
	v_rcp_f32_e32 v63, v63
	v_rcp_f32_e32 v58, v58
	v_add_f32_e32 v59, 1.0, v59
	v_max_f32_e32 v50, 0xc2a00000, v50
	v_rcp_f32_e32 v59, v59
	v_add_f32_e32 v60, 1.0, v60
	v_mul_f32_e32 v50, 0xbfb8aa3b, v50
	v_fma_f32 v64, v178, v64, v138
	v_fma_f32 v65, v177, v65, v139
	v_rcp_f32_e32 v60, v60
	v_exp_f32_e32 v50, v50
	v_log_f32_e32 v64, v64
	v_log_f32_e32 v65, v65
	v_fma_f32 v62, v180, v62, v136
	v_fma_f32 v63, v179, v63, v137
	v_fma_f32 v58, v170, v58, v133
	v_mul_f32_e32 v54, v54, v83
	v_log_f32_e32 v62, v62
	v_log_f32_e32 v63, v63
	v_log_f32_e32 v61, v58
	v_fma_f32 v58, v169, v59, v134
	v_max_f32_e32 v54, 0xc2a00000, v54
	v_mul_f32_e32 v51, v51, v83
	v_log_f32_e32 v67, v58
	v_fma_f32 v58, v155, v60, v135
	v_mul_f32_e32 v54, 0xbfb8aa3b, v54
	v_add_f32_e32 v50, 1.0, v50
	v_max_f32_e32 v51, 0xc2a00000, v51
	v_log_f32_e32 v68, v58
	v_cvt_pk_f16_f32 v59, v64, v65
	v_exp_f32_e32 v64, v54
	v_mul_f32_e32 v54, v55, v83
	v_rcp_f32_e32 v50, v50
	v_mul_f32_e32 v51, 0xbfb8aa3b, v51
	v_max_f32_e32 v54, 0xc2a00000, v54
	v_exp_f32_e32 v51, v51
	v_cvt_pk_f16_f32 v58, v62, v63
	v_lshl_add_u64 v[62:63], v[166:167], 0, s[14:15]
	v_mul_f32_e32 v54, 0xbfb8aa3b, v54
	s_mov_b32 s14, 0x80000
	v_exp_f32_e32 v65, v54
	v_add_co_u32_e32 v54, vcc, s14, v166
	v_cvt_pk_f16_f32 v60, v66, v61
	v_cvt_pk_f16_f32 v61, v67, v68
	v_addc_co_u32_e32 v55, vcc, 0, v167, vcc
	v_fma_f32 v50, v123, v50, v124
	s_waitcnt lgkmcnt(10)
	v_subrev_u32_e32 v248, s82, v248
	global_store_dwordx4 v248, v[244:247], s[82:83] offset:64
	ds_bpermute_b32 v244, v250, v58
	ds_bpermute_b32 v245, v250, v59
	ds_bpermute_b32 v246, v250, v60
	ds_bpermute_b32 v247, v250, v61
	ds_bpermute_b32 v248, v250, v54
	v_mul_f32_e32 v56, v56, v83
	v_mul_f32_e32 v57, v57, v83
	v_log_f32_e32 v58, v50
	v_add_f32_e32 v50, 1.0, v51
	v_mul_f32_e32 v51, v52, v83
	v_max_f32_e32 v51, 0xc2a00000, v51
	v_mul_f32_e32 v51, 0xbfb8aa3b, v51
	v_exp_f32_e32 v51, v51
	v_rcp_f32_e32 v50, v50
	v_mul_f32_e32 v52, v53, v83
	v_max_f32_e32 v56, 0xc2a00000, v56
	v_add_f32_e32 v51, 1.0, v51
	v_rcp_f32_e32 v51, v51
	v_fma_f32 v50, v120, v50, v125
	v_log_f32_e32 v59, v50
	v_max_f32_e32 v57, 0xc2a00000, v57
	v_fma_f32 v50, v118, v51, v126
	v_log_f32_e32 v60, v50
	ds_read2_b32 v[50:51], v176 offset0:144 offset1:160
	v_max_f32_e32 v52, 0xc2a00000, v52
	v_mul_f32_e32 v56, 0xbfb8aa3b, v56
	v_mul_f32_e32 v57, 0xbfb8aa3b, v57
	v_mul_f32_e32 v52, 0xbfb8aa3b, v52
	v_exp_f32_e32 v56, v56
	v_exp_f32_e32 v57, v57
	v_exp_f32_e32 v52, v52
	s_waitcnt lgkmcnt(0)
	v_mul_f32_e32 v42, v42, v50
	v_max_f32_e32 v42, 0xc2a00000, v42
	v_add_f32_e32 v64, 1.0, v64
	v_add_f32_e32 v65, 1.0, v65
	v_add_f32_e32 v56, 1.0, v56
	v_add_f32_e32 v57, 1.0, v57
	v_add_f32_e32 v52, 1.0, v52
	v_mul_f32_e32 v42, 0xbfb8aa3b, v42
	v_rcp_f32_e32 v64, v64
	v_rcp_f32_e32 v65, v65
	v_rcp_f32_e32 v56, v56
	v_rcp_f32_e32 v57, v57
	v_rcp_f32_e32 v52, v52
	v_exp_f32_e32 v42, v42
	v_mul_f32_e32 v43, v43, v50
	v_fma_f32 v54, v153, v64, v128
	v_fma_f32 v55, v168, v65, v129
	v_fma_f32 v56, v121, v56, v130
	v_fma_f32 v57, v122, v57, v131
	v_fma_f32 v52, v119, v52, v127
	v_add_f32_e32 v42, 1.0, v42
	v_max_f32_e32 v43, 0xc2a00000, v43
	v_log_f32_e32 v54, v54
	v_log_f32_e32 v55, v55
	v_log_f32_e32 v56, v56
	v_log_f32_e32 v57, v57
	v_log_f32_e32 v61, v52
	v_rcp_f32_e32 v42, v42
	v_mul_f32_e32 v43, 0xbfb8aa3b, v43
	v_exp_f32_e32 v43, v43
	v_mul_f32_e32 v48, v48, v50
	v_mul_f32_e32 v49, v49, v50
	v_max_f32_e32 v48, 0xc2a00000, v48
	v_max_f32_e32 v49, 0xc2a00000, v49
	v_cvt_pk_f16_f32 v52, v54, v55
	v_cvt_pk_f16_f32 v53, v56, v57
	v_cvt_pk_f16_f32 v54, v58, v59
	v_mul_f32_e32 v46, v46, v50
	v_mul_f32_e32 v47, v47, v50
	v_cvt_pk_f16_f32 v55, v60, v61
	v_mul_f32_e32 v48, 0xbfb8aa3b, v48
	v_mul_f32_e32 v49, 0xbfb8aa3b, v49
	v_fma_f32 v42, v171, v42, v132
	v_max_f32_e32 v46, 0xc2a00000, v46
	v_max_f32_e32 v47, 0xc2a00000, v47
	s_waitcnt lgkmcnt(11)
	v_subrev_u32_e32 v236, s82, v236
	global_store_dwordx4 v236, v[232:235], s[82:83]
	ds_bpermute_b32 v232, v250, v52
	ds_bpermute_b32 v233, v250, v53
	ds_bpermute_b32 v234, v250, v54
	ds_bpermute_b32 v235, v250, v55
	ds_bpermute_b32 v236, v250, v62
	v_exp_f32_e32 v48, v48
	v_exp_f32_e32 v49, v49
	v_log_f32_e32 v52, v42
	v_add_f32_e32 v42, 1.0, v43
	v_mul_f32_e32 v43, v44, v50
	v_mul_f32_e32 v46, 0xbfb8aa3b, v46
	v_mul_f32_e32 v47, 0xbfb8aa3b, v47
	v_max_f32_e32 v43, 0xc2a00000, v43
	v_mul_f32_e32 v44, v45, v50
	v_exp_f32_e32 v46, v46
	v_exp_f32_e32 v47, v47
	v_mul_f32_e32 v43, 0xbfb8aa3b, v43
	v_max_f32_e32 v44, 0xc2a00000, v44
	v_exp_f32_e32 v43, v43
	v_mul_f32_e32 v44, 0xbfb8aa3b, v44
	v_add_f32_e32 v48, 1.0, v48
	v_add_f32_e32 v49, 1.0, v49
	v_exp_f32_e32 v44, v44
	v_rcp_f32_e32 v48, v48
	v_rcp_f32_e32 v49, v49
	v_add_f32_e32 v46, 1.0, v46
	v_add_f32_e32 v47, 1.0, v47
	v_mul_f32_e32 v34, v34, v50
	v_rcp_f32_e32 v46, v46
	v_rcp_f32_e32 v47, v47
	v_rcp_f32_e32 v42, v42
	v_add_f32_e32 v43, 1.0, v43
	v_max_f32_e32 v34, 0xc2a00000, v34
	v_rcp_f32_e32 v43, v43
	v_add_f32_e32 v44, 1.0, v44
	v_mul_f32_e32 v34, 0xbfb8aa3b, v34
	v_fma_f32 v48, v178, v48, v138
	v_fma_f32 v49, v177, v49, v139
	v_rcp_f32_e32 v44, v44
	v_exp_f32_e32 v34, v34
	v_log_f32_e32 v48, v48
	v_log_f32_e32 v49, v49
	v_fma_f32 v46, v180, v46, v136
	v_fma_f32 v47, v179, v47, v137
	v_fma_f32 v42, v170, v42, v133
	v_mul_f32_e32 v38, v38, v50
	v_log_f32_e32 v46, v46
	v_log_f32_e32 v47, v47
	v_log_f32_e32 v45, v42
	v_fma_f32 v42, v169, v43, v134
	v_max_f32_e32 v38, 0xc2a00000, v38
	v_mul_f32_e32 v35, v35, v50
	v_log_f32_e32 v53, v42
	v_fma_f32 v42, v155, v44, v135
	v_mul_f32_e32 v38, 0xbfb8aa3b, v38
	v_add_f32_e32 v34, 1.0, v34
	v_max_f32_e32 v35, 0xc2a00000, v35
	v_log_f32_e32 v54, v42
	v_cvt_pk_f16_f32 v43, v48, v49
	v_exp_f32_e32 v48, v38
	v_mul_f32_e32 v38, v39, v50
	v_rcp_f32_e32 v34, v34
	v_mul_f32_e32 v35, 0xbfb8aa3b, v35
	s_mov_b64 s[14:15], 0x90000
	v_max_f32_e32 v38, 0xc2a00000, v38
	v_exp_f32_e32 v35, v35
	v_cvt_pk_f16_f32 v42, v46, v47
	v_lshl_add_u64 v[46:47], v[166:167], 0, s[14:15]
	v_mul_f32_e32 v38, 0xbfb8aa3b, v38
	s_mov_b32 s14, 0x90000
	v_exp_f32_e32 v49, v38
	v_add_co_u32_e32 v38, vcc, s14, v166
	v_cvt_pk_f16_f32 v44, v52, v45
	v_cvt_pk_f16_f32 v45, v53, v54
	v_addc_co_u32_e32 v39, vcc, 0, v167, vcc
	v_fma_f32 v34, v123, v34, v124
	s_waitcnt lgkmcnt(11)
	v_subrev_u32_e32 v242, s82, v242
	global_store_dwordx4 v242, v[238:241], s[82:83] offset:64
	ds_bpermute_b32 v238, v250, v42
	ds_bpermute_b32 v239, v250, v43
	ds_bpermute_b32 v240, v250, v44
	ds_bpermute_b32 v241, v250, v45
	ds_bpermute_b32 v242, v250, v38
	v_mul_f32_e32 v40, v40, v50
	v_mul_f32_e32 v41, v41, v50
	v_log_f32_e32 v42, v34
	v_add_f32_e32 v34, 1.0, v35
	v_mul_f32_e32 v35, v36, v50
	v_max_f32_e32 v35, 0xc2a00000, v35
	v_mul_f32_e32 v36, v37, v50
	v_max_f32_e32 v40, 0xc2a00000, v40
	v_max_f32_e32 v41, 0xc2a00000, v41
	v_mul_f32_e32 v35, 0xbfb8aa3b, v35
	v_max_f32_e32 v36, 0xc2a00000, v36
	v_mul_f32_e32 v40, 0xbfb8aa3b, v40
	v_mul_f32_e32 v41, 0xbfb8aa3b, v41
	v_exp_f32_e32 v35, v35
	v_mul_f32_e32 v36, 0xbfb8aa3b, v36
	v_exp_f32_e32 v40, v40
	v_exp_f32_e32 v41, v41
	v_exp_f32_e32 v36, v36
	v_mul_f32_e32 v26, v26, v51
	v_rcp_f32_e32 v34, v34
	v_add_f32_e32 v35, 1.0, v35
	v_max_f32_e32 v26, 0xc2a00000, v26
	v_add_f32_e32 v48, 1.0, v48
	v_add_f32_e32 v49, 1.0, v49
	v_add_f32_e32 v40, 1.0, v40
	v_add_f32_e32 v41, 1.0, v41
	v_rcp_f32_e32 v35, v35
	v_add_f32_e32 v36, 1.0, v36
	v_mul_f32_e32 v26, 0xbfb8aa3b, v26
	v_rcp_f32_e32 v48, v48
	v_rcp_f32_e32 v49, v49
	v_rcp_f32_e32 v40, v40
	v_rcp_f32_e32 v41, v41
	v_rcp_f32_e32 v36, v36
	v_exp_f32_e32 v26, v26
	v_fma_f32 v34, v120, v34, v125
	v_log_f32_e32 v37, v34
	v_fma_f32 v34, v118, v35, v126
	v_mul_f32_e32 v27, v27, v51
	v_fma_f32 v38, v153, v48, v128
	v_fma_f32 v39, v168, v49, v129
	v_fma_f32 v40, v121, v40, v130
	v_fma_f32 v41, v122, v41, v131
	v_log_f32_e32 v43, v34
	v_fma_f32 v34, v119, v36, v127
	v_add_f32_e32 v26, 1.0, v26
	v_max_f32_e32 v27, 0xc2a00000, v27
	v_log_f32_e32 v38, v38
	v_log_f32_e32 v39, v39
	v_log_f32_e32 v40, v40
	v_log_f32_e32 v41, v41
	v_log_f32_e32 v44, v34
	v_rcp_f32_e32 v26, v26
	v_mul_f32_e32 v27, 0xbfb8aa3b, v27
	v_exp_f32_e32 v27, v27
	v_mul_f32_e32 v32, v32, v51
	v_mul_f32_e32 v33, v33, v51
	v_max_f32_e32 v32, 0xc2a00000, v32
	v_max_f32_e32 v33, 0xc2a00000, v33
	v_cvt_pk_f16_f32 v34, v38, v39
	v_cvt_pk_f16_f32 v35, v40, v41
	v_cvt_pk_f16_f32 v36, v42, v37
	v_mul_f32_e32 v30, v30, v51
	v_mul_f32_e32 v31, v31, v51
	v_cvt_pk_f16_f32 v37, v43, v44
	v_mul_f32_e32 v32, 0xbfb8aa3b, v32
	v_mul_f32_e32 v33, 0xbfb8aa3b, v33
	v_fma_f32 v26, v171, v26, v132
	v_max_f32_e32 v30, 0xc2a00000, v30
	v_max_f32_e32 v31, 0xc2a00000, v31
	s_waitcnt lgkmcnt(11)
	v_subrev_u32_e32 v248, s82, v248
	global_store_dwordx4 v248, v[244:247], s[82:83]
	ds_bpermute_b32 v244, v250, v34
	ds_bpermute_b32 v245, v250, v35
	ds_bpermute_b32 v246, v250, v36
	ds_bpermute_b32 v247, v250, v37
	ds_bpermute_b32 v248, v250, v46
	v_exp_f32_e32 v32, v32
	v_exp_f32_e32 v33, v33
	v_log_f32_e32 v34, v26
	v_add_f32_e32 v26, 1.0, v27
	v_mul_f32_e32 v27, v28, v51
	v_mul_f32_e32 v30, 0xbfb8aa3b, v30
	v_mul_f32_e32 v31, 0xbfb8aa3b, v31
	v_max_f32_e32 v27, 0xc2a00000, v27
	v_mul_f32_e32 v28, v29, v51
	v_exp_f32_e32 v30, v30
	v_exp_f32_e32 v31, v31
	v_mul_f32_e32 v27, 0xbfb8aa3b, v27
	v_max_f32_e32 v28, 0xc2a00000, v28
	v_exp_f32_e32 v27, v27
	v_mul_f32_e32 v28, 0xbfb8aa3b, v28
	v_add_f32_e32 v32, 1.0, v32
	v_add_f32_e32 v33, 1.0, v33
	v_exp_f32_e32 v28, v28
	v_rcp_f32_e32 v32, v32
	v_rcp_f32_e32 v33, v33
	v_add_f32_e32 v30, 1.0, v30
	v_add_f32_e32 v31, 1.0, v31
	v_mul_f32_e32 v18, v18, v51
	v_rcp_f32_e32 v30, v30
	v_rcp_f32_e32 v31, v31
	v_rcp_f32_e32 v26, v26
	v_add_f32_e32 v27, 1.0, v27
	v_max_f32_e32 v18, 0xc2a00000, v18
	v_rcp_f32_e32 v27, v27
	v_add_f32_e32 v28, 1.0, v28
	v_mul_f32_e32 v18, 0xbfb8aa3b, v18
	v_fma_f32 v32, v178, v32, v138
	v_fma_f32 v33, v177, v33, v139
	v_rcp_f32_e32 v28, v28
	v_exp_f32_e32 v18, v18
	v_log_f32_e32 v32, v32
	v_log_f32_e32 v33, v33
	v_fma_f32 v30, v180, v30, v136
	v_fma_f32 v31, v179, v31, v137
	v_fma_f32 v26, v170, v26, v133
	v_mul_f32_e32 v22, v22, v51
	v_log_f32_e32 v30, v30
	v_log_f32_e32 v31, v31
	v_log_f32_e32 v29, v26
	v_fma_f32 v26, v169, v27, v134
	v_max_f32_e32 v22, 0xc2a00000, v22
	v_mul_f32_e32 v19, v19, v51
	v_log_f32_e32 v35, v26
	v_fma_f32 v26, v155, v28, v135
	v_mul_f32_e32 v22, 0xbfb8aa3b, v22
	v_add_f32_e32 v18, 1.0, v18
	v_max_f32_e32 v19, 0xc2a00000, v19
	v_log_f32_e32 v36, v26
	v_cvt_pk_f16_f32 v27, v32, v33
	v_exp_f32_e32 v32, v22
	v_mul_f32_e32 v22, v23, v51
	v_rcp_f32_e32 v18, v18
	v_mul_f32_e32 v19, 0xbfb8aa3b, v19
	s_mov_b64 s[14:15], 0xa0000
	v_max_f32_e32 v22, 0xc2a00000, v22
	v_exp_f32_e32 v19, v19
	v_cvt_pk_f16_f32 v26, v30, v31
	v_lshl_add_u64 v[30:31], v[166:167], 0, s[14:15]
	v_mul_f32_e32 v22, 0xbfb8aa3b, v22
	s_mov_b32 s14, 0xa0000
	v_exp_f32_e32 v33, v22
	v_add_co_u32_e32 v22, vcc, s14, v166
	v_cvt_pk_f16_f32 v28, v34, v29
	v_cvt_pk_f16_f32 v29, v35, v36
	v_addc_co_u32_e32 v23, vcc, 0, v167, vcc
	v_fma_f32 v18, v123, v18, v124
	s_waitcnt lgkmcnt(10)
	v_subrev_u32_e32 v236, s82, v236
	global_store_dwordx4 v236, v[232:235], s[82:83] offset:64
	ds_bpermute_b32 v232, v250, v26
	ds_bpermute_b32 v233, v250, v27
	ds_bpermute_b32 v234, v250, v28
	ds_bpermute_b32 v235, v250, v29
	ds_bpermute_b32 v236, v250, v22
	v_mul_f32_e32 v24, v24, v51
	v_mul_f32_e32 v25, v25, v51
	v_log_f32_e32 v26, v18
	v_add_f32_e32 v18, 1.0, v19
	v_mul_f32_e32 v19, v20, v51
	v_max_f32_e32 v19, 0xc2a00000, v19
	v_mul_f32_e32 v20, v21, v51
	ds_read_b32 v28, v176 offset:704
	v_max_f32_e32 v24, 0xc2a00000, v24
	v_max_f32_e32 v25, 0xc2a00000, v25
	v_mul_f32_e32 v19, 0xbfb8aa3b, v19
	v_max_f32_e32 v20, 0xc2a00000, v20
	v_mul_f32_e32 v24, 0xbfb8aa3b, v24
	v_mul_f32_e32 v25, 0xbfb8aa3b, v25
	v_exp_f32_e32 v19, v19
	v_mul_f32_e32 v20, 0xbfb8aa3b, v20
	v_exp_f32_e32 v24, v24
	v_exp_f32_e32 v25, v25
	v_exp_f32_e32 v20, v20
	s_waitcnt lgkmcnt(0)
	v_mul_f32_e32 v10, v10, v28
	v_rcp_f32_e32 v18, v18
	v_add_f32_e32 v19, 1.0, v19
	v_max_f32_e32 v10, 0xc2a00000, v10
	v_add_f32_e32 v32, 1.0, v32
	v_add_f32_e32 v33, 1.0, v33
	v_add_f32_e32 v24, 1.0, v24
	v_add_f32_e32 v25, 1.0, v25
	v_rcp_f32_e32 v19, v19
	v_add_f32_e32 v20, 1.0, v20
	v_mul_f32_e32 v10, 0xbfb8aa3b, v10
	v_rcp_f32_e32 v32, v32
	v_rcp_f32_e32 v33, v33
	v_rcp_f32_e32 v24, v24
	v_rcp_f32_e32 v25, v25
	v_rcp_f32_e32 v20, v20
	v_exp_f32_e32 v10, v10
	v_fma_f32 v18, v120, v18, v125
	v_log_f32_e32 v21, v18
	v_fma_f32 v18, v118, v19, v126
	v_mul_f32_e32 v11, v11, v28
	v_fma_f32 v22, v153, v32, v128
	v_fma_f32 v23, v168, v33, v129
	v_fma_f32 v24, v121, v24, v130
	v_fma_f32 v25, v122, v25, v131
	v_log_f32_e32 v27, v18
	v_fma_f32 v18, v119, v20, v127
	v_add_f32_e32 v10, 1.0, v10
	v_max_f32_e32 v11, 0xc2a00000, v11
	v_log_f32_e32 v22, v22
	v_log_f32_e32 v23, v23
	v_log_f32_e32 v24, v24
	v_log_f32_e32 v25, v25
	v_log_f32_e32 v29, v18
	v_rcp_f32_e32 v10, v10
	v_mul_f32_e32 v11, 0xbfb8aa3b, v11
	v_mul_f32_e32 v14, v14, v28
	v_mul_f32_e32 v15, v15, v28
	v_exp_f32_e32 v11, v11
	v_max_f32_e32 v14, 0xc2a00000, v14
	v_max_f32_e32 v15, 0xc2a00000, v15
	v_mul_f32_e32 v14, 0xbfb8aa3b, v14
	v_mul_f32_e32 v15, 0xbfb8aa3b, v15
	v_cvt_pk_f16_f32 v18, v22, v23
	v_cvt_pk_f16_f32 v19, v24, v25
	v_cvt_pk_f16_f32 v20, v26, v21
	v_exp_f32_e32 v14, v14
	v_exp_f32_e32 v15, v15
	v_cvt_pk_f16_f32 v21, v27, v29
	v_fma_f32 v10, v171, v10, v132
	s_waitcnt lgkmcnt(11)
	v_subrev_u32_e32 v242, s82, v242
	global_store_dwordx4 v242, v[238:241], s[82:83]
	ds_bpermute_b32 v238, v250, v18
	ds_bpermute_b32 v239, v250, v19
	ds_bpermute_b32 v240, v250, v20
	ds_bpermute_b32 v241, v250, v21
	ds_bpermute_b32 v242, v250, v30
	v_add_f32_e32 v14, 1.0, v14
	v_add_f32_e32 v15, 1.0, v15
	v_log_f32_e32 v18, v10
	v_add_f32_e32 v10, 1.0, v11
	v_mul_f32_e32 v11, v12, v28
	v_max_f32_e32 v11, 0xc2a00000, v11
	v_mul_f32_e32 v11, 0xbfb8aa3b, v11
	v_exp_f32_e32 v11, v11
	v_rcp_f32_e32 v14, v14
	v_rcp_f32_e32 v15, v15
	v_mul_f32_e32 v16, v16, v28
	v_mul_f32_e32 v17, v17, v28
	v_rcp_f32_e32 v10, v10
	v_mul_f32_e32 v12, v13, v28
	v_add_f32_e32 v11, 1.0, v11
	v_fma_f32 v14, v180, v14, v136
	v_fma_f32 v15, v179, v15, v137
	v_max_f32_e32 v16, 0xc2a00000, v16
	v_max_f32_e32 v17, 0xc2a00000, v17
	v_max_f32_e32 v12, 0xc2a00000, v12
	v_rcp_f32_e32 v11, v11
	v_log_f32_e32 v14, v14
	v_mul_f32_e32 v16, 0xbfb8aa3b, v16
	v_mul_f32_e32 v17, 0xbfb8aa3b, v17
	v_log_f32_e32 v15, v15
	v_mul_f32_e32 v12, 0xbfb8aa3b, v12
	v_exp_f32_e32 v16, v16
	v_exp_f32_e32 v17, v17
	v_exp_f32_e32 v12, v12
	v_mul_f32_e32 v6, v6, v28
	v_fma_f32 v10, v170, v10, v133
	v_max_f32_e32 v6, 0xc2a00000, v6
	v_log_f32_e32 v13, v10
	v_fma_f32 v10, v169, v11, v134
	v_mul_f32_e32 v6, 0xbfb8aa3b, v6
	v_log_f32_e32 v19, v10
	v_cvt_pk_f16_f32 v10, v14, v15
	v_exp_f32_e32 v14, v6
	v_mul_f32_e32 v6, v7, v28
	v_mul_f32_e32 v8, v8, v28
	v_mul_f32_e32 v9, v9, v28
	v_mul_f32_e32 v2, v2, v28
	v_mul_f32_e32 v3, v3, v28
	v_mul_f32_e32 v4, v4, v28
	v_mul_f32_e32 v5, v5, v28
	v_add_f32_e32 v16, 1.0, v16
	v_add_f32_e32 v17, 1.0, v17
	v_add_f32_e32 v12, 1.0, v12
	v_max_f32_e32 v6, 0xc2a00000, v6
	v_max_f32_e32 v8, 0xc2a00000, v8
	v_max_f32_e32 v9, 0xc2a00000, v9
	v_max_f32_e32 v2, 0xc2a00000, v2
	v_max_f32_e32 v3, 0xc2a00000, v3
	v_max_f32_e32 v4, 0xc2a00000, v4
	v_max_f32_e32 v5, 0xc2a00000, v5
	v_rcp_f32_e32 v16, v16
	v_rcp_f32_e32 v17, v17
	v_rcp_f32_e32 v12, v12
	v_mul_f32_e32 v6, 0xbfb8aa3b, v6
	v_mul_f32_e32 v8, 0xbfb8aa3b, v8
	v_mul_f32_e32 v9, 0xbfb8aa3b, v9
	v_mul_f32_e32 v2, 0xbfb8aa3b, v2
	v_mul_f32_e32 v3, 0xbfb8aa3b, v3
	v_mul_f32_e32 v4, 0xbfb8aa3b, v4
	v_mul_f32_e32 v5, 0xbfb8aa3b, v5
	v_exp_f32_e32 v15, v6
	v_exp_f32_e32 v8, v8
	v_exp_f32_e32 v9, v9
	v_exp_f32_e32 v2, v2
	v_exp_f32_e32 v3, v3
	v_exp_f32_e32 v4, v4
	v_exp_f32_e32 v5, v5
	v_fma_f32 v16, v178, v16, v138
	v_fmac_f32_e32 v139, v177, v17
	v_fmac_f32_e32 v135, v155, v12
	v_log_f32_e32 v16, v16
	v_log_f32_e32 v17, v139
	v_log_f32_e32 v20, v135
	v_add_f32_e32 v14, 1.0, v14
	v_add_f32_e32 v15, 1.0, v15
	v_add_f32_e32 v8, 1.0, v8
	v_add_f32_e32 v9, 1.0, v9
	v_add_f32_e32 v2, 1.0, v2
	v_add_f32_e32 v3, 1.0, v3
	v_add_f32_e32 v4, 1.0, v4
	v_add_f32_e32 v5, 1.0, v5
	s_mov_b64 s[14:15], 0xb0000
	v_rcp_f32_e32 v14, v14
	v_rcp_f32_e32 v15, v15
	v_rcp_f32_e32 v8, v8
	v_rcp_f32_e32 v9, v9
	v_rcp_f32_e32 v2, v2
	v_rcp_f32_e32 v3, v3
	v_rcp_f32_e32 v4, v4
	v_rcp_f32_e32 v5, v5
	v_lshl_add_u64 v[136:137], v[166:167], 0, s[14:15]
	s_mov_b32 s14, 0xb0000
	v_add_co_u32_e32 v6, vcc, s14, v166
	v_cvt_pk_f16_f32 v11, v16, v17
	v_cvt_pk_f16_f32 v12, v18, v13
	v_cvt_pk_f16_f32 v13, v19, v20
	v_addc_co_u32_e32 v7, vcc, 0, v167, vcc
	s_waitcnt lgkmcnt(11)
	v_subrev_u32_e32 v248, s82, v248
	global_store_dwordx4 v248, v[244:247], s[82:83] offset:64
	ds_bpermute_b32 v244, v250, v10
	ds_bpermute_b32 v245, v250, v11
	ds_bpermute_b32 v246, v250, v12
	ds_bpermute_b32 v247, v250, v13
	ds_bpermute_b32 v248, v250, v6
	v_fma_f32 v6, v153, v14, v128
	v_fma_f32 v7, v168, v15, v129
	v_fma_f32 v8, v121, v8, v130
	v_fmac_f32_e32 v131, v122, v9
	v_fma_f32 v2, v123, v2, v124
	v_fma_f32 v3, v120, v3, v125
	v_fma_f32 v4, v118, v4, v126
	v_fmac_f32_e32 v127, v119, v5
	v_log_f32_e32 v6, v6
	v_log_f32_e32 v7, v7
	v_log_f32_e32 v8, v8
	v_log_f32_e32 v9, v131
	v_log_f32_e32 v2, v2
	v_log_f32_e32 v3, v3
	v_log_f32_e32 v4, v4
	v_log_f32_e32 v5, v127
	v_cvt_pk_f16_f32 v196, v181, v182
	v_cvt_pk_f16_f32 v132, v6, v7
	v_cvt_pk_f16_f32 v133, v8, v9
	v_cvt_pk_f16_f32 v134, v2, v3
	v_cvt_pk_f16_f32 v135, v4, v5
	s_waitcnt lgkmcnt(11)
	v_subrev_u32_e32 v236, s82, v236
	global_store_dwordx4 v236, v[232:235], s[82:83]
	ds_bpermute_b32 v232, v250, v194
	ds_bpermute_b32 v233, v250, v195
	ds_bpermute_b32 v234, v250, v196
	ds_bpermute_b32 v235, v250, v197
	ds_bpermute_b32 v236, v250, v166
	s_andn2_b64 vcc, exec, s[38:39]
	s_mov_b64 s[28:29], -1
	s_waitcnt lgkmcnt(10)
	v_subrev_u32_e32 v242, s82, v242
	global_store_dwordx4 v242, v[238:241], s[82:83] offset:64
	ds_bpermute_b32 v238, v250, v132
	ds_bpermute_b32 v239, v250, v133
	ds_bpermute_b32 v240, v250, v134
	ds_bpermute_b32 v241, v250, v135
	ds_bpermute_b32 v242, v250, v136
	s_waitcnt lgkmcnt(10)
	v_subrev_u32_e32 v248, s82, v248
	global_store_dwordx4 v248, v[244:247], s[82:83]
	s_waitcnt lgkmcnt(5)
	v_subrev_u32_e32 v236, s82, v236
	global_store_dwordx4 v236, v[232:235], s[82:83] offset:64
	s_waitcnt lgkmcnt(0)
	v_subrev_u32_e32 v242, s82, v242
	global_store_dwordx4 v242, v[238:241], s[82:83] offset:64
	s_cbranch_vccnz .LBB0_338

.LBB0_541:
	s_and_b64 vcc, exec, s[40:41]
	s_cbranch_vccz .LBB0_540
	v_lshlrev_b32_e32 v155, 2, v177
	global_load_dwordx4 v[136:139], v155, s[42:43]
	global_load_dwordx4 v[132:135], v155, s[42:43] offset:16
	s_waitcnt lgkmcnt(0)
	v_mul_f32_e32 v160, v128, v154
	v_mul_f32_e32 v161, v129, v154
	v_mul_f32_e32 v166, v130, v154
	v_mul_f32_e32 v167, v131, v154
	v_mul_f32_e32 v168, v124, v154
	v_mul_f32_e32 v169, v125, v154
	v_mul_f32_e32 v170, v126, v154
	v_mul_f32_e32 v171, v127, v154
	global_load_dwordx4 v[124:127], v155, s[42:43] offset:144
	global_load_dwordx4 v[128:131], v155, s[42:43] offset:128
	v_ashrrev_i32_e32 v153, 31, v152
	v_lshlrev_b64 v[158:159], 12, v[152:153]
	v_max_f32_e32 v153, 0xc2a00000, v160
	v_max_f32_e32 v155, 0xc2a00000, v161
	v_max_f32_e32 v160, 0xc2a00000, v166
	v_max_f32_e32 v161, 0xc2a00000, v167
	v_max_f32_e32 v166, 0xc2a00000, v168
	v_max_f32_e32 v167, 0xc2a00000, v169
	v_max_f32_e32 v168, 0xc2a00000, v170
	v_max_f32_e32 v169, 0xc2a00000, v171
	v_mul_f32_e32 v153, 0xbfb8aa3b, v153
	v_mul_f32_e32 v155, 0xbfb8aa3b, v155
	v_mul_f32_e32 v168, 0xbfb8aa3b, v168
	v_mul_f32_e32 v169, 0xbfb8aa3b, v169
	v_exp_f32_e32 v153, v153
	v_exp_f32_e32 v155, v155
	v_mul_f32_e32 v160, 0xbfb8aa3b, v160
	v_mul_f32_e32 v161, 0xbfb8aa3b, v161
	v_exp_f32_e32 v168, v168
	v_exp_f32_e32 v169, v169
	v_exp_f32_e32 v160, v160
	v_exp_f32_e32 v161, v161
	v_mul_f32_e32 v120, v120, v154
	v_max_f32_e32 v120, 0xc2a00000, v120
	v_add_f32_e32 v153, 1.0, v153
	v_add_f32_e32 v155, 1.0, v155
	v_mul_f32_e32 v121, v121, v154
	v_lshlrev_b32_e32 v114, 1, v177
	v_mul_f32_e32 v166, 0xbfb8aa3b, v166
	v_mul_f32_e32 v167, 0xbfb8aa3b, v167
	v_lshl_add_u64 v[158:159], s[26:27], 0, v[158:159]
	v_add_f32_e32 v168, 1.0, v168
	v_add_f32_e32 v169, 1.0, v169
	v_rcp_f32_e32 v153, v153
	v_rcp_f32_e32 v181, v155
	v_mul_f32_e32 v120, 0xbfb8aa3b, v120
	v_max_f32_e32 v121, 0xc2a00000, v121
	v_exp_f32_e32 v170, v166
	v_exp_f32_e32 v171, v167
	v_lshl_add_u64 v[166:167], v[158:159], 0, v[114:115]
	v_add_f32_e32 v158, 1.0, v160
	v_add_f32_e32 v159, 1.0, v161
	v_rcp_f32_e32 v168, v168
	v_rcp_f32_e32 v182, v169
	v_exp_f32_e32 v120, v120
	v_mul_f32_e32 v121, 0xbfb8aa3b, v121
	v_rcp_f32_e32 v158, v158
	v_rcp_f32_e32 v159, v159
	v_exp_f32_e32 v121, v121
	v_add_f32_e32 v120, 1.0, v120
	v_rcp_f32_e32 v120, v120
	v_mul_f32_e32 v116, v116, v154
	v_add_f32_e32 v121, 1.0, v121
	v_rcp_f32_e32 v121, v121
	v_add_f32_e32 v160, 1.0, v170
	v_add_f32_e32 v161, 1.0, v171
	v_max_f32_e32 v116, 0xc2a00000, v116
	v_mul_f32_e32 v117, v117, v154
	v_rcp_f32_e32 v160, v160
	v_rcp_f32_e32 v161, v161
	v_mul_f32_e32 v116, 0xbfb8aa3b, v116
	v_max_f32_e32 v117, 0xc2a00000, v117
	v_exp_f32_e32 v116, v116
	v_mul_f32_e32 v117, 0xbfb8aa3b, v117
	v_exp_f32_e32 v117, v117
	s_mov_b64 s[14:15], 0x80000
	v_add_f32_e32 v116, 1.0, v116
	v_rcp_f32_e32 v116, v116
	v_add_f32_e32 v117, 1.0, v117
	s_waitcnt vmcnt(0)
	v_sub_f32_e32 v180, 1.0, v136
	v_sub_f32_e32 v179, 1.0, v137
	v_sub_f32_e32 v169, 1.0, v134
	v_sub_f32_e32 v155, 1.0, v135
	v_fma_f32 v153, v180, v153, v136
	v_fma_f32 v181, v179, v181, v137
	v_sub_f32_e32 v178, 1.0, v138
	v_sub_f32_e32 v177, 1.0, v139
	v_fma_f32 v168, v169, v168, v134
	v_fma_f32 v182, v155, v182, v135
	v_log_f32_e32 v153, v153
	v_log_f32_e32 v181, v181
	v_fma_f32 v158, v178, v158, v138
	v_fma_f32 v159, v177, v159, v139
	v_log_f32_e32 v168, v168
	v_log_f32_e32 v182, v182
	v_log_f32_e32 v158, v158
	v_log_f32_e32 v159, v159
	v_cvt_pk_f16_f32 v194, v153, v181
	v_sub_f32_e32 v153, 1.0, v128
	v_cvt_pk_f16_f32 v197, v168, v182
	v_fma_f32 v120, v153, v120, v128
	v_sub_f32_e32 v168, 1.0, v129
	v_cvt_pk_f16_f32 v195, v158, v159
	v_log_f32_e32 v158, v120
	v_fma_f32 v120, v168, v121, v129
	v_log_f32_e32 v159, v120
	v_mul_f32_e32 v120, v122, v154
	v_max_f32_e32 v120, 0xc2a00000, v120
	v_mul_f32_e32 v121, v123, v154
	v_mul_f32_e32 v120, 0xbfb8aa3b, v120
	v_max_f32_e32 v121, 0xc2a00000, v121
	v_exp_f32_e32 v120, v120
	v_mul_f32_e32 v121, 0xbfb8aa3b, v121
	v_exp_f32_e32 v122, v121
	v_sub_f32_e32 v171, 1.0, v132
	v_sub_f32_e32 v170, 1.0, v133
	v_add_f32_e32 v120, 1.0, v120
	v_fma_f32 v160, v171, v160, v132
	v_fma_f32 v161, v170, v161, v133
	v_rcp_f32_e32 v120, v120
	v_add_f32_e32 v122, 1.0, v122
	v_log_f32_e32 v160, v160
	v_log_f32_e32 v161, v161
	v_rcp_f32_e32 v123, v122
	v_sub_f32_e32 v121, 1.0, v130
	v_rcp_f32_e32 v117, v117
	v_fma_f32 v120, v121, v120, v130
	v_sub_f32_e32 v122, 1.0, v131
	v_cvt_pk_f16_f32 v196, v160, v161
	v_log_f32_e32 v160, v120
	v_fma_f32 v120, v122, v123, v131
	v_sub_f32_e32 v123, 1.0, v124
	v_log_f32_e32 v161, v120
	v_fma_f32 v116, v123, v116, v124
	v_sub_f32_e32 v120, 1.0, v125
	v_log_f32_e32 v181, v116
	v_fma_f32 v116, v120, v117, v125
	v_log_f32_e32 v182, v116
	v_mul_f32_e32 v116, v118, v154
	v_max_f32_e32 v116, 0xc2a00000, v116
	v_mul_f32_e32 v117, v119, v154
	v_mul_f32_e32 v116, 0xbfb8aa3b, v116
	v_max_f32_e32 v117, 0xc2a00000, v117
	v_exp_f32_e32 v116, v116
	v_mul_f32_e32 v117, 0xbfb8aa3b, v117
	v_exp_f32_e32 v117, v117
	v_sub_f32_e32 v118, 1.0, v126
	v_add_f32_e32 v116, 1.0, v116
	v_rcp_f32_e32 v116, v116
	v_add_f32_e32 v117, 1.0, v117
	v_rcp_f32_e32 v117, v117
	v_sub_f32_e32 v119, 1.0, v127
	v_fma_f32 v116, v118, v116, v126
	v_log_f32_e32 v154, v116
	v_fma_f32 v116, v119, v117, v127
	v_log_f32_e32 v183, v116
	ds_read2_b32 v[116:117], v176 offset0:16 offset1:32
	ds_bpermute_b32 v238, v250, v194
	ds_bpermute_b32 v239, v250, v195
	ds_bpermute_b32 v240, v250, v196
	ds_bpermute_b32 v241, v250, v197
	ds_bpermute_b32 v242, v250, v166
	s_waitcnt lgkmcnt(0)
	v_mul_f32_e32 v106, v106, v116
	v_max_f32_e32 v106, 0xc2a00000, v106
	v_mul_f32_e32 v106, 0xbfb8aa3b, v106
	v_exp_f32_e32 v106, v106
	v_mul_f32_e32 v110, v110, v116
	v_max_f32_e32 v110, 0xc2a00000, v110
	v_mul_f32_e32 v111, v111, v116
	v_mul_f32_e32 v110, 0xbfb8aa3b, v110
	v_max_f32_e32 v111, 0xc2a00000, v111
	v_mul_f32_e32 v107, v107, v116
	v_exp_f32_e32 v110, v110
	v_mul_f32_e32 v111, 0xbfb8aa3b, v111
	v_add_f32_e32 v106, 1.0, v106
	v_max_f32_e32 v107, 0xc2a00000, v107
	v_exp_f32_e32 v111, v111
	v_rcp_f32_e32 v106, v106
	v_mul_f32_e32 v107, 0xbfb8aa3b, v107
	v_exp_f32_e32 v107, v107
	v_cvt_pk_f16_f32 v194, v158, v159
	v_or_b32_e32 v158, 16, v152
	v_add_f32_e32 v110, 1.0, v110
	v_mul_f32_e32 v112, v112, v116
	v_mul_f32_e32 v113, v113, v116
	v_cvt_pk_f16_f32 v197, v154, v183
	v_ashrrev_i32_e32 v159, 31, v158
	v_rcp_f32_e32 v154, v110
	v_add_f32_e32 v110, 1.0, v111
	v_max_f32_e32 v112, 0xc2a00000, v112
	v_max_f32_e32 v113, 0xc2a00000, v113
	v_fma_f32 v106, v171, v106, v132
	v_cvt_pk_f16_f32 v195, v160, v161
	v_rcp_f32_e32 v160, v110
	v_lshlrev_b64 v[110:111], 12, v[158:159]
	v_mul_f32_e32 v112, 0xbfb8aa3b, v112
	v_mul_f32_e32 v113, 0xbfb8aa3b, v113
	v_log_f32_e32 v159, v106
	v_add_f32_e32 v106, 1.0, v107
	v_mul_f32_e32 v107, v108, v116
	v_exp_f32_e32 v112, v112
	v_exp_f32_e32 v113, v113
	v_max_f32_e32 v107, 0xc2a00000, v107
	v_mul_f32_e32 v108, v109, v116
	v_mul_f32_e32 v107, 0xbfb8aa3b, v107
	v_max_f32_e32 v108, 0xc2a00000, v108
	v_exp_f32_e32 v107, v107
	v_mul_f32_e32 v108, 0xbfb8aa3b, v108
	v_exp_f32_e32 v108, v108
	v_add_f32_e32 v112, 1.0, v112
	v_add_f32_e32 v113, 1.0, v113
	v_rcp_f32_e32 v112, v112
	v_rcp_f32_e32 v113, v113
	v_mul_f32_e32 v98, v98, v116
	v_rcp_f32_e32 v106, v106
	v_add_f32_e32 v107, 1.0, v107
	v_max_f32_e32 v98, 0xc2a00000, v98
	v_rcp_f32_e32 v107, v107
	v_add_f32_e32 v108, 1.0, v108
	v_mul_f32_e32 v98, 0xbfb8aa3b, v98
	v_rcp_f32_e32 v108, v108
	v_exp_f32_e32 v98, v98
	v_fma_f32 v112, v178, v112, v138
	v_fma_f32 v113, v177, v113, v139
	v_log_f32_e32 v112, v112
	v_log_f32_e32 v113, v113
	v_fma_f32 v106, v170, v106, v133
	v_log_f32_e32 v109, v106
	v_fma_f32 v106, v169, v107, v134
	v_mul_f32_e32 v102, v102, v116
	v_mul_f32_e32 v99, v99, v116
	v_fma_f32 v154, v180, v154, v136
	v_fma_f32 v158, v179, v160, v137
	v_log_f32_e32 v160, v106
	v_fma_f32 v106, v155, v108, v135
	v_max_f32_e32 v102, 0xc2a00000, v102
	v_add_f32_e32 v98, 1.0, v98
	v_max_f32_e32 v99, 0xc2a00000, v99
	v_log_f32_e32 v154, v154
	v_log_f32_e32 v158, v158
	v_log_f32_e32 v161, v106
	v_mul_f32_e32 v102, 0xbfb8aa3b, v102
	v_rcp_f32_e32 v98, v98
	v_mul_f32_e32 v99, 0xbfb8aa3b, v99
	v_cvt_pk_f16_f32 v107, v112, v113
	v_exp_f32_e32 v112, v102
	v_mul_f32_e32 v102, v103, v116
	v_exp_f32_e32 v99, v99
	v_max_f32_e32 v102, 0xc2a00000, v102
	v_lshl_add_u64 v[110:111], s[26:27], 0, v[110:111]
	v_mul_f32_e32 v102, 0xbfb8aa3b, v102
	v_cvt_pk_f16_f32 v106, v154, v158
	v_cvt_pk_f16_f32 v108, v159, v109
	v_cvt_pk_f16_f32 v109, v160, v161
	v_exp_f32_e32 v113, v102
	v_lshl_add_u64 v[102:103], v[110:111], 0, v[114:115]
	v_fma_f32 v98, v123, v98, v124
	ds_bpermute_b32 v244, v250, v106
	ds_bpermute_b32 v245, v250, v107
	ds_bpermute_b32 v246, v250, v108
	ds_bpermute_b32 v247, v250, v109
	ds_bpermute_b32 v248, v250, v102
	v_mul_f32_e32 v104, v104, v116
	v_mul_f32_e32 v105, v105, v116
	v_log_f32_e32 v108, v98
	v_add_f32_e32 v98, 1.0, v99
	v_mul_f32_e32 v99, v100, v116
	v_max_f32_e32 v99, 0xc2a00000, v99
	v_mul_f32_e32 v100, v101, v116
	v_max_f32_e32 v104, 0xc2a00000, v104
	v_max_f32_e32 v105, 0xc2a00000, v105
	v_mul_f32_e32 v99, 0xbfb8aa3b, v99
	v_max_f32_e32 v100, 0xc2a00000, v100
	v_mul_f32_e32 v104, 0xbfb8aa3b, v104
	v_mul_f32_e32 v105, 0xbfb8aa3b, v105
	v_exp_f32_e32 v99, v99
	v_mul_f32_e32 v100, 0xbfb8aa3b, v100
	v_exp_f32_e32 v104, v104
	v_exp_f32_e32 v105, v105
	v_exp_f32_e32 v100, v100
	v_rcp_f32_e32 v98, v98
	v_add_f32_e32 v99, 1.0, v99
	v_add_f32_e32 v110, 1.0, v112
	v_add_f32_e32 v111, 1.0, v113
	v_add_f32_e32 v104, 1.0, v104
	v_add_f32_e32 v105, 1.0, v105
	v_rcp_f32_e32 v99, v99
	v_add_f32_e32 v100, 1.0, v100
	v_rcp_f32_e32 v110, v110
	v_rcp_f32_e32 v111, v111
	v_rcp_f32_e32 v104, v104
	v_rcp_f32_e32 v105, v105
	v_rcp_f32_e32 v100, v100
	v_mul_f32_e32 v90, v90, v117
	v_fma_f32 v98, v120, v98, v125
	v_mul_f32_e32 v94, v94, v117
	v_max_f32_e32 v90, 0xc2a00000, v90
	v_log_f32_e32 v101, v98
	v_fma_f32 v98, v118, v99, v126
	v_max_f32_e32 v94, 0xc2a00000, v94
	v_mul_f32_e32 v90, 0xbfb8aa3b, v90
	v_fma_f32 v106, v153, v110, v128
	v_fma_f32 v107, v168, v111, v129
	v_fma_f32 v104, v121, v104, v130
	v_fma_f32 v105, v122, v105, v131
	v_log_f32_e32 v109, v98
	v_fma_f32 v98, v119, v100, v127
	v_mul_f32_e32 v94, 0xbfb8aa3b, v94
	v_exp_f32_e32 v90, v90
	v_log_f32_e32 v106, v106
	v_log_f32_e32 v107, v107
	v_log_f32_e32 v104, v104
	v_log_f32_e32 v105, v105
	v_log_f32_e32 v110, v98
	v_exp_f32_e32 v94, v94
	v_mul_f32_e32 v95, v95, v117
	v_max_f32_e32 v95, 0xc2a00000, v95
	v_mul_f32_e32 v91, v91, v117
	v_mul_f32_e32 v95, 0xbfb8aa3b, v95
	v_add_f32_e32 v90, 1.0, v90
	v_max_f32_e32 v91, 0xc2a00000, v91
	v_cvt_pk_f16_f32 v98, v106, v107
	v_cvt_pk_f16_f32 v99, v104, v105
	v_cvt_pk_f16_f32 v100, v108, v101
	v_cvt_pk_f16_f32 v101, v109, v110
	v_exp_f32_e32 v95, v95
	v_add_f32_e32 v94, 1.0, v94
	v_rcp_f32_e32 v90, v90
	v_mul_f32_e32 v91, 0xbfb8aa3b, v91
	ds_bpermute_b32 v232, v250, v98
	ds_bpermute_b32 v233, v250, v99
	ds_bpermute_b32 v234, v250, v100
	ds_bpermute_b32 v235, v250, v101
	ds_bpermute_b32 v236, v250, v102
	v_exp_f32_e32 v91, v91
	v_fma_f32 v90, v171, v90, v132
	v_rcp_f32_e32 v100, v94
	v_or_b32_e32 v98, 32, v152
	v_ashrrev_i32_e32 v99, 31, v98
	v_add_f32_e32 v94, 1.0, v95
	v_rcp_f32_e32 v101, v94
	v_lshlrev_b64 v[94:95], 12, v[98:99]
	v_fma_f32 v98, v180, v100, v136
	v_log_f32_e32 v100, v90
	v_add_f32_e32 v90, 1.0, v91
	v_mul_f32_e32 v91, v92, v117
	v_mul_f32_e32 v96, v96, v117
	v_mul_f32_e32 v97, v97, v117
	v_max_f32_e32 v91, 0xc2a00000, v91
	v_mul_f32_e32 v92, v93, v117
	v_max_f32_e32 v96, 0xc2a00000, v96
	v_max_f32_e32 v97, 0xc2a00000, v97
	v_mul_f32_e32 v91, 0xbfb8aa3b, v91
	v_max_f32_e32 v92, 0xc2a00000, v92
	v_mul_f32_e32 v96, 0xbfb8aa3b, v96
	v_mul_f32_e32 v97, 0xbfb8aa3b, v97
	v_exp_f32_e32 v91, v91
	v_mul_f32_e32 v92, 0xbfb8aa3b, v92
	v_exp_f32_e32 v96, v96
	v_exp_f32_e32 v97, v97
	v_exp_f32_e32 v92, v92
	v_mul_f32_e32 v82, v82, v117
	v_rcp_f32_e32 v90, v90
	v_add_f32_e32 v91, 1.0, v91
	v_max_f32_e32 v82, 0xc2a00000, v82
	v_add_f32_e32 v96, 1.0, v96
	v_add_f32_e32 v97, 1.0, v97
	v_rcp_f32_e32 v91, v91
	v_add_f32_e32 v92, 1.0, v92
	v_mul_f32_e32 v82, 0xbfb8aa3b, v82
	v_rcp_f32_e32 v96, v96
	v_rcp_f32_e32 v97, v97
	v_rcp_f32_e32 v92, v92
	v_exp_f32_e32 v82, v82
	v_fma_f32 v90, v170, v90, v133
	v_log_f32_e32 v93, v90
	v_fma_f32 v90, v169, v91, v134
	v_mul_f32_e32 v83, v83, v117
	v_fma_f32 v99, v179, v101, v137
	v_fma_f32 v96, v178, v96, v138
	v_fma_f32 v97, v177, v97, v139
	v_log_f32_e32 v101, v90
	v_fma_f32 v90, v155, v92, v135
	v_add_f32_e32 v82, 1.0, v82
	v_max_f32_e32 v83, 0xc2a00000, v83
	v_log_f32_e32 v98, v98
	v_log_f32_e32 v99, v99
	v_log_f32_e32 v96, v96
	v_log_f32_e32 v97, v97
	v_log_f32_e32 v102, v90
	v_rcp_f32_e32 v82, v82
	v_mul_f32_e32 v83, 0xbfb8aa3b, v83
	v_exp_f32_e32 v83, v83
	v_lshl_add_u64 v[94:95], s[26:27], 0, v[94:95]
	v_cvt_pk_f16_f32 v90, v98, v99
	v_cvt_pk_f16_f32 v91, v96, v97
	v_cvt_pk_f16_f32 v92, v100, v93
	v_cvt_pk_f16_f32 v93, v101, v102
	v_lshl_add_u64 v[94:95], v[94:95], 0, v[114:115]
	v_fma_f32 v82, v123, v82, v124
	s_waitcnt lgkmcnt(10)
	v_subrev_u32_e32 v242, s82, v242
	global_store_dwordx4 v242, v[238:241], s[82:83]
	ds_bpermute_b32 v238, v250, v90
	ds_bpermute_b32 v239, v250, v91
	ds_bpermute_b32 v240, v250, v92
	ds_bpermute_b32 v241, v250, v93
	ds_bpermute_b32 v242, v250, v94
	v_mul_f32_e32 v86, v86, v117
	v_mul_f32_e32 v87, v87, v117
	v_log_f32_e32 v90, v82
	v_add_f32_e32 v82, 1.0, v83
	v_mul_f32_e32 v83, v84, v117
	v_max_f32_e32 v83, 0xc2a00000, v83
	v_mul_f32_e32 v84, v85, v117
	v_mul_f32_e32 v83, 0xbfb8aa3b, v83
	v_max_f32_e32 v84, 0xc2a00000, v84
	v_exp_f32_e32 v83, v83
	v_mul_f32_e32 v84, 0xbfb8aa3b, v84
	v_exp_f32_e32 v84, v84
	v_rcp_f32_e32 v82, v82
	v_add_f32_e32 v83, 1.0, v83
	v_rcp_f32_e32 v83, v83
	v_add_f32_e32 v84, 1.0, v84
	v_rcp_f32_e32 v84, v84
	v_mul_f32_e32 v88, v88, v117
	v_mul_f32_e32 v89, v89, v117
	v_max_f32_e32 v86, 0xc2a00000, v86
	v_max_f32_e32 v87, 0xc2a00000, v87
	v_max_f32_e32 v88, 0xc2a00000, v88
	v_max_f32_e32 v89, 0xc2a00000, v89
	v_fma_f32 v82, v120, v82, v125
	v_mul_f32_e32 v86, 0xbfb8aa3b, v86
	v_mul_f32_e32 v87, 0xbfb8aa3b, v87
	v_mul_f32_e32 v88, 0xbfb8aa3b, v88
	v_mul_f32_e32 v89, 0xbfb8aa3b, v89
	v_log_f32_e32 v91, v82
	v_fma_f32 v82, v118, v83, v126
	v_exp_f32_e32 v86, v86
	v_exp_f32_e32 v87, v87
	v_exp_f32_e32 v88, v88
	v_exp_f32_e32 v89, v89
	v_log_f32_e32 v92, v82
	v_fma_f32 v82, v119, v84, v127
	v_log_f32_e32 v93, v82
	ds_read2_b32 v[82:83], v176 offset0:48 offset1:128
	v_add_f32_e32 v86, 1.0, v86
	v_add_f32_e32 v87, 1.0, v87
	v_add_f32_e32 v88, 1.0, v88
	v_add_f32_e32 v89, 1.0, v89
	v_rcp_f32_e32 v86, v86
	v_rcp_f32_e32 v87, v87
	v_rcp_f32_e32 v88, v88
	v_rcp_f32_e32 v89, v89
	s_waitcnt lgkmcnt(0)
	v_mul_f32_e32 v74, v74, v82
	v_mul_f32_e32 v78, v78, v82
	v_max_f32_e32 v74, 0xc2a00000, v74
	v_max_f32_e32 v78, 0xc2a00000, v78
	v_mul_f32_e32 v74, 0xbfb8aa3b, v74
	v_fma_f32 v86, v153, v86, v128
	v_fma_f32 v87, v168, v87, v129
	v_fma_f32 v88, v121, v88, v130
	v_fma_f32 v89, v122, v89, v131
	v_mul_f32_e32 v78, 0xbfb8aa3b, v78
	v_exp_f32_e32 v74, v74
	v_log_f32_e32 v86, v86
	v_log_f32_e32 v87, v87
	v_log_f32_e32 v88, v88
	v_log_f32_e32 v89, v89
	v_exp_f32_e32 v78, v78
	v_mul_f32_e32 v79, v79, v82
	v_max_f32_e32 v79, 0xc2a00000, v79
	v_mul_f32_e32 v75, v75, v82
	v_mul_f32_e32 v79, 0xbfb8aa3b, v79
	v_add_f32_e32 v74, 1.0, v74
	v_max_f32_e32 v75, 0xc2a00000, v75
	v_cvt_pk_f16_f32 v84, v86, v87
	v_cvt_pk_f16_f32 v85, v88, v89
	v_cvt_pk_f16_f32 v86, v90, v91
	v_cvt_pk_f16_f32 v87, v92, v93
	v_exp_f32_e32 v79, v79
	v_add_f32_e32 v78, 1.0, v78
	v_rcp_f32_e32 v74, v74
	v_mul_f32_e32 v75, 0xbfb8aa3b, v75
	s_waitcnt lgkmcnt(11)
	v_subrev_u32_e32 v248, s82, v248
	global_store_dwordx4 v248, v[244:247], s[82:83]
	ds_bpermute_b32 v244, v250, v84
	ds_bpermute_b32 v245, v250, v85
	ds_bpermute_b32 v246, v250, v86
	ds_bpermute_b32 v247, v250, v87
	ds_bpermute_b32 v248, v250, v94
	v_exp_f32_e32 v75, v75
	v_mul_f32_e32 v80, v80, v82
	v_rcp_f32_e32 v86, v78
	v_or_b32_e32 v84, 48, v152
	v_mul_f32_e32 v81, v81, v82
	v_ashrrev_i32_e32 v85, 31, v84
	v_add_f32_e32 v78, 1.0, v79
	v_max_f32_e32 v80, 0xc2a00000, v80
	v_max_f32_e32 v81, 0xc2a00000, v81
	v_fma_f32 v74, v171, v74, v132
	v_rcp_f32_e32 v87, v78
	v_lshlrev_b64 v[78:79], 12, v[84:85]
	v_fma_f32 v84, v180, v86, v136
	v_mul_f32_e32 v80, 0xbfb8aa3b, v80
	v_mul_f32_e32 v81, 0xbfb8aa3b, v81
	v_log_f32_e32 v86, v74
	v_add_f32_e32 v74, 1.0, v75
	v_mul_f32_e32 v75, v76, v82
	v_exp_f32_e32 v80, v80
	v_exp_f32_e32 v81, v81
	v_max_f32_e32 v75, 0xc2a00000, v75
	v_mul_f32_e32 v76, v77, v82
	v_mul_f32_e32 v75, 0xbfb8aa3b, v75
	v_max_f32_e32 v76, 0xc2a00000, v76
	v_exp_f32_e32 v75, v75
	v_mul_f32_e32 v76, 0xbfb8aa3b, v76
	v_exp_f32_e32 v76, v76
	v_add_f32_e32 v80, 1.0, v80
	v_add_f32_e32 v81, 1.0, v81
	v_rcp_f32_e32 v80, v80
	v_rcp_f32_e32 v81, v81
	v_mul_f32_e32 v66, v66, v82
	v_rcp_f32_e32 v74, v74
	v_add_f32_e32 v75, 1.0, v75
	v_max_f32_e32 v66, 0xc2a00000, v66
	v_rcp_f32_e32 v75, v75
	v_add_f32_e32 v76, 1.0, v76
	v_mul_f32_e32 v66, 0xbfb8aa3b, v66
	v_rcp_f32_e32 v76, v76
	v_exp_f32_e32 v66, v66
	v_fma_f32 v80, v178, v80, v138
	v_fma_f32 v81, v177, v81, v139
	v_log_f32_e32 v80, v80
	v_log_f32_e32 v81, v81
	v_fma_f32 v74, v170, v74, v133
	v_log_f32_e32 v77, v74
	v_fma_f32 v74, v169, v75, v134
	v_mul_f32_e32 v70, v70, v82
	v_mul_f32_e32 v67, v67, v82
	v_fma_f32 v85, v179, v87, v137
	v_log_f32_e32 v87, v74
	v_fma_f32 v74, v155, v76, v135
	v_max_f32_e32 v70, 0xc2a00000, v70
	v_add_f32_e32 v66, 1.0, v66
	v_max_f32_e32 v67, 0xc2a00000, v67
	v_log_f32_e32 v84, v84
	v_log_f32_e32 v85, v85
	v_log_f32_e32 v88, v74
	v_mul_f32_e32 v70, 0xbfb8aa3b, v70
	v_rcp_f32_e32 v66, v66
	v_mul_f32_e32 v67, 0xbfb8aa3b, v67
	v_cvt_pk_f16_f32 v75, v80, v81
	v_exp_f32_e32 v80, v70
	v_mul_f32_e32 v70, v71, v82
	v_exp_f32_e32 v67, v67
	v_max_f32_e32 v70, 0xc2a00000, v70
	v_lshl_add_u64 v[78:79], s[26:27], 0, v[78:79]
	v_mul_f32_e32 v70, 0xbfb8aa3b, v70
	v_cvt_pk_f16_f32 v74, v84, v85
	v_cvt_pk_f16_f32 v76, v86, v77
	v_cvt_pk_f16_f32 v77, v87, v88
	v_exp_f32_e32 v81, v70
	v_lshl_add_u64 v[70:71], v[78:79], 0, v[114:115]
	v_fma_f32 v66, v123, v66, v124
	s_waitcnt lgkmcnt(11)
	v_subrev_u32_e32 v236, s82, v236
	global_store_dwordx4 v236, v[232:235], s[82:83] offset:64
	ds_bpermute_b32 v232, v250, v74
	ds_bpermute_b32 v233, v250, v75
	ds_bpermute_b32 v234, v250, v76
	ds_bpermute_b32 v235, v250, v77
	ds_bpermute_b32 v236, v250, v70
	v_mul_f32_e32 v72, v72, v82
	v_mul_f32_e32 v73, v73, v82
	v_log_f32_e32 v76, v66
	v_add_f32_e32 v66, 1.0, v67
	v_mul_f32_e32 v67, v68, v82
	v_max_f32_e32 v67, 0xc2a00000, v67
	v_mul_f32_e32 v68, v69, v82
	v_max_f32_e32 v72, 0xc2a00000, v72
	v_max_f32_e32 v73, 0xc2a00000, v73
	v_mul_f32_e32 v67, 0xbfb8aa3b, v67
	v_max_f32_e32 v68, 0xc2a00000, v68
	v_mul_f32_e32 v72, 0xbfb8aa3b, v72
	v_mul_f32_e32 v73, 0xbfb8aa3b, v73
	v_exp_f32_e32 v67, v67
	v_mul_f32_e32 v68, 0xbfb8aa3b, v68
	v_exp_f32_e32 v72, v72
	v_exp_f32_e32 v73, v73
	v_exp_f32_e32 v68, v68
	v_mul_f32_e32 v58, v58, v83
	v_rcp_f32_e32 v66, v66
	v_add_f32_e32 v67, 1.0, v67
	v_max_f32_e32 v58, 0xc2a00000, v58
	v_add_f32_e32 v78, 1.0, v80
	v_add_f32_e32 v79, 1.0, v81
	v_add_f32_e32 v72, 1.0, v72
	v_add_f32_e32 v73, 1.0, v73
	v_rcp_f32_e32 v67, v67
	v_add_f32_e32 v68, 1.0, v68
	v_mul_f32_e32 v58, 0xbfb8aa3b, v58
	v_rcp_f32_e32 v78, v78
	v_rcp_f32_e32 v79, v79
	v_rcp_f32_e32 v72, v72
	v_rcp_f32_e32 v73, v73
	v_rcp_f32_e32 v68, v68
	v_exp_f32_e32 v58, v58
	v_fma_f32 v66, v120, v66, v125
	v_log_f32_e32 v69, v66
	v_fma_f32 v66, v118, v67, v126
	v_mul_f32_e32 v59, v59, v83
	v_fma_f32 v74, v153, v78, v128
	v_fma_f32 v75, v168, v79, v129
	v_fma_f32 v72, v121, v72, v130
	v_fma_f32 v73, v122, v73, v131
	v_log_f32_e32 v77, v66
	v_fma_f32 v66, v119, v68, v127
	v_add_f32_e32 v58, 1.0, v58
	v_max_f32_e32 v59, 0xc2a00000, v59
	v_log_f32_e32 v74, v74
	v_log_f32_e32 v75, v75
	v_log_f32_e32 v72, v72
	v_log_f32_e32 v73, v73
	v_log_f32_e32 v78, v66
	v_rcp_f32_e32 v58, v58
	v_mul_f32_e32 v59, 0xbfb8aa3b, v59
	v_exp_f32_e32 v59, v59
	v_mul_f32_e32 v64, v64, v83
	v_mul_f32_e32 v65, v65, v83
	v_max_f32_e32 v64, 0xc2a00000, v64
	v_max_f32_e32 v65, 0xc2a00000, v65
	v_cvt_pk_f16_f32 v66, v74, v75
	v_cvt_pk_f16_f32 v67, v72, v73
	v_cvt_pk_f16_f32 v68, v76, v69
	v_mul_f32_e32 v62, v62, v83
	v_mul_f32_e32 v63, v63, v83
	v_cvt_pk_f16_f32 v69, v77, v78
	v_mul_f32_e32 v64, 0xbfb8aa3b, v64
	v_mul_f32_e32 v65, 0xbfb8aa3b, v65
	v_fma_f32 v58, v171, v58, v132
	v_max_f32_e32 v62, 0xc2a00000, v62
	v_max_f32_e32 v63, 0xc2a00000, v63
	s_waitcnt lgkmcnt(11)
	v_subrev_u32_e32 v242, s82, v242
	global_store_dwordx4 v242, v[238:241], s[82:83]
	ds_bpermute_b32 v238, v250, v66
	ds_bpermute_b32 v239, v250, v67
	ds_bpermute_b32 v240, v250, v68
	ds_bpermute_b32 v241, v250, v69
	ds_bpermute_b32 v242, v250, v70
	v_exp_f32_e32 v64, v64
	v_exp_f32_e32 v65, v65
	v_log_f32_e32 v66, v58
	v_add_f32_e32 v58, 1.0, v59
	v_mul_f32_e32 v59, v60, v83
	v_mul_f32_e32 v62, 0xbfb8aa3b, v62
	v_mul_f32_e32 v63, 0xbfb8aa3b, v63
	v_max_f32_e32 v59, 0xc2a00000, v59
	v_mul_f32_e32 v60, v61, v83
	v_exp_f32_e32 v62, v62
	v_exp_f32_e32 v63, v63
	v_mul_f32_e32 v59, 0xbfb8aa3b, v59
	v_max_f32_e32 v60, 0xc2a00000, v60
	v_exp_f32_e32 v59, v59
	v_mul_f32_e32 v60, 0xbfb8aa3b, v60
	v_add_f32_e32 v64, 1.0, v64
	v_add_f32_e32 v65, 1.0, v65
	v_exp_f32_e32 v60, v60
	v_rcp_f32_e32 v64, v64
	v_rcp_f32_e32 v65, v65
	v_add_f32_e32 v62, 1.0, v62
	v_add_f32_e32 v63, 1.0, v63
	v_mul_f32_e32 v50, v50, v83
	v_rcp_f32_e32 v62, v62
	v_rcp_f32_e32 v63, v63
	v_rcp_f32_e32 v58, v58
	v_add_f32_e32 v59, 1.0, v59
	v_max_f32_e32 v50, 0xc2a00000, v50
	v_rcp_f32_e32 v59, v59
	v_add_f32_e32 v60, 1.0, v60
	v_mul_f32_e32 v50, 0xbfb8aa3b, v50
	v_fma_f32 v64, v178, v64, v138
	v_fma_f32 v65, v177, v65, v139
	v_rcp_f32_e32 v60, v60
	v_exp_f32_e32 v50, v50
	v_log_f32_e32 v64, v64
	v_log_f32_e32 v65, v65
	v_fma_f32 v62, v180, v62, v136
	v_fma_f32 v63, v179, v63, v137
	v_fma_f32 v58, v170, v58, v133
	v_mul_f32_e32 v54, v54, v83
	v_log_f32_e32 v62, v62
	v_log_f32_e32 v63, v63
	v_log_f32_e32 v61, v58
	v_fma_f32 v58, v169, v59, v134
	v_max_f32_e32 v54, 0xc2a00000, v54
	v_mul_f32_e32 v51, v51, v83
	v_log_f32_e32 v67, v58
	v_fma_f32 v58, v155, v60, v135
	v_mul_f32_e32 v54, 0xbfb8aa3b, v54
	v_add_f32_e32 v50, 1.0, v50
	v_max_f32_e32 v51, 0xc2a00000, v51
	v_log_f32_e32 v68, v58
	v_cvt_pk_f16_f32 v59, v64, v65
	v_exp_f32_e32 v64, v54
	v_mul_f32_e32 v54, v55, v83
	v_rcp_f32_e32 v50, v50
	v_mul_f32_e32 v51, 0xbfb8aa3b, v51
	v_max_f32_e32 v54, 0xc2a00000, v54
	v_exp_f32_e32 v51, v51
	v_cvt_pk_f16_f32 v58, v62, v63
	v_lshl_add_u64 v[62:63], v[166:167], 0, s[14:15]
	v_mul_f32_e32 v54, 0xbfb8aa3b, v54
	s_mov_b32 s14, 0x80000
	v_exp_f32_e32 v65, v54
	v_add_co_u32_e32 v54, vcc, s14, v166
	v_cvt_pk_f16_f32 v60, v66, v61
	v_cvt_pk_f16_f32 v61, v67, v68
	v_addc_co_u32_e32 v55, vcc, 0, v167, vcc
	v_fma_f32 v50, v123, v50, v124
	s_waitcnt lgkmcnt(10)
	v_subrev_u32_e32 v248, s82, v248
	global_store_dwordx4 v248, v[244:247], s[82:83] offset:64
	ds_bpermute_b32 v244, v250, v58
	ds_bpermute_b32 v245, v250, v59
	ds_bpermute_b32 v246, v250, v60
	ds_bpermute_b32 v247, v250, v61
	ds_bpermute_b32 v248, v250, v54
	v_mul_f32_e32 v56, v56, v83
	v_mul_f32_e32 v57, v57, v83
	v_log_f32_e32 v58, v50
	v_add_f32_e32 v50, 1.0, v51
	v_mul_f32_e32 v51, v52, v83
	v_max_f32_e32 v51, 0xc2a00000, v51
	v_mul_f32_e32 v51, 0xbfb8aa3b, v51
	v_exp_f32_e32 v51, v51
	v_rcp_f32_e32 v50, v50
	v_mul_f32_e32 v52, v53, v83
	v_max_f32_e32 v56, 0xc2a00000, v56
	v_add_f32_e32 v51, 1.0, v51
	v_rcp_f32_e32 v51, v51
	v_fma_f32 v50, v120, v50, v125
	v_log_f32_e32 v59, v50
	v_max_f32_e32 v57, 0xc2a00000, v57
	v_fma_f32 v50, v118, v51, v126
	v_log_f32_e32 v60, v50
	ds_read2_b32 v[50:51], v176 offset0:144 offset1:160
	v_max_f32_e32 v52, 0xc2a00000, v52
	v_mul_f32_e32 v56, 0xbfb8aa3b, v56
	v_mul_f32_e32 v57, 0xbfb8aa3b, v57
	v_mul_f32_e32 v52, 0xbfb8aa3b, v52
	v_exp_f32_e32 v56, v56
	v_exp_f32_e32 v57, v57
	v_exp_f32_e32 v52, v52
	s_waitcnt lgkmcnt(0)
	v_mul_f32_e32 v42, v42, v50
	v_max_f32_e32 v42, 0xc2a00000, v42
	v_add_f32_e32 v64, 1.0, v64
	v_add_f32_e32 v65, 1.0, v65
	v_add_f32_e32 v56, 1.0, v56
	v_add_f32_e32 v57, 1.0, v57
	v_add_f32_e32 v52, 1.0, v52
	v_mul_f32_e32 v42, 0xbfb8aa3b, v42
	v_rcp_f32_e32 v64, v64
	v_rcp_f32_e32 v65, v65
	v_rcp_f32_e32 v56, v56
	v_rcp_f32_e32 v57, v57
	v_rcp_f32_e32 v52, v52
	v_exp_f32_e32 v42, v42
	v_mul_f32_e32 v43, v43, v50
	v_fma_f32 v54, v153, v64, v128
	v_fma_f32 v55, v168, v65, v129
	v_fma_f32 v56, v121, v56, v130
	v_fma_f32 v57, v122, v57, v131
	v_fma_f32 v52, v119, v52, v127
	v_add_f32_e32 v42, 1.0, v42
	v_max_f32_e32 v43, 0xc2a00000, v43
	v_log_f32_e32 v54, v54
	v_log_f32_e32 v55, v55
	v_log_f32_e32 v56, v56
	v_log_f32_e32 v57, v57
	v_log_f32_e32 v61, v52
	v_rcp_f32_e32 v42, v42
	v_mul_f32_e32 v43, 0xbfb8aa3b, v43
	v_exp_f32_e32 v43, v43
	v_mul_f32_e32 v48, v48, v50
	v_mul_f32_e32 v49, v49, v50
	v_max_f32_e32 v48, 0xc2a00000, v48
	v_max_f32_e32 v49, 0xc2a00000, v49
	v_cvt_pk_f16_f32 v52, v54, v55
	v_cvt_pk_f16_f32 v53, v56, v57
	v_cvt_pk_f16_f32 v54, v58, v59
	v_mul_f32_e32 v46, v46, v50
	v_mul_f32_e32 v47, v47, v50
	v_cvt_pk_f16_f32 v55, v60, v61
	v_mul_f32_e32 v48, 0xbfb8aa3b, v48
	v_mul_f32_e32 v49, 0xbfb8aa3b, v49
	v_fma_f32 v42, v171, v42, v132
	v_max_f32_e32 v46, 0xc2a00000, v46
	v_max_f32_e32 v47, 0xc2a00000, v47
	s_waitcnt lgkmcnt(11)
	v_subrev_u32_e32 v236, s82, v236
	global_store_dwordx4 v236, v[232:235], s[82:83]
	ds_bpermute_b32 v232, v250, v52
	ds_bpermute_b32 v233, v250, v53
	ds_bpermute_b32 v234, v250, v54
	ds_bpermute_b32 v235, v250, v55
	ds_bpermute_b32 v236, v250, v62
	v_exp_f32_e32 v48, v48
	v_exp_f32_e32 v49, v49
	v_log_f32_e32 v52, v42
	v_add_f32_e32 v42, 1.0, v43
	v_mul_f32_e32 v43, v44, v50
	v_mul_f32_e32 v46, 0xbfb8aa3b, v46
	v_mul_f32_e32 v47, 0xbfb8aa3b, v47
	v_max_f32_e32 v43, 0xc2a00000, v43
	v_mul_f32_e32 v44, v45, v50
	v_exp_f32_e32 v46, v46
	v_exp_f32_e32 v47, v47
	v_mul_f32_e32 v43, 0xbfb8aa3b, v43
	v_max_f32_e32 v44, 0xc2a00000, v44
	v_exp_f32_e32 v43, v43
	v_mul_f32_e32 v44, 0xbfb8aa3b, v44
	v_add_f32_e32 v48, 1.0, v48
	v_add_f32_e32 v49, 1.0, v49
	v_exp_f32_e32 v44, v44
	v_rcp_f32_e32 v48, v48
	v_rcp_f32_e32 v49, v49
	v_add_f32_e32 v46, 1.0, v46
	v_add_f32_e32 v47, 1.0, v47
	v_mul_f32_e32 v34, v34, v50
	v_rcp_f32_e32 v46, v46
	v_rcp_f32_e32 v47, v47
	v_rcp_f32_e32 v42, v42
	v_add_f32_e32 v43, 1.0, v43
	v_max_f32_e32 v34, 0xc2a00000, v34
	v_rcp_f32_e32 v43, v43
	v_add_f32_e32 v44, 1.0, v44
	v_mul_f32_e32 v34, 0xbfb8aa3b, v34
	v_fma_f32 v48, v178, v48, v138
	v_fma_f32 v49, v177, v49, v139
	v_rcp_f32_e32 v44, v44
	v_exp_f32_e32 v34, v34
	v_log_f32_e32 v48, v48
	v_log_f32_e32 v49, v49
	v_fma_f32 v46, v180, v46, v136
	v_fma_f32 v47, v179, v47, v137
	v_fma_f32 v42, v170, v42, v133
	v_mul_f32_e32 v38, v38, v50
	v_log_f32_e32 v46, v46
	v_log_f32_e32 v47, v47
	v_log_f32_e32 v45, v42
	v_fma_f32 v42, v169, v43, v134
	v_max_f32_e32 v38, 0xc2a00000, v38
	v_mul_f32_e32 v35, v35, v50
	v_log_f32_e32 v53, v42
	v_fma_f32 v42, v155, v44, v135
	v_mul_f32_e32 v38, 0xbfb8aa3b, v38
	v_add_f32_e32 v34, 1.0, v34
	v_max_f32_e32 v35, 0xc2a00000, v35
	v_log_f32_e32 v54, v42
	v_cvt_pk_f16_f32 v43, v48, v49
	v_exp_f32_e32 v48, v38
	v_mul_f32_e32 v38, v39, v50
	v_rcp_f32_e32 v34, v34
	v_mul_f32_e32 v35, 0xbfb8aa3b, v35
	s_mov_b64 s[14:15], 0x90000
	v_max_f32_e32 v38, 0xc2a00000, v38
	v_exp_f32_e32 v35, v35
	v_cvt_pk_f16_f32 v42, v46, v47
	v_lshl_add_u64 v[46:47], v[166:167], 0, s[14:15]
	v_mul_f32_e32 v38, 0xbfb8aa3b, v38
	s_mov_b32 s14, 0x90000
	v_exp_f32_e32 v49, v38
	v_add_co_u32_e32 v38, vcc, s14, v166
	v_cvt_pk_f16_f32 v44, v52, v45
	v_cvt_pk_f16_f32 v45, v53, v54
	v_addc_co_u32_e32 v39, vcc, 0, v167, vcc
	v_fma_f32 v34, v123, v34, v124
	s_waitcnt lgkmcnt(11)
	v_subrev_u32_e32 v242, s82, v242
	global_store_dwordx4 v242, v[238:241], s[82:83] offset:64
	ds_bpermute_b32 v238, v250, v42
	ds_bpermute_b32 v239, v250, v43
	ds_bpermute_b32 v240, v250, v44
	ds_bpermute_b32 v241, v250, v45
	ds_bpermute_b32 v242, v250, v38
	v_mul_f32_e32 v40, v40, v50
	v_mul_f32_e32 v41, v41, v50
	v_log_f32_e32 v42, v34
	v_add_f32_e32 v34, 1.0, v35
	v_mul_f32_e32 v35, v36, v50
	v_max_f32_e32 v35, 0xc2a00000, v35
	v_mul_f32_e32 v36, v37, v50
	v_max_f32_e32 v40, 0xc2a00000, v40
	v_max_f32_e32 v41, 0xc2a00000, v41
	v_mul_f32_e32 v35, 0xbfb8aa3b, v35
	v_max_f32_e32 v36, 0xc2a00000, v36
	v_mul_f32_e32 v40, 0xbfb8aa3b, v40
	v_mul_f32_e32 v41, 0xbfb8aa3b, v41
	v_exp_f32_e32 v35, v35
	v_mul_f32_e32 v36, 0xbfb8aa3b, v36
	v_exp_f32_e32 v40, v40
	v_exp_f32_e32 v41, v41
	v_exp_f32_e32 v36, v36
	v_mul_f32_e32 v26, v26, v51
	v_rcp_f32_e32 v34, v34
	v_add_f32_e32 v35, 1.0, v35
	v_max_f32_e32 v26, 0xc2a00000, v26
	v_add_f32_e32 v48, 1.0, v48
	v_add_f32_e32 v49, 1.0, v49
	v_add_f32_e32 v40, 1.0, v40
	v_add_f32_e32 v41, 1.0, v41
	v_rcp_f32_e32 v35, v35
	v_add_f32_e32 v36, 1.0, v36
	v_mul_f32_e32 v26, 0xbfb8aa3b, v26
	v_rcp_f32_e32 v48, v48
	v_rcp_f32_e32 v49, v49
	v_rcp_f32_e32 v40, v40
	v_rcp_f32_e32 v41, v41
	v_rcp_f32_e32 v36, v36
	v_exp_f32_e32 v26, v26
	v_fma_f32 v34, v120, v34, v125
	v_log_f32_e32 v37, v34
	v_fma_f32 v34, v118, v35, v126
	v_mul_f32_e32 v27, v27, v51
	v_fma_f32 v38, v153, v48, v128
	v_fma_f32 v39, v168, v49, v129
	v_fma_f32 v40, v121, v40, v130
	v_fma_f32 v41, v122, v41, v131
	v_log_f32_e32 v43, v34
	v_fma_f32 v34, v119, v36, v127
	v_add_f32_e32 v26, 1.0, v26
	v_max_f32_e32 v27, 0xc2a00000, v27
	v_log_f32_e32 v38, v38
	v_log_f32_e32 v39, v39
	v_log_f32_e32 v40, v40
	v_log_f32_e32 v41, v41
	v_log_f32_e32 v44, v34
	v_rcp_f32_e32 v26, v26
	v_mul_f32_e32 v27, 0xbfb8aa3b, v27
	v_exp_f32_e32 v27, v27
	v_mul_f32_e32 v32, v32, v51
	v_mul_f32_e32 v33, v33, v51
	v_max_f32_e32 v32, 0xc2a00000, v32
	v_max_f32_e32 v33, 0xc2a00000, v33
	v_cvt_pk_f16_f32 v34, v38, v39
	v_cvt_pk_f16_f32 v35, v40, v41
	v_cvt_pk_f16_f32 v36, v42, v37
	v_mul_f32_e32 v30, v30, v51
	v_mul_f32_e32 v31, v31, v51
	v_cvt_pk_f16_f32 v37, v43, v44
	v_mul_f32_e32 v32, 0xbfb8aa3b, v32
	v_mul_f32_e32 v33, 0xbfb8aa3b, v33
	v_fma_f32 v26, v171, v26, v132
	v_max_f32_e32 v30, 0xc2a00000, v30
	v_max_f32_e32 v31, 0xc2a00000, v31
	s_waitcnt lgkmcnt(11)
	v_subrev_u32_e32 v248, s82, v248
	global_store_dwordx4 v248, v[244:247], s[82:83]
	ds_bpermute_b32 v244, v250, v34
	ds_bpermute_b32 v245, v250, v35
	ds_bpermute_b32 v246, v250, v36
	ds_bpermute_b32 v247, v250, v37
	ds_bpermute_b32 v248, v250, v46
	v_exp_f32_e32 v32, v32
	v_exp_f32_e32 v33, v33
	v_log_f32_e32 v34, v26
	v_add_f32_e32 v26, 1.0, v27
	v_mul_f32_e32 v27, v28, v51
	v_mul_f32_e32 v30, 0xbfb8aa3b, v30
	v_mul_f32_e32 v31, 0xbfb8aa3b, v31
	v_max_f32_e32 v27, 0xc2a00000, v27
	v_mul_f32_e32 v28, v29, v51
	v_exp_f32_e32 v30, v30
	v_exp_f32_e32 v31, v31
	v_mul_f32_e32 v27, 0xbfb8aa3b, v27
	v_max_f32_e32 v28, 0xc2a00000, v28
	v_exp_f32_e32 v27, v27
	v_mul_f32_e32 v28, 0xbfb8aa3b, v28
	v_add_f32_e32 v32, 1.0, v32
	v_add_f32_e32 v33, 1.0, v33
	v_exp_f32_e32 v28, v28
	v_rcp_f32_e32 v32, v32
	v_rcp_f32_e32 v33, v33
	v_add_f32_e32 v30, 1.0, v30
	v_add_f32_e32 v31, 1.0, v31
	v_mul_f32_e32 v18, v18, v51
	v_rcp_f32_e32 v30, v30
	v_rcp_f32_e32 v31, v31
	v_rcp_f32_e32 v26, v26
	v_add_f32_e32 v27, 1.0, v27
	v_max_f32_e32 v18, 0xc2a00000, v18
	v_rcp_f32_e32 v27, v27
	v_add_f32_e32 v28, 1.0, v28
	v_mul_f32_e32 v18, 0xbfb8aa3b, v18
	v_fma_f32 v32, v178, v32, v138
	v_fma_f32 v33, v177, v33, v139
	v_rcp_f32_e32 v28, v28
	v_exp_f32_e32 v18, v18
	v_log_f32_e32 v32, v32
	v_log_f32_e32 v33, v33
	v_fma_f32 v30, v180, v30, v136
	v_fma_f32 v31, v179, v31, v137
	v_fma_f32 v26, v170, v26, v133
	v_mul_f32_e32 v22, v22, v51
	v_log_f32_e32 v30, v30
	v_log_f32_e32 v31, v31
	v_log_f32_e32 v29, v26
	v_fma_f32 v26, v169, v27, v134
	v_max_f32_e32 v22, 0xc2a00000, v22
	v_mul_f32_e32 v19, v19, v51
	v_log_f32_e32 v35, v26
	v_fma_f32 v26, v155, v28, v135
	v_mul_f32_e32 v22, 0xbfb8aa3b, v22
	v_add_f32_e32 v18, 1.0, v18
	v_max_f32_e32 v19, 0xc2a00000, v19
	v_log_f32_e32 v36, v26
	v_cvt_pk_f16_f32 v27, v32, v33
	v_exp_f32_e32 v32, v22
	v_mul_f32_e32 v22, v23, v51
	v_rcp_f32_e32 v18, v18
	v_mul_f32_e32 v19, 0xbfb8aa3b, v19
	s_mov_b64 s[14:15], 0xa0000
	v_max_f32_e32 v22, 0xc2a00000, v22
	v_exp_f32_e32 v19, v19
	v_cvt_pk_f16_f32 v26, v30, v31
	v_lshl_add_u64 v[30:31], v[166:167], 0, s[14:15]
	v_mul_f32_e32 v22, 0xbfb8aa3b, v22
	s_mov_b32 s14, 0xa0000
	v_exp_f32_e32 v33, v22
	v_add_co_u32_e32 v22, vcc, s14, v166
	v_cvt_pk_f16_f32 v28, v34, v29
	v_cvt_pk_f16_f32 v29, v35, v36
	v_addc_co_u32_e32 v23, vcc, 0, v167, vcc
	v_fma_f32 v18, v123, v18, v124
	s_waitcnt lgkmcnt(10)
	v_subrev_u32_e32 v236, s82, v236
	global_store_dwordx4 v236, v[232:235], s[82:83] offset:64
	ds_bpermute_b32 v232, v250, v26
	ds_bpermute_b32 v233, v250, v27
	ds_bpermute_b32 v234, v250, v28
	ds_bpermute_b32 v235, v250, v29
	ds_bpermute_b32 v236, v250, v22
	v_mul_f32_e32 v24, v24, v51
	v_mul_f32_e32 v25, v25, v51
	v_log_f32_e32 v26, v18
	v_add_f32_e32 v18, 1.0, v19
	v_mul_f32_e32 v19, v20, v51
	v_max_f32_e32 v19, 0xc2a00000, v19
	v_mul_f32_e32 v20, v21, v51
	ds_read_b32 v28, v176 offset:704
	v_max_f32_e32 v24, 0xc2a00000, v24
	v_max_f32_e32 v25, 0xc2a00000, v25
	v_mul_f32_e32 v19, 0xbfb8aa3b, v19
	v_max_f32_e32 v20, 0xc2a00000, v20
	v_mul_f32_e32 v24, 0xbfb8aa3b, v24
	v_mul_f32_e32 v25, 0xbfb8aa3b, v25
	v_exp_f32_e32 v19, v19
	v_mul_f32_e32 v20, 0xbfb8aa3b, v20
	v_exp_f32_e32 v24, v24
	v_exp_f32_e32 v25, v25
	v_exp_f32_e32 v20, v20
	s_waitcnt lgkmcnt(0)
	v_mul_f32_e32 v10, v10, v28
	v_rcp_f32_e32 v18, v18
	v_add_f32_e32 v19, 1.0, v19
	v_max_f32_e32 v10, 0xc2a00000, v10
	v_add_f32_e32 v32, 1.0, v32
	v_add_f32_e32 v33, 1.0, v33
	v_add_f32_e32 v24, 1.0, v24
	v_add_f32_e32 v25, 1.0, v25
	v_rcp_f32_e32 v19, v19
	v_add_f32_e32 v20, 1.0, v20
	v_mul_f32_e32 v10, 0xbfb8aa3b, v10
	v_rcp_f32_e32 v32, v32
	v_rcp_f32_e32 v33, v33
	v_rcp_f32_e32 v24, v24
	v_rcp_f32_e32 v25, v25
	v_rcp_f32_e32 v20, v20
	v_exp_f32_e32 v10, v10
	v_fma_f32 v18, v120, v18, v125
	v_log_f32_e32 v21, v18
	v_fma_f32 v18, v118, v19, v126
	v_mul_f32_e32 v11, v11, v28
	v_fma_f32 v22, v153, v32, v128
	v_fma_f32 v23, v168, v33, v129
	v_fma_f32 v24, v121, v24, v130
	v_fma_f32 v25, v122, v25, v131
	v_log_f32_e32 v27, v18
	v_fma_f32 v18, v119, v20, v127
	v_add_f32_e32 v10, 1.0, v10
	v_max_f32_e32 v11, 0xc2a00000, v11
	v_log_f32_e32 v22, v22
	v_log_f32_e32 v23, v23
	v_log_f32_e32 v24, v24
	v_log_f32_e32 v25, v25
	v_log_f32_e32 v29, v18
	v_rcp_f32_e32 v10, v10
	v_mul_f32_e32 v11, 0xbfb8aa3b, v11
	v_mul_f32_e32 v14, v14, v28
	v_mul_f32_e32 v15, v15, v28
	v_exp_f32_e32 v11, v11
	v_max_f32_e32 v14, 0xc2a00000, v14
	v_max_f32_e32 v15, 0xc2a00000, v15
	v_mul_f32_e32 v14, 0xbfb8aa3b, v14
	v_mul_f32_e32 v15, 0xbfb8aa3b, v15
	v_cvt_pk_f16_f32 v18, v22, v23
	v_cvt_pk_f16_f32 v19, v24, v25
	v_cvt_pk_f16_f32 v20, v26, v21
	v_exp_f32_e32 v14, v14
	v_exp_f32_e32 v15, v15
	v_cvt_pk_f16_f32 v21, v27, v29
	v_fma_f32 v10, v171, v10, v132
	s_waitcnt lgkmcnt(11)
	v_subrev_u32_e32 v242, s82, v242
	global_store_dwordx4 v242, v[238:241], s[82:83]
	ds_bpermute_b32 v238, v250, v18
	ds_bpermute_b32 v239, v250, v19
	ds_bpermute_b32 v240, v250, v20
	ds_bpermute_b32 v241, v250, v21
	ds_bpermute_b32 v242, v250, v30
	v_add_f32_e32 v14, 1.0, v14
	v_add_f32_e32 v15, 1.0, v15
	v_log_f32_e32 v18, v10
	v_add_f32_e32 v10, 1.0, v11
	v_mul_f32_e32 v11, v12, v28
	v_max_f32_e32 v11, 0xc2a00000, v11
	v_mul_f32_e32 v11, 0xbfb8aa3b, v11
	v_exp_f32_e32 v11, v11
	v_rcp_f32_e32 v14, v14
	v_rcp_f32_e32 v15, v15
	v_mul_f32_e32 v16, v16, v28
	v_mul_f32_e32 v17, v17, v28
	v_rcp_f32_e32 v10, v10
	v_mul_f32_e32 v12, v13, v28
	v_add_f32_e32 v11, 1.0, v11
	v_fma_f32 v14, v180, v14, v136
	v_fma_f32 v15, v179, v15, v137
	v_max_f32_e32 v16, 0xc2a00000, v16
	v_max_f32_e32 v17, 0xc2a00000, v17
	v_max_f32_e32 v12, 0xc2a00000, v12
	v_rcp_f32_e32 v11, v11
	v_log_f32_e32 v14, v14
	v_mul_f32_e32 v16, 0xbfb8aa3b, v16
	v_mul_f32_e32 v17, 0xbfb8aa3b, v17
	v_log_f32_e32 v15, v15
	v_mul_f32_e32 v12, 0xbfb8aa3b, v12
	v_exp_f32_e32 v16, v16
	v_exp_f32_e32 v17, v17
	v_exp_f32_e32 v12, v12
	v_mul_f32_e32 v6, v6, v28
	v_fma_f32 v10, v170, v10, v133
	v_max_f32_e32 v6, 0xc2a00000, v6
	v_log_f32_e32 v13, v10
	v_fma_f32 v10, v169, v11, v134
	v_mul_f32_e32 v6, 0xbfb8aa3b, v6
	v_log_f32_e32 v19, v10
	v_cvt_pk_f16_f32 v10, v14, v15
	v_exp_f32_e32 v14, v6
	v_mul_f32_e32 v6, v7, v28
	v_mul_f32_e32 v8, v8, v28
	v_mul_f32_e32 v9, v9, v28
	v_mul_f32_e32 v2, v2, v28
	v_mul_f32_e32 v3, v3, v28
	v_mul_f32_e32 v4, v4, v28
	v_mul_f32_e32 v5, v5, v28
	v_add_f32_e32 v16, 1.0, v16
	v_add_f32_e32 v17, 1.0, v17
	v_add_f32_e32 v12, 1.0, v12
	v_max_f32_e32 v6, 0xc2a00000, v6
	v_max_f32_e32 v8, 0xc2a00000, v8
	v_max_f32_e32 v9, 0xc2a00000, v9
	v_max_f32_e32 v2, 0xc2a00000, v2
	v_max_f32_e32 v3, 0xc2a00000, v3
	v_max_f32_e32 v4, 0xc2a00000, v4
	v_max_f32_e32 v5, 0xc2a00000, v5
	v_rcp_f32_e32 v16, v16
	v_rcp_f32_e32 v17, v17
	v_rcp_f32_e32 v12, v12
	v_mul_f32_e32 v6, 0xbfb8aa3b, v6
	v_mul_f32_e32 v8, 0xbfb8aa3b, v8
	v_mul_f32_e32 v9, 0xbfb8aa3b, v9
	v_mul_f32_e32 v2, 0xbfb8aa3b, v2
	v_mul_f32_e32 v3, 0xbfb8aa3b, v3
	v_mul_f32_e32 v4, 0xbfb8aa3b, v4
	v_mul_f32_e32 v5, 0xbfb8aa3b, v5
	v_exp_f32_e32 v15, v6
	v_exp_f32_e32 v8, v8
	v_exp_f32_e32 v9, v9
	v_exp_f32_e32 v2, v2
	v_exp_f32_e32 v3, v3
	v_exp_f32_e32 v4, v4
	v_exp_f32_e32 v5, v5
	v_fma_f32 v16, v178, v16, v138
	v_fmac_f32_e32 v139, v177, v17
	v_fmac_f32_e32 v135, v155, v12
	v_log_f32_e32 v16, v16
	v_log_f32_e32 v17, v139
	v_log_f32_e32 v20, v135
	v_add_f32_e32 v14, 1.0, v14
	v_add_f32_e32 v15, 1.0, v15
	v_add_f32_e32 v8, 1.0, v8
	v_add_f32_e32 v9, 1.0, v9
	v_add_f32_e32 v2, 1.0, v2
	v_add_f32_e32 v3, 1.0, v3
	v_add_f32_e32 v4, 1.0, v4
	v_add_f32_e32 v5, 1.0, v5
	s_mov_b64 s[14:15], 0xb0000
	v_rcp_f32_e32 v14, v14
	v_rcp_f32_e32 v15, v15
	v_rcp_f32_e32 v8, v8
	v_rcp_f32_e32 v9, v9
	v_rcp_f32_e32 v2, v2
	v_rcp_f32_e32 v3, v3
	v_rcp_f32_e32 v4, v4
	v_rcp_f32_e32 v5, v5
	v_lshl_add_u64 v[136:137], v[166:167], 0, s[14:15]
	s_mov_b32 s14, 0xb0000
	v_add_co_u32_e32 v6, vcc, s14, v166
	v_cvt_pk_f16_f32 v11, v16, v17
	v_cvt_pk_f16_f32 v12, v18, v13
	v_cvt_pk_f16_f32 v13, v19, v20
	v_addc_co_u32_e32 v7, vcc, 0, v167, vcc
	s_waitcnt lgkmcnt(11)
	v_subrev_u32_e32 v248, s82, v248
	global_store_dwordx4 v248, v[244:247], s[82:83] offset:64
	ds_bpermute_b32 v244, v250, v10
	ds_bpermute_b32 v245, v250, v11
	ds_bpermute_b32 v246, v250, v12
	ds_bpermute_b32 v247, v250, v13
	ds_bpermute_b32 v248, v250, v6
	v_fma_f32 v6, v153, v14, v128
	v_fma_f32 v7, v168, v15, v129
	v_fma_f32 v8, v121, v8, v130
	v_fmac_f32_e32 v131, v122, v9
	v_fma_f32 v2, v123, v2, v124
	v_fma_f32 v3, v120, v3, v125
	v_fma_f32 v4, v118, v4, v126
	v_fmac_f32_e32 v127, v119, v5
	v_log_f32_e32 v6, v6
	v_log_f32_e32 v7, v7
	v_log_f32_e32 v8, v8
	v_log_f32_e32 v9, v131
	v_log_f32_e32 v2, v2
	v_log_f32_e32 v3, v3
	v_log_f32_e32 v4, v4
	v_log_f32_e32 v5, v127
	v_cvt_pk_f16_f32 v196, v181, v182
	v_cvt_pk_f16_f32 v132, v6, v7
	v_cvt_pk_f16_f32 v133, v8, v9
	v_cvt_pk_f16_f32 v134, v2, v3
	v_cvt_pk_f16_f32 v135, v4, v5
	s_waitcnt lgkmcnt(11)
	v_subrev_u32_e32 v236, s82, v236
	global_store_dwordx4 v236, v[232:235], s[82:83]
	ds_bpermute_b32 v232, v250, v194
	ds_bpermute_b32 v233, v250, v195
	ds_bpermute_b32 v234, v250, v196
	ds_bpermute_b32 v235, v250, v197
	ds_bpermute_b32 v236, v250, v166
	s_andn2_b64 vcc, exec, s[38:39]
	s_mov_b64 s[28:29], -1
	s_waitcnt lgkmcnt(10)
	v_subrev_u32_e32 v242, s82, v242
	global_store_dwordx4 v242, v[238:241], s[82:83] offset:64
	ds_bpermute_b32 v238, v250, v132
	ds_bpermute_b32 v239, v250, v133
	ds_bpermute_b32 v240, v250, v134
	ds_bpermute_b32 v241, v250, v135
	ds_bpermute_b32 v242, v250, v136
	s_waitcnt lgkmcnt(10)
	v_subrev_u32_e32 v248, s82, v248
	global_store_dwordx4 v248, v[244:247], s[82:83]
	s_waitcnt lgkmcnt(5)
	v_subrev_u32_e32 v236, s82, v236
	global_store_dwordx4 v236, v[232:235], s[82:83] offset:64
	s_waitcnt lgkmcnt(0)
	v_subrev_u32_e32 v242, s82, v242
	global_store_dwordx4 v242, v[238:241], s[82:83] offset:64
	s_cbranch_vccnz .LBB0_495

.LBB0_1233:
	v_mbcnt_lo_u32_b32 v250, -1, 0
	v_mbcnt_hi_u32_b32 v250, -1, v250
	v_lshrrev_b32_e32 v251, 2, v250
	v_and_b32_e32 v250, 3, v250
	v_lshl_add_u32 v250, v250, 4, v251
	v_lshlrev_b32_e32 v250, 2, v250
	v_lshl_add_u32 v148, s59, 10, v146
	ds_read2_b32 v[150:151], v148 offset1:16
	s_lshl_b32 s17, s58, 2
	v_med3_f32 v124, v124, 0, v193
	v_med3_f32 v125, v125, 0, v193
	s_lshl_b32 s16, s44, 7
	s_or_b32 s17, s17, s45
	s_waitcnt lgkmcnt(0)
	v_mul_f32_e32 v150, v150, v150
	v_pk_mul_f32 v[124:125], v[124:125], v[124:125]
	s_add_i32 s16, s17, s16
	v_pk_mul_f32 v[152:153], v[124:125], v[150:151] op_sel_hi:[1,0]
	v_med3_f32 v124, v130, 0, v193
	v_med3_f32 v125, v131, 0, v193
	s_ashr_i32 s17, s16, 31
	v_med3_f32 v128, v128, 0, v193
	v_med3_f32 v129, v129, 0, v193
	v_med3_f32 v126, v126, 0, v193
	v_med3_f32 v127, v127, 0, v193
	v_pk_mul_f32 v[124:125], v[124:125], v[124:125]
	s_lshl_b64 s[16:17], s[16:17], 15
	v_pk_mul_f32 v[128:129], v[128:129], v[128:129]
	v_pk_mul_f32 v[130:131], v[124:125], v[150:151] op_sel_hi:[1,0]
	v_pk_mul_f32 v[124:125], v[126:127], v[126:127]
	v_med3_f32 v116, v116, 0, v193
	v_med3_f32 v117, v117, 0, v193
	v_lshl_add_u64 v[144:145], v[138:139], 0, s[16:17]
	v_pk_mul_f32 v[128:129], v[128:129], v[150:151] op_sel_hi:[1,0]
	v_pk_mul_f32 v[154:155], v[124:125], v[150:151] op_sel_hi:[1,0]
	v_cvt_pk_bf16_f32 v124, v128, v129
	v_cvt_pk_bf16_f32 v125, v130, v131
	v_pk_mul_f32 v[116:117], v[116:117], v[116:117]
	v_cvt_pk_bf16_f32 v126, v152, v153
	v_cvt_pk_bf16_f32 v127, v154, v155
	ds_bpermute_b32 v232, v250, v124
	ds_bpermute_b32 v233, v250, v125
	ds_bpermute_b32 v234, v250, v126
	ds_bpermute_b32 v235, v250, v127
	ds_bpermute_b32 v236, v250, v144
	v_med3_f32 v120, v120, 0, v193
	v_med3_f32 v121, v121, 0, v193
	v_pk_mul_f32 v[124:125], v[116:117], v[150:151] op_sel_hi:[1,0]
	v_med3_f32 v116, v122, 0, v193
	v_med3_f32 v117, v123, 0, v193
	v_med3_f32 v118, v118, 0, v193
	v_med3_f32 v119, v119, 0, v193
	v_pk_mul_f32 v[116:117], v[116:117], v[116:117]
	v_pk_mul_f32 v[120:121], v[120:121], v[120:121]
	v_pk_mul_f32 v[122:123], v[116:117], v[150:151] op_sel_hi:[1,0]
	v_pk_mul_f32 v[116:117], v[118:119], v[118:119]
	v_pk_mul_f32 v[120:121], v[120:121], v[150:151] op_sel_hi:[1,0]
	v_pk_mul_f32 v[126:127], v[116:117], v[150:151] op_sel_hi:[1,0]
	v_cvt_pk_bf16_f32 v116, v120, v121
	v_med3_f32 v106, v106, 0, v193
	v_med3_f32 v107, v107, 0, v193
	v_cvt_pk_bf16_f32 v117, v122, v123
	v_cvt_pk_bf16_f32 v118, v124, v125
	v_cvt_pk_bf16_f32 v119, v126, v127
	ds_bpermute_b32 v238, v250, v116
	ds_bpermute_b32 v239, v250, v117
	ds_bpermute_b32 v240, v250, v118
	ds_bpermute_b32 v241, v250, v119
	ds_bpermute_b32 v242, v250, v144
	v_pk_mul_f32 v[106:107], v[106:107], v[106:107]
	v_med3_f32 v110, v110, 0, v193
	v_mul_f32_e32 v116, v151, v151
	v_pk_mul_f32 v[118:119], v[106:107], v[116:117] op_sel_hi:[1,0]
	v_med3_f32 v106, v112, 0, v193
	v_med3_f32 v107, v113, 0, v193
	v_med3_f32 v111, v111, 0, v193
	v_med3_f32 v108, v108, 0, v193
	v_med3_f32 v109, v109, 0, v193
	v_pk_mul_f32 v[106:107], v[106:107], v[106:107]
	v_pk_mul_f32 v[110:111], v[110:111], v[110:111]
	v_pk_mul_f32 v[112:113], v[106:107], v[116:117] op_sel_hi:[1,0]
	v_pk_mul_f32 v[106:107], v[108:109], v[108:109]
	v_med3_f32 v98, v98, 0, v193
	v_med3_f32 v99, v99, 0, v193
	v_pk_mul_f32 v[110:111], v[110:111], v[116:117] op_sel_hi:[1,0]
	v_pk_mul_f32 v[120:121], v[106:107], v[116:117] op_sel_hi:[1,0]
	v_cvt_pk_bf16_f32 v106, v110, v111
	v_cvt_pk_bf16_f32 v107, v112, v113
	v_pk_mul_f32 v[98:99], v[98:99], v[98:99]
	v_cvt_pk_bf16_f32 v108, v118, v119
	v_cvt_pk_bf16_f32 v109, v120, v121
	ds_bpermute_b32 v244, v250, v106
	ds_bpermute_b32 v245, v250, v107
	ds_bpermute_b32 v246, v250, v108
	ds_bpermute_b32 v247, v250, v109
	ds_bpermute_b32 v248, v250, v144
	v_med3_f32 v102, v102, 0, v193
	v_med3_f32 v103, v103, 0, v193
	v_pk_mul_f32 v[106:107], v[98:99], v[116:117] op_sel_hi:[1,0]
	v_med3_f32 v98, v104, 0, v193
	v_med3_f32 v99, v105, 0, v193
	v_pk_mul_f32 v[102:103], v[102:103], v[102:103]
	v_med3_f32 v100, v100, 0, v193
	v_med3_f32 v101, v101, 0, v193
	v_pk_mul_f32 v[98:99], v[98:99], v[98:99]
	v_pk_mul_f32 v[102:103], v[102:103], v[116:117] op_sel_hi:[1,0]
	v_pk_mul_f32 v[104:105], v[98:99], v[116:117] op_sel_hi:[1,0]
	v_pk_mul_f32 v[98:99], v[100:101], v[100:101]
	v_med3_f32 v90, v90, 0, v193
	v_pk_mul_f32 v[108:109], v[98:99], v[116:117] op_sel_hi:[1,0]
	v_cvt_pk_bf16_f32 v98, v102, v103
	ds_read2_b32 v[102:103], v148 offset0:32 offset1:48
	v_med3_f32 v91, v91, 0, v193
	v_cvt_pk_bf16_f32 v99, v104, v105
	v_cvt_pk_bf16_f32 v100, v106, v107
	v_cvt_pk_bf16_f32 v101, v108, v109
	s_waitcnt lgkmcnt(11)
	v_subrev_u32_e32 v236, s82, v236
	global_store_dwordx4 v236, v[232:235], s[82:83]
	ds_bpermute_b32 v232, v250, v98
	ds_bpermute_b32 v233, v250, v99
	ds_bpermute_b32 v234, v250, v100
	ds_bpermute_b32 v235, v250, v101
	ds_bpermute_b32 v236, v250, v144
	v_pk_mul_f32 v[90:91], v[90:91], v[90:91]
	v_med3_f32 v94, v94, 0, v193
	s_waitcnt lgkmcnt(0)
	v_mul_f32_e32 v98, v102, v102
	v_med3_f32 v95, v95, 0, v193
	v_pk_mul_f32 v[100:101], v[90:91], v[98:99] op_sel_hi:[1,0]
	v_med3_f32 v90, v96, 0, v193
	v_med3_f32 v91, v97, 0, v193
	v_pk_mul_f32 v[94:95], v[94:95], v[94:95]
	v_med3_f32 v92, v92, 0, v193
	v_med3_f32 v93, v93, 0, v193
	v_pk_mul_f32 v[90:91], v[90:91], v[90:91]
	v_pk_mul_f32 v[94:95], v[94:95], v[98:99] op_sel_hi:[1,0]
	v_pk_mul_f32 v[96:97], v[90:91], v[98:99] op_sel_hi:[1,0]
	v_pk_mul_f32 v[90:91], v[92:93], v[92:93]
	v_med3_f32 v82, v82, 0, v193
	v_pk_mul_f32 v[104:105], v[90:91], v[98:99] op_sel_hi:[1,0]
	v_cvt_pk_bf16_f32 v90, v94, v95
	v_add_co_u32_e32 v94, vcc, s73, v144
	v_med3_f32 v83, v83, 0, v193
	v_cvt_pk_bf16_f32 v91, v96, v97
	s_nop 0
	v_addc_co_u32_e32 v95, vcc, 0, v145, vcc
	v_pk_mul_f32 v[82:83], v[82:83], v[82:83]
	v_cvt_pk_bf16_f32 v92, v100, v101
	v_cvt_pk_bf16_f32 v93, v104, v105
	s_waitcnt lgkmcnt(11)
	v_subrev_u32_e32 v242, s82, v242
	global_store_dwordx4 v242, v[238:241], s[82:83] offset:64
	ds_bpermute_b32 v238, v250, v90
	ds_bpermute_b32 v239, v250, v91
	ds_bpermute_b32 v240, v250, v92
	ds_bpermute_b32 v241, v250, v93
	ds_bpermute_b32 v242, v250, v94
	v_med3_f32 v86, v86, 0, v193
	v_med3_f32 v87, v87, 0, v193
	v_pk_mul_f32 v[90:91], v[82:83], v[98:99] op_sel_hi:[1,0]
	v_med3_f32 v82, v88, 0, v193
	v_med3_f32 v83, v89, 0, v193
	v_med3_f32 v84, v84, 0, v193
	v_med3_f32 v85, v85, 0, v193
	v_pk_mul_f32 v[82:83], v[82:83], v[82:83]
	v_pk_mul_f32 v[86:87], v[86:87], v[86:87]
	v_pk_mul_f32 v[88:89], v[82:83], v[98:99] op_sel_hi:[1,0]
	v_pk_mul_f32 v[82:83], v[84:85], v[84:85]
	v_pk_mul_f32 v[86:87], v[86:87], v[98:99] op_sel_hi:[1,0]
	v_pk_mul_f32 v[92:93], v[82:83], v[98:99] op_sel_hi:[1,0]
	v_cvt_pk_bf16_f32 v82, v86, v87
	v_med3_f32 v74, v74, 0, v193
	v_med3_f32 v75, v75, 0, v193
	v_cvt_pk_bf16_f32 v83, v88, v89
	v_cvt_pk_bf16_f32 v84, v90, v91
	v_cvt_pk_bf16_f32 v85, v92, v93
	s_waitcnt lgkmcnt(11)
	v_subrev_u32_e32 v248, s82, v248
	global_store_dwordx4 v248, v[244:247], s[82:83] offset:2048
	ds_bpermute_b32 v244, v250, v82
	ds_bpermute_b32 v245, v250, v83
	ds_bpermute_b32 v246, v250, v84
	ds_bpermute_b32 v247, v250, v85
	ds_bpermute_b32 v248, v250, v94
	v_pk_mul_f32 v[74:75], v[74:75], v[74:75]
	v_med3_f32 v78, v78, 0, v193
	v_mul_f32_e32 v82, v103, v103
	v_pk_mul_f32 v[84:85], v[74:75], v[82:83] op_sel_hi:[1,0]
	v_med3_f32 v74, v80, 0, v193
	v_med3_f32 v75, v81, 0, v193
	v_med3_f32 v79, v79, 0, v193
	v_med3_f32 v76, v76, 0, v193
	v_med3_f32 v77, v77, 0, v193
	v_pk_mul_f32 v[74:75], v[74:75], v[74:75]
	v_pk_mul_f32 v[78:79], v[78:79], v[78:79]
	v_pk_mul_f32 v[80:81], v[74:75], v[82:83] op_sel_hi:[1,0]
	v_pk_mul_f32 v[74:75], v[76:77], v[76:77]
	v_med3_f32 v66, v66, 0, v193
	v_med3_f32 v67, v67, 0, v193
	v_pk_mul_f32 v[78:79], v[78:79], v[82:83] op_sel_hi:[1,0]
	v_pk_mul_f32 v[86:87], v[74:75], v[82:83] op_sel_hi:[1,0]
	v_cvt_pk_bf16_f32 v74, v78, v79
	v_cvt_pk_bf16_f32 v75, v80, v81
	v_pk_mul_f32 v[66:67], v[66:67], v[66:67]
	v_cvt_pk_bf16_f32 v76, v84, v85
	v_cvt_pk_bf16_f32 v77, v86, v87
	s_waitcnt lgkmcnt(10)
	v_subrev_u32_e32 v236, s82, v236
	global_store_dwordx4 v236, v[232:235], s[82:83] offset:2112
	ds_bpermute_b32 v232, v250, v74
	ds_bpermute_b32 v233, v250, v75
	ds_bpermute_b32 v234, v250, v76
	ds_bpermute_b32 v235, v250, v77
	ds_bpermute_b32 v236, v250, v94
	v_med3_f32 v70, v70, 0, v193
	v_med3_f32 v71, v71, 0, v193
	v_pk_mul_f32 v[74:75], v[66:67], v[82:83] op_sel_hi:[1,0]
	v_med3_f32 v66, v72, 0, v193
	v_med3_f32 v67, v73, 0, v193
	v_pk_mul_f32 v[70:71], v[70:71], v[70:71]
	v_med3_f32 v68, v68, 0, v193
	v_med3_f32 v69, v69, 0, v193
	v_pk_mul_f32 v[66:67], v[66:67], v[66:67]
	v_pk_mul_f32 v[70:71], v[70:71], v[82:83] op_sel_hi:[1,0]
	v_pk_mul_f32 v[72:73], v[66:67], v[82:83] op_sel_hi:[1,0]
	v_pk_mul_f32 v[66:67], v[68:69], v[68:69]
	v_med3_f32 v64, v64, 0, v193
	v_pk_mul_f32 v[76:77], v[66:67], v[82:83] op_sel_hi:[1,0]
	v_cvt_pk_bf16_f32 v66, v70, v71
	ds_read2_b32 v[70:71], v148 offset0:128 offset1:144
	v_med3_f32 v65, v65, 0, v193
	v_cvt_pk_bf16_f32 v67, v72, v73
	v_cvt_pk_bf16_f32 v68, v74, v75
	v_cvt_pk_bf16_f32 v69, v76, v77
	s_waitcnt lgkmcnt(11)
	v_subrev_u32_e32 v242, s82, v242
	global_store_dwordx4 v242, v[238:241], s[82:83]
	ds_bpermute_b32 v238, v250, v66
	ds_bpermute_b32 v239, v250, v67
	ds_bpermute_b32 v240, v250, v68
	ds_bpermute_b32 v241, v250, v69
	ds_bpermute_b32 v242, v250, v94
	v_med3_f32 v60, v60, 0, v193
	v_med3_f32 v61, v61, 0, v193
	s_waitcnt lgkmcnt(0)
	v_mul_f32_e32 v66, v70, v70
	v_pk_mul_f32 v[64:65], v[64:65], v[64:65]
	v_med3_f32 v62, v62, 0, v193
	v_med3_f32 v63, v63, 0, v193
	v_med3_f32 v58, v58, 0, v193
	v_med3_f32 v59, v59, 0, v193
	v_pk_mul_f32 v[64:65], v[64:65], v[66:67] op_sel_hi:[1,0]
	v_pk_mul_f32 v[60:61], v[60:61], v[60:61]
	v_pk_mul_f32 v[62:63], v[62:63], v[62:63]
	v_pk_mul_f32 v[58:59], v[58:59], v[58:59]
	v_pk_mul_f32 v[68:69], v[60:61], v[66:67] op_sel_hi:[1,0]
	v_cvt_pk_bf16_f32 v61, v64, v65
	v_add_co_u32_e32 v64, vcc, s72, v144
	v_pk_mul_f32 v[62:63], v[62:63], v[66:67] op_sel_hi:[1,0]
	v_pk_mul_f32 v[58:59], v[58:59], v[66:67] op_sel_hi:[1,0]
	v_addc_co_u32_e32 v65, vcc, 0, v145, vcc
	v_cvt_pk_bf16_f32 v60, v62, v63
	v_cvt_pk_bf16_f32 v62, v58, v59
	v_add_co_u32_e32 v58, vcc, s31, v144
	v_med3_f32 v50, v50, 0, v193
	v_med3_f32 v51, v51, 0, v193
	v_addc_co_u32_e32 v59, vcc, 0, v145, vcc
	v_pk_mul_f32 v[50:51], v[50:51], v[50:51]
	v_cvt_pk_bf16_f32 v63, v68, v69
	s_waitcnt lgkmcnt(11)
	v_subrev_u32_e32 v248, s82, v248
	global_store_dwordx4 v248, v[244:247], s[82:83] offset:64
	ds_bpermute_b32 v244, v250, v60
	ds_bpermute_b32 v245, v250, v61
	ds_bpermute_b32 v246, v250, v62
	ds_bpermute_b32 v247, v250, v63
	ds_bpermute_b32 v248, v250, v58
	v_med3_f32 v54, v54, 0, v193
	v_med3_f32 v55, v55, 0, v193
	v_pk_mul_f32 v[60:61], v[50:51], v[66:67] op_sel_hi:[1,0]
	v_med3_f32 v50, v56, 0, v193
	v_med3_f32 v51, v57, 0, v193
	v_med3_f32 v52, v52, 0, v193
	v_med3_f32 v53, v53, 0, v193
	v_pk_mul_f32 v[50:51], v[50:51], v[50:51]
	v_pk_mul_f32 v[54:55], v[54:55], v[54:55]
	v_pk_mul_f32 v[56:57], v[50:51], v[66:67] op_sel_hi:[1,0]
	v_pk_mul_f32 v[50:51], v[52:53], v[52:53]
	v_pk_mul_f32 v[54:55], v[54:55], v[66:67] op_sel_hi:[1,0]
	v_pk_mul_f32 v[62:63], v[50:51], v[66:67] op_sel_hi:[1,0]
	v_cvt_pk_bf16_f32 v50, v54, v55
	v_med3_f32 v42, v42, 0, v193
	v_med3_f32 v43, v43, 0, v193
	v_cvt_pk_bf16_f32 v51, v56, v57
	v_cvt_pk_bf16_f32 v52, v60, v61
	v_cvt_pk_bf16_f32 v53, v62, v63
	s_waitcnt lgkmcnt(11)
	v_subrev_u32_e32 v236, s82, v236
	global_store_dwordx4 v236, v[232:235], s[82:83] offset:2048
	ds_bpermute_b32 v232, v250, v50
	ds_bpermute_b32 v233, v250, v51
	ds_bpermute_b32 v234, v250, v52
	ds_bpermute_b32 v235, v250, v53
	ds_bpermute_b32 v236, v250, v64
	v_pk_mul_f32 v[42:43], v[42:43], v[42:43]
	v_med3_f32 v46, v46, 0, v193
	v_mul_f32_e32 v50, v71, v71
	v_pk_mul_f32 v[52:53], v[42:43], v[50:51] op_sel_hi:[1,0]
	v_med3_f32 v42, v48, 0, v193
	v_med3_f32 v43, v49, 0, v193
	v_med3_f32 v47, v47, 0, v193
	v_med3_f32 v44, v44, 0, v193
	v_med3_f32 v45, v45, 0, v193
	v_pk_mul_f32 v[42:43], v[42:43], v[42:43]
	v_pk_mul_f32 v[46:47], v[46:47], v[46:47]
	v_pk_mul_f32 v[48:49], v[42:43], v[50:51] op_sel_hi:[1,0]
	v_pk_mul_f32 v[42:43], v[44:45], v[44:45]
	v_med3_f32 v34, v34, 0, v193
	v_med3_f32 v35, v35, 0, v193
	v_pk_mul_f32 v[46:47], v[46:47], v[50:51] op_sel_hi:[1,0]
	v_pk_mul_f32 v[54:55], v[42:43], v[50:51] op_sel_hi:[1,0]
	v_cvt_pk_bf16_f32 v42, v46, v47
	v_cvt_pk_bf16_f32 v43, v48, v49
	v_pk_mul_f32 v[34:35], v[34:35], v[34:35]
	v_cvt_pk_bf16_f32 v44, v52, v53
	v_cvt_pk_bf16_f32 v45, v54, v55
	s_waitcnt lgkmcnt(10)
	v_subrev_u32_e32 v242, s82, v242
	global_store_dwordx4 v242, v[238:241], s[82:83] offset:2112
	ds_bpermute_b32 v238, v250, v42
	ds_bpermute_b32 v239, v250, v43
	ds_bpermute_b32 v240, v250, v44
	ds_bpermute_b32 v241, v250, v45
	ds_bpermute_b32 v242, v250, v64
	v_med3_f32 v38, v38, 0, v193
	v_med3_f32 v39, v39, 0, v193
	v_pk_mul_f32 v[42:43], v[34:35], v[50:51] op_sel_hi:[1,0]
	v_med3_f32 v34, v40, 0, v193
	v_med3_f32 v35, v41, 0, v193
	v_pk_mul_f32 v[38:39], v[38:39], v[38:39]
	v_med3_f32 v36, v36, 0, v193
	v_med3_f32 v37, v37, 0, v193
	v_pk_mul_f32 v[34:35], v[34:35], v[34:35]
	v_pk_mul_f32 v[38:39], v[38:39], v[50:51] op_sel_hi:[1,0]
	v_pk_mul_f32 v[40:41], v[34:35], v[50:51] op_sel_hi:[1,0]
	v_pk_mul_f32 v[34:35], v[36:37], v[36:37]
	v_med3_f32 v26, v26, 0, v193
	v_pk_mul_f32 v[44:45], v[34:35], v[50:51] op_sel_hi:[1,0]
	v_cvt_pk_bf16_f32 v34, v38, v39
	ds_read2_b32 v[38:39], v148 offset0:160 offset1:176
	v_med3_f32 v27, v27, 0, v193
	v_cvt_pk_bf16_f32 v35, v40, v41
	v_cvt_pk_bf16_f32 v36, v42, v43
	v_cvt_pk_bf16_f32 v37, v44, v45
	s_waitcnt lgkmcnt(11)
	v_subrev_u32_e32 v248, s82, v248
	global_store_dwordx4 v248, v[244:247], s[82:83] offset:-4096
	ds_bpermute_b32 v244, v250, v34
	ds_bpermute_b32 v245, v250, v35
	ds_bpermute_b32 v246, v250, v36
	ds_bpermute_b32 v247, v250, v37
	ds_bpermute_b32 v248, v250, v64
	v_pk_mul_f32 v[26:27], v[26:27], v[26:27]
	v_med3_f32 v30, v30, 0, v193
	s_waitcnt lgkmcnt(0)
	v_mul_f32_e32 v34, v38, v38
	v_pk_mul_f32 v[36:37], v[26:27], v[34:35] op_sel_hi:[1,0]
	v_med3_f32 v26, v32, 0, v193
	v_med3_f32 v27, v33, 0, v193
	v_med3_f32 v31, v31, 0, v193
	v_med3_f32 v28, v28, 0, v193
	v_med3_f32 v29, v29, 0, v193
	v_pk_mul_f32 v[26:27], v[26:27], v[26:27]
	v_pk_mul_f32 v[30:31], v[30:31], v[30:31]
	v_pk_mul_f32 v[32:33], v[26:27], v[34:35] op_sel_hi:[1,0]
	v_pk_mul_f32 v[26:27], v[28:29], v[28:29]
	v_med3_f32 v18, v18, 0, v193
	v_med3_f32 v19, v19, 0, v193
	v_pk_mul_f32 v[30:31], v[30:31], v[34:35] op_sel_hi:[1,0]
	v_pk_mul_f32 v[40:41], v[26:27], v[34:35] op_sel_hi:[1,0]
	v_cvt_pk_bf16_f32 v26, v30, v31
	v_cvt_pk_bf16_f32 v27, v32, v33
	v_pk_mul_f32 v[18:19], v[18:19], v[18:19]
	v_cvt_pk_bf16_f32 v28, v36, v37
	v_cvt_pk_bf16_f32 v29, v40, v41
	s_waitcnt lgkmcnt(11)
	v_subrev_u32_e32 v236, s82, v236
	global_store_dwordx4 v236, v[232:235], s[82:83] offset:64
	ds_bpermute_b32 v232, v250, v26
	ds_bpermute_b32 v233, v250, v27
	ds_bpermute_b32 v234, v250, v28
	ds_bpermute_b32 v235, v250, v29
	ds_bpermute_b32 v236, v250, v58
	v_med3_f32 v22, v22, 0, v193
	v_med3_f32 v23, v23, 0, v193
	v_pk_mul_f32 v[26:27], v[18:19], v[34:35] op_sel_hi:[1,0]
	v_med3_f32 v18, v24, 0, v193
	v_med3_f32 v19, v25, 0, v193
	v_med3_f32 v20, v20, 0, v193
	v_med3_f32 v21, v21, 0, v193
	v_pk_mul_f32 v[18:19], v[18:19], v[18:19]
	v_pk_mul_f32 v[22:23], v[22:23], v[22:23]
	v_pk_mul_f32 v[24:25], v[18:19], v[34:35] op_sel_hi:[1,0]
	v_pk_mul_f32 v[18:19], v[20:21], v[20:21]
	v_pk_mul_f32 v[22:23], v[22:23], v[34:35] op_sel_hi:[1,0]
	v_pk_mul_f32 v[28:29], v[18:19], v[34:35] op_sel_hi:[1,0]
	v_cvt_pk_bf16_f32 v18, v22, v23
	v_med3_f32 v10, v10, 0, v193
	v_med3_f32 v11, v11, 0, v193
	v_cvt_pk_bf16_f32 v19, v24, v25
	v_cvt_pk_bf16_f32 v20, v26, v27
	v_cvt_pk_bf16_f32 v21, v28, v29
	s_waitcnt lgkmcnt(11)
	v_subrev_u32_e32 v242, s82, v242
	global_store_dwordx4 v242, v[238:241], s[82:83] offset:2048
	ds_bpermute_b32 v238, v250, v18
	ds_bpermute_b32 v239, v250, v19
	ds_bpermute_b32 v240, v250, v20
	ds_bpermute_b32 v241, v250, v21
	ds_bpermute_b32 v242, v250, v58
	v_pk_mul_f32 v[10:11], v[10:11], v[10:11]
	v_med3_f32 v14, v14, 0, v193
	v_mul_f32_e32 v18, v39, v39
	v_pk_mul_f32 v[20:21], v[10:11], v[18:19] op_sel_hi:[1,0]
	v_med3_f32 v10, v16, 0, v193
	v_med3_f32 v11, v17, 0, v193
	v_med3_f32 v15, v15, 0, v193
	v_med3_f32 v12, v12, 0, v193
	v_med3_f32 v13, v13, 0, v193
	v_pk_mul_f32 v[10:11], v[10:11], v[10:11]
	v_pk_mul_f32 v[14:15], v[14:15], v[14:15]
	v_pk_mul_f32 v[16:17], v[10:11], v[18:19] op_sel_hi:[1,0]
	v_pk_mul_f32 v[10:11], v[12:13], v[12:13]
	v_med3_f32 v2, v2, 0, v193
	v_med3_f32 v3, v3, 0, v193
	v_pk_mul_f32 v[14:15], v[14:15], v[18:19] op_sel_hi:[1,0]
	v_pk_mul_f32 v[22:23], v[10:11], v[18:19] op_sel_hi:[1,0]
	v_cvt_pk_bf16_f32 v10, v14, v15
	v_cvt_pk_bf16_f32 v11, v16, v17
	v_pk_mul_f32 v[2:3], v[2:3], v[2:3]
	v_cvt_pk_bf16_f32 v12, v20, v21
	v_cvt_pk_bf16_f32 v13, v22, v23
	s_waitcnt lgkmcnt(10)
	v_subrev_u32_e32 v248, s82, v248
	global_store_dwordx4 v248, v[244:247], s[82:83] offset:2112
	ds_bpermute_b32 v244, v250, v10
	ds_bpermute_b32 v245, v250, v11
	ds_bpermute_b32 v246, v250, v12
	ds_bpermute_b32 v247, v250, v13
	ds_bpermute_b32 v248, v250, v58
	v_med3_f32 v6, v6, 0, v193
	v_med3_f32 v7, v7, 0, v193
	v_pk_mul_f32 v[10:11], v[2:3], v[18:19] op_sel_hi:[1,0]
	v_med3_f32 v2, v8, 0, v193
	v_med3_f32 v3, v9, 0, v193
	v_med3_f32 v4, v4, 0, v193
	v_med3_f32 v5, v5, 0, v193
	v_pk_mul_f32 v[2:3], v[2:3], v[2:3]
	v_pk_mul_f32 v[6:7], v[6:7], v[6:7]
	v_pk_mul_f32 v[8:9], v[2:3], v[18:19] op_sel_hi:[1,0]
	v_pk_mul_f32 v[2:3], v[4:5], v[4:5]
	s_andn2_b64 vcc, exec, s[38:39]
	s_mov_b64 s[38:39], -1
	v_pk_mul_f32 v[6:7], v[6:7], v[18:19] op_sel_hi:[1,0]
	v_pk_mul_f32 v[12:13], v[2:3], v[18:19] op_sel_hi:[1,0]
	v_cvt_pk_bf16_f32 v2, v6, v7
	v_cvt_pk_bf16_f32 v3, v8, v9
	v_cvt_pk_bf16_f32 v4, v10, v11
	s_nop 0
	v_cvt_pk_bf16_f32 v5, v12, v13
	s_waitcnt lgkmcnt(10)
	v_subrev_u32_e32 v236, s82, v236
	global_store_dwordx4 v236, v[232:235], s[82:83]
	ds_bpermute_b32 v232, v250, v2
	ds_bpermute_b32 v233, v250, v3
	ds_bpermute_b32 v234, v250, v4
	ds_bpermute_b32 v235, v250, v5
	ds_bpermute_b32 v236, v250, v58
	s_waitcnt lgkmcnt(10)
	v_subrev_u32_e32 v242, s82, v242
	global_store_dwordx4 v242, v[238:241], s[82:83] offset:64
	s_waitcnt lgkmcnt(5)
	v_subrev_u32_e32 v248, s82, v248
	global_store_dwordx4 v248, v[244:247], s[82:83] offset:2048
	s_waitcnt lgkmcnt(0)
	v_subrev_u32_e32 v236, s82, v236
	global_store_dwordx4 v236, v[232:235], s[82:83] offset:2112
	s_cbranch_vccnz .LBB0_1222
	s_andn2_b64 vcc, exec, s[0:1]
	s_cbranch_vccnz .LBB0_1221
	s_barrier
	s_branch .LBB0_1221
